# v81 + K-loop MMA-segment slot trims (redundant lgkmcnt(0) behind the pre-MMA barrier, back-to-back setprio pairs)
# baseline (speedup 1.0000x reference)
.LBB0_98:
	s_add_u32 s54, s50, s52
	s_addc_u32 s55, s51, s53
	v_or_b32_e32 v146, 0x10000, v145
	v_add_u32_e32 v150, 0x10400, v145
	v_add_u32_e32 v154, 0x10800, v145
	v_add_u32_e32 v158, 0x10c00, v145
	v_or_b32_e32 v162, 0x14000, v145
	v_add_u32_e32 v166, 0x14400, v145
	v_add_u32_e32 v170, 0x14800, v145
	v_add_u32_e32 v174, 0x14c00, v145
	s_add_u32 s54, s54, 0x100
	ds_read_b128 v[146:149], v146
	ds_read_b128 v[150:153], v150
	ds_read_b128 v[154:157], v154
	ds_read_b128 v[158:161], v158
	ds_read_b128 v[162:165], v162
	ds_read_b128 v[166:169], v166
	ds_read_b128 v[170:173], v170
	ds_read_b128 v[174:177], v174
	s_addc_u32 s55, s55, 0
	s_add_u32 vcc_lo, s95, s52
	s_addc_u32 vcc_hi, s46, s53
	s_cmpk_eq_i32 s52, 0x1500
	s_cselect_b32 s57, s43, s55
	s_cselect_b32 s56, s42, s54
	s_cselect_b32 s55, s49, vcc_hi
	s_cselect_b32 s54, s48, vcc_lo
	s_mov_b32 m0, s89
	v_lshl_add_u64 v[194:195], v[140:141], 0, s[52:53]
	ds_read_b128 v[178:181], v144
	ds_read_b128 v[182:185], v144 offset:1024
	ds_read_b128 v[186:189], v144 offset:2048
	ds_read_b128 v[190:193], v144 offset:3072
	ds_read_b128 v[200:203], v144 offset:4096
	ds_read_b128 v[204:207], v144 offset:5120
	ds_read_b128 v[208:211], v144 offset:6144
	ds_read_b128 v[212:215], v144 offset:7168
	global_load_lds_dwordx4 v[194:195], off
	v_lshl_add_u64 v[194:195], v[142:143], 0, s[52:53]
	s_mov_b32 m0, s90
	s_nop 0
	global_load_lds_dwordx4 v[194:195], off
	s_waitcnt vmcnt(8)
	s_waitcnt lgkmcnt(0)
	s_barrier
	s_setprio 1
	v_mfma_f32_16x16x32_bf16 v[126:129], v[146:149], v[178:181], v[126:129]
	v_mfma_f32_16x16x32_bf16 v[122:125], v[154:157], v[178:181], v[122:125]
	v_mfma_f32_16x16x32_bf16 v[110:113], v[146:149], v[186:189], v[110:113]
	v_mfma_f32_16x16x32_bf16 v[106:109], v[154:157], v[186:189], v[106:109]
	v_mfma_f32_16x16x32_bf16 v[94:97], v[146:149], v[200:203], v[94:97]
	v_mfma_f32_16x16x32_bf16 v[90:93], v[154:157], v[200:203], v[90:93]
	v_mfma_f32_16x16x32_bf16 v[78:81], v[146:149], v[208:211], v[78:81]
	v_mfma_f32_16x16x32_bf16 v[74:77], v[154:157], v[208:211], v[74:77]
	v_mfma_f32_16x16x32_bf16 v[126:129], v[150:153], v[182:185], v[126:129]
	v_mfma_f32_16x16x32_bf16 v[122:125], v[158:161], v[182:185], v[122:125]
	v_mfma_f32_16x16x32_bf16 v[110:113], v[150:153], v[190:193], v[110:113]
	v_mfma_f32_16x16x32_bf16 v[106:109], v[158:161], v[190:193], v[106:109]
	v_mfma_f32_16x16x32_bf16 v[94:97], v[150:153], v[204:207], v[94:97]
	v_mfma_f32_16x16x32_bf16 v[90:93], v[158:161], v[204:207], v[90:93]
	v_mfma_f32_16x16x32_bf16 v[78:81], v[150:153], v[212:215], v[78:81]
	v_mfma_f32_16x16x32_bf16 v[74:77], v[158:161], v[212:215], v[74:77]
	v_mfma_f32_16x16x32_bf16 v[118:121], v[162:165], v[178:181], v[118:121]
	v_mfma_f32_16x16x32_bf16 v[114:117], v[170:173], v[178:181], v[114:117]
	v_mfma_f32_16x16x32_bf16 v[102:105], v[162:165], v[186:189], v[102:105]
	v_mfma_f32_16x16x32_bf16 v[98:101], v[170:173], v[186:189], v[98:101]
	v_mfma_f32_16x16x32_bf16 v[86:89], v[162:165], v[200:203], v[86:89]
	v_mfma_f32_16x16x32_bf16 v[82:85], v[170:173], v[200:203], v[82:85]
	v_mfma_f32_16x16x32_bf16 v[70:73], v[162:165], v[208:211], v[70:73]
	v_mfma_f32_16x16x32_bf16 v[66:69], v[170:173], v[208:211], v[66:69]
	v_mfma_f32_16x16x32_bf16 v[118:121], v[166:169], v[182:185], v[118:121]
	v_mfma_f32_16x16x32_bf16 v[114:117], v[174:177], v[182:185], v[114:117]
	v_mfma_f32_16x16x32_bf16 v[102:105], v[166:169], v[190:193], v[102:105]
	v_mfma_f32_16x16x32_bf16 v[98:101], v[174:177], v[190:193], v[98:101]
	v_mfma_f32_16x16x32_bf16 v[86:89], v[166:169], v[204:207], v[86:89]
	v_mfma_f32_16x16x32_bf16 v[82:85], v[174:177], v[204:207], v[82:85]
	v_mfma_f32_16x16x32_bf16 v[70:73], v[166:169], v[212:215], v[70:73]
	v_mfma_f32_16x16x32_bf16 v[66:69], v[174:177], v[212:215], v[66:69]
	s_setprio 0
	s_barrier
	s_mov_b32 m0, s58
	v_lshl_add_u64 v[194:195], s[54:55], 0, v[0:1]
	s_add_u32 vcc_lo, s54, 0xb0000
	ds_read_b128 v[178:181], v144 offset:16384
	ds_read_b128 v[182:185], v144 offset:17408
	ds_read_b128 v[186:189], v144 offset:18432
	ds_read_b128 v[190:193], v144 offset:19456
	ds_read_b128 v[200:203], v144 offset:20480
	ds_read_b128 v[204:207], v144 offset:21504
	ds_read_b128 v[208:211], v144 offset:22528
	ds_read_b128 v[212:215], v144 offset:23552
	global_load_lds_dwordx4 v0, s[54:55]
	v_lshl_add_u64 v[216:217], s[54:55], 0, v[130:131]
	s_mov_b32 m0, s59
	s_addc_u32 vcc_hi, s55, 0
	global_load_lds_dwordx4 v130, s[54:55]
	s_mov_b32 m0, s60
	v_lshl_add_u64 v[220:221], s[56:57], 0, v[132:133]
	global_load_lds_dwordx4 v0, vcc
	s_mov_b32 m0, s61
	s_nop 0
	global_load_lds_dwordx4 v130, vcc
	v_lshl_add_u64 v[218:219], s[56:57], 0, v[134:135]
	s_mov_b32 m0, s39
	s_nop 0
	global_load_lds_dwordx4 v134, s[56:57]
	s_mov_b32 m0, s64
	s_nop 0
	global_load_lds_dwordx4 v132, s[56:57]
	s_waitcnt vmcnt(8)
	s_waitcnt lgkmcnt(0)
	s_barrier
	s_setprio 1
	v_mfma_f32_16x16x32_bf16 v[62:65], v[146:149], v[178:181], v[62:65]
	v_mfma_f32_16x16x32_bf16 v[58:61], v[154:157], v[178:181], v[58:61]
	v_mfma_f32_16x16x32_bf16 v[46:49], v[146:149], v[186:189], v[46:49]
	v_mfma_f32_16x16x32_bf16 v[42:45], v[154:157], v[186:189], v[42:45]
	v_mfma_f32_16x16x32_bf16 v[30:33], v[146:149], v[200:203], v[30:33]
	v_mfma_f32_16x16x32_bf16 v[26:29], v[154:157], v[200:203], v[26:29]
	v_mfma_f32_16x16x32_bf16 v[14:17], v[146:149], v[208:211], v[14:17]
	v_mfma_f32_16x16x32_bf16 v[10:13], v[154:157], v[208:211], v[10:13]
	v_mfma_f32_16x16x32_bf16 v[62:65], v[150:153], v[182:185], v[62:65]
	v_mfma_f32_16x16x32_bf16 v[58:61], v[158:161], v[182:185], v[58:61]
	v_mfma_f32_16x16x32_bf16 v[46:49], v[150:153], v[190:193], v[46:49]
	v_mfma_f32_16x16x32_bf16 v[42:45], v[158:161], v[190:193], v[42:45]
	v_mfma_f32_16x16x32_bf16 v[30:33], v[150:153], v[204:207], v[30:33]
	v_mfma_f32_16x16x32_bf16 v[26:29], v[158:161], v[204:207], v[26:29]
	v_mfma_f32_16x16x32_bf16 v[14:17], v[150:153], v[212:215], v[14:17]
	v_mfma_f32_16x16x32_bf16 v[10:13], v[158:161], v[212:215], v[10:13]
	v_mfma_f32_16x16x32_bf16 v[54:57], v[162:165], v[178:181], v[54:57]
	v_mfma_f32_16x16x32_bf16 v[50:53], v[170:173], v[178:181], v[50:53]
	v_mfma_f32_16x16x32_bf16 v[38:41], v[162:165], v[186:189], v[38:41]
	v_mfma_f32_16x16x32_bf16 v[34:37], v[170:173], v[186:189], v[34:37]
	v_mfma_f32_16x16x32_bf16 v[22:25], v[162:165], v[200:203], v[22:25]
	v_mfma_f32_16x16x32_bf16 v[18:21], v[170:173], v[200:203], v[18:21]
	v_mfma_f32_16x16x32_bf16 v[6:9], v[162:165], v[208:211], v[6:9]
	v_mfma_f32_16x16x32_bf16 v[2:5], v[170:173], v[208:211], v[2:5]
	v_mfma_f32_16x16x32_bf16 v[54:57], v[166:169], v[182:185], v[54:57]
	v_mfma_f32_16x16x32_bf16 v[50:53], v[174:177], v[182:185], v[50:53]
	v_mfma_f32_16x16x32_bf16 v[38:41], v[166:169], v[190:193], v[38:41]
	v_mfma_f32_16x16x32_bf16 v[34:37], v[174:177], v[190:193], v[34:37]
	v_mfma_f32_16x16x32_bf16 v[22:25], v[166:169], v[204:207], v[22:25]
	v_mfma_f32_16x16x32_bf16 v[18:21], v[174:177], v[204:207], v[18:21]
	v_mfma_f32_16x16x32_bf16 v[6:9], v[166:169], v[212:215], v[6:9]
	v_mfma_f32_16x16x32_bf16 v[2:5], v[174:177], v[212:215], v[2:5]
	s_setprio 0
	s_barrier
	v_or_b32_e32 v146, 0x18000, v145
	v_add_u32_e32 v150, 0x18400, v145
	v_add_u32_e32 v154, 0x18800, v145
	v_add_u32_e32 v158, 0x18c00, v145
	v_or_b32_e32 v162, 0x1c000, v145
	v_add_u32_e32 v166, 0x1c400, v145
	v_add_u32_e32 v170, 0x1c800, v145
	v_add_u32_e32 v174, 0x1cc00, v145
	ds_read_b128 v[146:149], v146
	ds_read_b128 v[150:153], v150
	ds_read_b128 v[154:157], v154
	ds_read_b128 v[158:161], v158
	ds_read_b128 v[162:165], v162
	ds_read_b128 v[166:169], v166
	ds_read_b128 v[170:173], v170
	ds_read_b128 v[174:177], v174
	s_add_u32 s56, s56, 0xb0000
	s_addc_u32 s57, s57, 0
	s_mov_b32 m0, s65
	ds_read_b128 v[178:181], v144 offset:32768
	ds_read_b128 v[182:185], v144 offset:33792
	ds_read_b128 v[186:189], v144 offset:34816
	ds_read_b128 v[190:193], v144 offset:35840
	ds_read_b128 v[200:203], v144 offset:36864
	ds_read_b128 v[204:207], v144 offset:37888
	ds_read_b128 v[208:211], v144 offset:38912
	ds_read_b128 v[212:215], v144 offset:39936
	global_load_lds_dwordx4 v134, s[56:57]
	s_mov_b32 m0, s66
	s_nop 0
	global_load_lds_dwordx4 v132, s[56:57]
	s_waitcnt vmcnt(8)
	s_waitcnt lgkmcnt(0)
	s_barrier
	s_setprio 1
	v_mfma_f32_16x16x32_bf16 v[126:129], v[146:149], v[178:181], v[126:129]
	v_mfma_f32_16x16x32_bf16 v[122:125], v[154:157], v[178:181], v[122:125]
	v_mfma_f32_16x16x32_bf16 v[110:113], v[146:149], v[186:189], v[110:113]
	v_mfma_f32_16x16x32_bf16 v[106:109], v[154:157], v[186:189], v[106:109]
	v_mfma_f32_16x16x32_bf16 v[94:97], v[146:149], v[200:203], v[94:97]
	v_mfma_f32_16x16x32_bf16 v[90:93], v[154:157], v[200:203], v[90:93]
	v_mfma_f32_16x16x32_bf16 v[78:81], v[146:149], v[208:211], v[78:81]
	v_mfma_f32_16x16x32_bf16 v[74:77], v[154:157], v[208:211], v[74:77]
	v_mfma_f32_16x16x32_bf16 v[126:129], v[150:153], v[182:185], v[126:129]
	v_mfma_f32_16x16x32_bf16 v[122:125], v[158:161], v[182:185], v[122:125]
	v_mfma_f32_16x16x32_bf16 v[110:113], v[150:153], v[190:193], v[110:113]
	v_mfma_f32_16x16x32_bf16 v[106:109], v[158:161], v[190:193], v[106:109]
	v_mfma_f32_16x16x32_bf16 v[94:97], v[150:153], v[204:207], v[94:97]
	v_mfma_f32_16x16x32_bf16 v[90:93], v[158:161], v[204:207], v[90:93]
	v_mfma_f32_16x16x32_bf16 v[78:81], v[150:153], v[212:215], v[78:81]
	v_mfma_f32_16x16x32_bf16 v[74:77], v[158:161], v[212:215], v[74:77]
	v_mfma_f32_16x16x32_bf16 v[118:121], v[162:165], v[178:181], v[118:121]
	v_mfma_f32_16x16x32_bf16 v[114:117], v[170:173], v[178:181], v[114:117]
	v_mfma_f32_16x16x32_bf16 v[102:105], v[162:165], v[186:189], v[102:105]
	v_mfma_f32_16x16x32_bf16 v[98:101], v[170:173], v[186:189], v[98:101]
	v_mfma_f32_16x16x32_bf16 v[86:89], v[162:165], v[200:203], v[86:89]
	v_mfma_f32_16x16x32_bf16 v[82:85], v[170:173], v[200:203], v[82:85]
	v_mfma_f32_16x16x32_bf16 v[70:73], v[162:165], v[208:211], v[70:73]
	v_mfma_f32_16x16x32_bf16 v[66:69], v[170:173], v[208:211], v[66:69]
	v_mfma_f32_16x16x32_bf16 v[118:121], v[166:169], v[182:185], v[118:121]
	v_mfma_f32_16x16x32_bf16 v[114:117], v[174:177], v[182:185], v[114:117]
	v_mfma_f32_16x16x32_bf16 v[102:105], v[166:169], v[190:193], v[102:105]
	v_mfma_f32_16x16x32_bf16 v[98:101], v[174:177], v[190:193], v[98:101]
	v_mfma_f32_16x16x32_bf16 v[86:89], v[166:169], v[204:207], v[86:89]
	v_mfma_f32_16x16x32_bf16 v[82:85], v[174:177], v[204:207], v[82:85]
	v_mfma_f32_16x16x32_bf16 v[70:73], v[166:169], v[212:215], v[70:73]
	v_mfma_f32_16x16x32_bf16 v[66:69], v[174:177], v[212:215], v[66:69]
	s_setprio 0
	s_barrier
	s_mov_b32 m0, s67
	v_lshl_add_u64 v[194:195], v[194:195], 0, s[18:19]
	s_add_u32 s54, s54, 0xb0080
	ds_read_b128 v[178:181], v144 offset:49152
	ds_read_b128 v[182:185], v144 offset:50176
	ds_read_b128 v[186:189], v144 offset:51200
	ds_read_b128 v[190:193], v144 offset:52224
	ds_read_b128 v[200:203], v144 offset:53248
	ds_read_b128 v[204:207], v144 offset:54272
	ds_read_b128 v[208:211], v144 offset:55296
	ds_read_b128 v[212:215], v144 offset:56320
	global_load_lds_dwordx4 v[194:195], off
	v_lshl_add_u64 v[194:195], v[216:217], 0, s[18:19]
	s_mov_b32 m0, s80
	s_addc_u32 s55, s55, 0
	global_load_lds_dwordx4 v[194:195], off
	s_mov_b32 m0, s84
	s_nop 0
	global_load_lds_dwordx4 v0, s[54:55]
	s_mov_b32 m0, s85
	s_nop 0
	global_load_lds_dwordx4 v130, s[54:55]
	v_lshl_add_u64 v[194:195], v[218:219], 0, s[18:19]
	s_mov_b32 m0, s82
	s_nop 0
	global_load_lds_dwordx4 v[194:195], off
	v_lshl_add_u64 v[194:195], v[220:221], 0, s[18:19]
	s_mov_b32 m0, s83
	s_nop 0
	global_load_lds_dwordx4 v[194:195], off
	s_waitcnt vmcnt(8)
	s_waitcnt lgkmcnt(0)
	s_barrier
	s_setprio 1
	v_mfma_f32_16x16x32_bf16 v[62:65], v[146:149], v[178:181], v[62:65]
	v_mfma_f32_16x16x32_bf16 v[58:61], v[154:157], v[178:181], v[58:61]
	v_mfma_f32_16x16x32_bf16 v[46:49], v[146:149], v[186:189], v[46:49]
	v_mfma_f32_16x16x32_bf16 v[42:45], v[154:157], v[186:189], v[42:45]
	v_mfma_f32_16x16x32_bf16 v[30:33], v[146:149], v[200:203], v[30:33]
	v_mfma_f32_16x16x32_bf16 v[26:29], v[154:157], v[200:203], v[26:29]
	v_mfma_f32_16x16x32_bf16 v[14:17], v[146:149], v[208:211], v[14:17]
	v_mfma_f32_16x16x32_bf16 v[10:13], v[154:157], v[208:211], v[10:13]
	v_mfma_f32_16x16x32_bf16 v[62:65], v[150:153], v[182:185], v[62:65]
	v_mfma_f32_16x16x32_bf16 v[58:61], v[158:161], v[182:185], v[58:61]
	v_mfma_f32_16x16x32_bf16 v[46:49], v[150:153], v[190:193], v[46:49]
	v_mfma_f32_16x16x32_bf16 v[42:45], v[158:161], v[190:193], v[42:45]
	v_mfma_f32_16x16x32_bf16 v[30:33], v[150:153], v[204:207], v[30:33]
	v_mfma_f32_16x16x32_bf16 v[26:29], v[158:161], v[204:207], v[26:29]
	v_mfma_f32_16x16x32_bf16 v[14:17], v[150:153], v[212:215], v[14:17]
	v_mfma_f32_16x16x32_bf16 v[10:13], v[158:161], v[212:215], v[10:13]
	v_mfma_f32_16x16x32_bf16 v[54:57], v[162:165], v[178:181], v[54:57]
	v_mfma_f32_16x16x32_bf16 v[50:53], v[170:173], v[178:181], v[50:53]
	v_mfma_f32_16x16x32_bf16 v[38:41], v[162:165], v[186:189], v[38:41]
	v_mfma_f32_16x16x32_bf16 v[34:37], v[170:173], v[186:189], v[34:37]
	v_mfma_f32_16x16x32_bf16 v[22:25], v[162:165], v[200:203], v[22:25]
	v_mfma_f32_16x16x32_bf16 v[18:21], v[170:173], v[200:203], v[18:21]
	v_mfma_f32_16x16x32_bf16 v[6:9], v[162:165], v[208:211], v[6:9]
	v_mfma_f32_16x16x32_bf16 v[2:5], v[170:173], v[208:211], v[2:5]
	v_mfma_f32_16x16x32_bf16 v[54:57], v[166:169], v[182:185], v[54:57]
	v_mfma_f32_16x16x32_bf16 v[50:53], v[174:177], v[182:185], v[50:53]
	v_mfma_f32_16x16x32_bf16 v[38:41], v[166:169], v[190:193], v[38:41]
	v_mfma_f32_16x16x32_bf16 v[34:37], v[174:177], v[190:193], v[34:37]
	v_mfma_f32_16x16x32_bf16 v[22:25], v[166:169], v[204:207], v[22:25]
	v_mfma_f32_16x16x32_bf16 v[18:21], v[174:177], v[204:207], v[18:21]
	v_mfma_f32_16x16x32_bf16 v[6:9], v[166:169], v[212:215], v[6:9]
	v_mfma_f32_16x16x32_bf16 v[2:5], v[174:177], v[212:215], v[2:5]
	s_setprio 0
	s_barrier
	s_add_i32 s47, s47, 2
	s_add_u32 s52, s52, 0x100
	s_addc_u32 s53, s53, 0
	s_cmp_gt_u32 s47, 41
	s_cbranch_scc0 .LBB0_98
	s_and_b64 vcc, exec, s[16:17]
	s_cbranch_vccz .LBB0_101
	s_barrier

.LBB0_357:
	v_or_b32_e32 v0, 0x10000, v220
	v_add_u32_e32 v50, 0x10400, v220
	ds_read_b128 v[46:49], v0
	ds_read_b128 v[50:53], v50
	v_add_u32_e32 v0, 0x10800, v220
	v_add_u32_e32 v62, 0x10c00, v220
	ds_read_b128 v[58:61], v0
	ds_read_b128 v[62:65], v62
	v_or_b32_e32 v0, 0x14000, v220
	v_add_u32_e32 v78, 0x14400, v220
	ds_read_b128 v[74:77], v0
	ds_read_b128 v[78:81], v78
	v_add_u32_e32 v0, 0x14800, v220
	v_add_u32_e32 v86, 0x14c00, v220
	ds_read_b128 v[82:85], v0
	ds_read_b128 v[86:89], v86
	s_add_u32 s50, s40, 0xfffc0080
	s_addc_u32 s51, s41, -1
	s_cmp_eq_u32 vcc_hi, 12
	s_cselect_b32 s83, s29, s51
	s_cselect_b32 s82, s37, s50
	s_cselect_b32 s67, s39, vcc_lo
	s_cselect_b32 s66, s57, s59
	s_add_i32 m0, s88, 0xc000
	ds_read_b128 v[192:195], v219
	ds_read_b128 v[200:203], v219 offset:1024
	ds_read_b128 v[204:207], v219 offset:2048
	ds_read_b128 v[208:211], v219 offset:3072
	ds_read_b128 v[212:215], v219 offset:4096
	ds_read_b128 v[236:239], v219 offset:5120
	ds_read_b128 v[240:243], v219 offset:6144
	ds_read_b128 v[244:247], v219 offset:7168
	global_load_lds_dwordx4 v170, s[40:41]
	s_add_i32 m0, s88, 0xe000
	s_nop 0
	global_load_lds_dwordx4 v172, s[40:41]
	s_waitcnt vmcnt(8)
	s_waitcnt lgkmcnt(0)
	s_barrier
	s_setprio 1
	v_mfma_f32_16x16x32_bf16 v[158:161], v[46:49], v[192:195], v[158:161]
	v_mfma_f32_16x16x32_bf16 v[154:157], v[58:61], v[192:195], v[154:157]
	v_mfma_f32_16x16x32_bf16 v[142:145], v[46:49], v[204:207], v[142:145]
	v_mfma_f32_16x16x32_bf16 v[138:141], v[58:61], v[204:207], v[138:141]
	v_mfma_f32_16x16x32_bf16 v[126:129], v[46:49], v[212:215], v[126:129]
	v_mfma_f32_16x16x32_bf16 v[122:125], v[58:61], v[212:215], v[122:125]
	v_mfma_f32_16x16x32_bf16 v[110:113], v[46:49], v[240:243], v[110:113]
	v_mfma_f32_16x16x32_bf16 v[106:109], v[58:61], v[240:243], v[106:109]
	v_mfma_f32_16x16x32_bf16 v[158:161], v[50:53], v[200:203], v[158:161]
	v_mfma_f32_16x16x32_bf16 v[154:157], v[62:65], v[200:203], v[154:157]
	v_mfma_f32_16x16x32_bf16 v[142:145], v[50:53], v[208:211], v[142:145]
	v_mfma_f32_16x16x32_bf16 v[138:141], v[62:65], v[208:211], v[138:141]
	v_mfma_f32_16x16x32_bf16 v[126:129], v[50:53], v[236:239], v[126:129]
	v_mfma_f32_16x16x32_bf16 v[122:125], v[62:65], v[236:239], v[122:125]
	v_mfma_f32_16x16x32_bf16 v[110:113], v[50:53], v[244:247], v[110:113]
	v_mfma_f32_16x16x32_bf16 v[106:109], v[62:65], v[244:247], v[106:109]
	v_mfma_f32_16x16x32_bf16 v[150:153], v[74:77], v[192:195], v[150:153]
	v_mfma_f32_16x16x32_bf16 v[146:149], v[82:85], v[192:195], v[146:149]
	v_mfma_f32_16x16x32_bf16 v[134:137], v[74:77], v[204:207], v[134:137]
	v_mfma_f32_16x16x32_bf16 v[130:133], v[82:85], v[204:207], v[130:133]
	v_mfma_f32_16x16x32_bf16 v[118:121], v[74:77], v[212:215], v[118:121]
	v_mfma_f32_16x16x32_bf16 v[114:117], v[82:85], v[212:215], v[114:117]
	v_mfma_f32_16x16x32_bf16 v[102:105], v[74:77], v[240:243], v[102:105]
	v_mfma_f32_16x16x32_bf16 v[98:101], v[82:85], v[240:243], v[98:101]
	v_mfma_f32_16x16x32_bf16 v[150:153], v[78:81], v[200:203], v[150:153]
	v_mfma_f32_16x16x32_bf16 v[146:149], v[86:89], v[200:203], v[146:149]
	v_mfma_f32_16x16x32_bf16 v[134:137], v[78:81], v[208:211], v[134:137]
	v_mfma_f32_16x16x32_bf16 v[130:133], v[86:89], v[208:211], v[130:133]
	v_mfma_f32_16x16x32_bf16 v[118:121], v[78:81], v[236:239], v[118:121]
	v_mfma_f32_16x16x32_bf16 v[114:117], v[86:89], v[236:239], v[114:117]
	v_mfma_f32_16x16x32_bf16 v[102:105], v[78:81], v[244:247], v[102:105]
	v_mfma_f32_16x16x32_bf16 v[98:101], v[86:89], v[244:247], v[98:101]
	s_setprio 0
	s_barrier
	s_mov_b32 m0, s90
	s_add_u32 s50, s66, 0x40000
	ds_read_b128 v[192:195], v219 offset:16384
	ds_read_b128 v[200:203], v219 offset:17408
	ds_read_b128 v[204:207], v219 offset:18432
	ds_read_b128 v[208:211], v219 offset:19456
	ds_read_b128 v[212:215], v219 offset:20480
	ds_read_b128 v[236:239], v219 offset:21504
	ds_read_b128 v[240:243], v219 offset:22528
	ds_read_b128 v[244:247], v219 offset:23552
	global_load_lds_dwordx4 v166, s[66:67]
	v_lshl_add_u64 v[216:217], s[66:67], 0, v[162:163]
	s_mov_b32 m0, s91
	s_addc_u32 s51, s67, 0
	global_load_lds_dwordx4 v162, s[66:67]
	s_mov_b32 m0, s92
	s_nop 0
	global_load_lds_dwordx4 v166, s[50:51]
	s_mov_b32 m0, s93
	s_nop 0
	global_load_lds_dwordx4 v162, s[50:51]
	s_mov_b32 m0, s88
	s_nop 0
	global_load_lds_dwordx4 v168, s[82:83]
	s_mov_b32 m0, s94
	s_nop 0
	global_load_lds_dwordx4 v164, s[82:83]
	s_waitcnt vmcnt(8)
	s_waitcnt lgkmcnt(0)
	s_barrier
	s_setprio 1
	v_mfma_f32_16x16x32_bf16 v[94:97], v[46:49], v[192:195], v[94:97]
	v_mfma_f32_16x16x32_bf16 v[90:93], v[58:61], v[192:195], v[90:93]
	v_mfma_f32_16x16x32_bf16 v[54:57], v[46:49], v[204:207], v[54:57]
	v_mfma_f32_16x16x32_bf16 v[42:45], v[58:61], v[204:207], v[42:45]
	v_mfma_f32_16x16x32_bf16 v[30:33], v[46:49], v[212:215], v[30:33]
	v_mfma_f32_16x16x32_bf16 v[26:29], v[58:61], v[212:215], v[26:29]
	v_mfma_f32_16x16x32_bf16 v[14:17], v[46:49], v[240:243], v[14:17]
	v_mfma_f32_16x16x32_bf16 v[10:13], v[58:61], v[240:243], v[10:13]
	v_mfma_f32_16x16x32_bf16 v[94:97], v[50:53], v[200:203], v[94:97]
	v_mfma_f32_16x16x32_bf16 v[90:93], v[62:65], v[200:203], v[90:93]
	v_mfma_f32_16x16x32_bf16 v[54:57], v[50:53], v[208:211], v[54:57]
	v_mfma_f32_16x16x32_bf16 v[42:45], v[62:65], v[208:211], v[42:45]
	v_mfma_f32_16x16x32_bf16 v[30:33], v[50:53], v[236:239], v[30:33]
	v_mfma_f32_16x16x32_bf16 v[26:29], v[62:65], v[236:239], v[26:29]
	v_mfma_f32_16x16x32_bf16 v[14:17], v[50:53], v[244:247], v[14:17]
	v_mfma_f32_16x16x32_bf16 v[10:13], v[62:65], v[244:247], v[10:13]
	v_mfma_f32_16x16x32_bf16 v[38:41], v[74:77], v[204:207], v[38:41]
	v_mfma_f32_16x16x32_bf16 v[34:37], v[82:85], v[204:207], v[34:37]
	v_mfma_f32_16x16x32_bf16 v[22:25], v[74:77], v[212:215], v[22:25]
	v_mfma_f32_16x16x32_bf16 v[18:21], v[82:85], v[212:215], v[18:21]
	v_mfma_f32_16x16x32_bf16 v[6:9], v[74:77], v[240:243], v[6:9]
	v_mfma_f32_16x16x32_bf16 v[2:5], v[82:85], v[240:243], v[2:5]
	v_mfma_f32_16x16x32_bf16 v[46:49], v[74:77], v[192:195], v[70:73]
	v_mfma_f32_16x16x32_bf16 v[50:53], v[82:85], v[192:195], v[66:69]
	v_mfma_f32_16x16x32_bf16 v[38:41], v[78:81], v[208:211], v[38:41]
	v_mfma_f32_16x16x32_bf16 v[34:37], v[86:89], v[208:211], v[34:37]
	v_mfma_f32_16x16x32_bf16 v[22:25], v[78:81], v[236:239], v[22:25]
	v_mfma_f32_16x16x32_bf16 v[18:21], v[86:89], v[236:239], v[18:21]
	v_mfma_f32_16x16x32_bf16 v[6:9], v[78:81], v[244:247], v[6:9]
	v_mfma_f32_16x16x32_bf16 v[2:5], v[86:89], v[244:247], v[2:5]
	v_mfma_f32_16x16x32_bf16 v[46:49], v[78:81], v[200:203], v[46:49]
	v_mfma_f32_16x16x32_bf16 v[50:53], v[86:89], v[200:203], v[50:53]
	s_setprio 0
	s_barrier
	v_or_b32_e32 v0, 0x18000, v220
	v_add_u32_e32 v62, 0x18400, v220
	ds_read_b128 v[58:61], v0
	ds_read_b128 v[62:65], v62
	v_add_u32_e32 v0, 0x18800, v220
	v_add_u32_e32 v70, 0x18c00, v220
	ds_read_b128 v[66:69], v0
	ds_read_b128 v[70:73], v70
	v_or_b32_e32 v0, 0x1c000, v220
	v_add_u32_e32 v78, 0x1c400, v220
	ds_read_b128 v[74:77], v0
	ds_read_b128 v[78:81], v78
	v_add_u32_e32 v0, 0x1c800, v220
	v_add_u32_e32 v86, 0x1cc00, v220
	ds_read_b128 v[82:85], v0
	ds_read_b128 v[86:89], v86
	s_add_u32 s50, s82, 0x40000
	s_addc_u32 s51, s83, 0
	s_mov_b32 m0, s95
	ds_read_b128 v[192:195], v219 offset:32768
	ds_read_b128 v[200:203], v219 offset:33792
	ds_read_b128 v[204:207], v219 offset:34816
	ds_read_b128 v[208:211], v219 offset:35840
	ds_read_b128 v[212:215], v219 offset:36864
	ds_read_b128 v[236:239], v219 offset:37888
	ds_read_b128 v[240:243], v219 offset:38912
	ds_read_b128 v[244:247], v219 offset:39936
	global_load_lds_dwordx4 v168, s[50:51]
	s_mov_b32 m0, s0
	s_nop 0
	global_load_lds_dwordx4 v164, s[50:51]
	s_waitcnt vmcnt(8)
	s_waitcnt lgkmcnt(0)
	s_barrier
	s_setprio 1
	v_mfma_f32_16x16x32_bf16 v[158:161], v[58:61], v[192:195], v[158:161]
	v_mfma_f32_16x16x32_bf16 v[154:157], v[66:69], v[192:195], v[154:157]
	v_mfma_f32_16x16x32_bf16 v[142:145], v[58:61], v[204:207], v[142:145]
	v_mfma_f32_16x16x32_bf16 v[138:141], v[66:69], v[204:207], v[138:141]
	v_mfma_f32_16x16x32_bf16 v[126:129], v[58:61], v[212:215], v[126:129]
	v_mfma_f32_16x16x32_bf16 v[122:125], v[66:69], v[212:215], v[122:125]
	v_mfma_f32_16x16x32_bf16 v[110:113], v[58:61], v[240:243], v[110:113]
	v_mfma_f32_16x16x32_bf16 v[106:109], v[66:69], v[240:243], v[106:109]
	v_mfma_f32_16x16x32_bf16 v[158:161], v[62:65], v[200:203], v[158:161]
	v_mfma_f32_16x16x32_bf16 v[154:157], v[70:73], v[200:203], v[154:157]
	v_mfma_f32_16x16x32_bf16 v[142:145], v[62:65], v[208:211], v[142:145]
	v_mfma_f32_16x16x32_bf16 v[138:141], v[70:73], v[208:211], v[138:141]
	v_mfma_f32_16x16x32_bf16 v[126:129], v[62:65], v[236:239], v[126:129]
	v_mfma_f32_16x16x32_bf16 v[122:125], v[70:73], v[236:239], v[122:125]
	v_mfma_f32_16x16x32_bf16 v[110:113], v[62:65], v[244:247], v[110:113]
	v_mfma_f32_16x16x32_bf16 v[106:109], v[70:73], v[244:247], v[106:109]
	v_mfma_f32_16x16x32_bf16 v[150:153], v[74:77], v[192:195], v[150:153]
	v_mfma_f32_16x16x32_bf16 v[146:149], v[82:85], v[192:195], v[146:149]
	v_mfma_f32_16x16x32_bf16 v[134:137], v[74:77], v[204:207], v[134:137]
	v_mfma_f32_16x16x32_bf16 v[130:133], v[82:85], v[204:207], v[130:133]
	v_mfma_f32_16x16x32_bf16 v[118:121], v[74:77], v[212:215], v[118:121]
	v_mfma_f32_16x16x32_bf16 v[114:117], v[82:85], v[212:215], v[114:117]
	v_mfma_f32_16x16x32_bf16 v[102:105], v[74:77], v[240:243], v[102:105]
	v_mfma_f32_16x16x32_bf16 v[98:101], v[82:85], v[240:243], v[98:101]
	v_mfma_f32_16x16x32_bf16 v[150:153], v[78:81], v[200:203], v[150:153]
	v_mfma_f32_16x16x32_bf16 v[146:149], v[86:89], v[200:203], v[146:149]
	v_mfma_f32_16x16x32_bf16 v[134:137], v[78:81], v[208:211], v[134:137]
	v_mfma_f32_16x16x32_bf16 v[130:133], v[86:89], v[208:211], v[130:133]
	v_mfma_f32_16x16x32_bf16 v[118:121], v[78:81], v[236:239], v[118:121]
	v_mfma_f32_16x16x32_bf16 v[114:117], v[86:89], v[236:239], v[114:117]
	v_mfma_f32_16x16x32_bf16 v[102:105], v[78:81], v[244:247], v[102:105]
	v_mfma_f32_16x16x32_bf16 v[98:101], v[86:89], v[244:247], v[98:101]
	s_setprio 0
	s_barrier
	s_add_i32 m0, s1, 0xffffff80
	s_add_u32 s50, s66, 0x40080
	ds_read_b128 v[192:195], v219 offset:49152
	ds_read_b128 v[200:203], v219 offset:50176
	ds_read_b128 v[204:207], v219 offset:51200
	ds_read_b128 v[208:211], v219 offset:52224
	ds_read_b128 v[212:215], v219 offset:53248
	ds_read_b128 v[236:239], v219 offset:54272
	ds_read_b128 v[240:243], v219 offset:55296
	ds_read_b128 v[244:247], v219 offset:56320
	global_load_lds_dwordx4 v166, s[66:67] offset:128
	v_lshl_add_u64 v[182:183], v[216:217], 0, s[18:19]
	s_mov_b32 m0, s14
	s_addc_u32 s51, s67, 0
	global_load_lds_dwordx4 v[182:183], off
	s_mov_b32 m0, s34
	s_nop 0
	global_load_lds_dwordx4 v166, s[50:51]
	s_mov_b32 m0, s35
	s_nop 0
	global_load_lds_dwordx4 v162, s[50:51]
	s_add_i32 m0, s15, 0xffffff80
	s_nop 0
	global_load_lds_dwordx4 v168, s[82:83] offset:128
	s_add_i32 m0, s31, 0xffffff80
	s_nop 0
	global_load_lds_dwordx4 v164, s[82:83] offset:128
	s_waitcnt vmcnt(8)
	s_waitcnt lgkmcnt(0)
	s_barrier
	s_setprio 1
	v_mfma_f32_16x16x32_bf16 v[94:97], v[58:61], v[192:195], v[94:97]
	v_mfma_f32_16x16x32_bf16 v[90:93], v[66:69], v[192:195], v[90:93]
	v_mfma_f32_16x16x32_bf16 v[54:57], v[58:61], v[204:207], v[54:57]
	v_mfma_f32_16x16x32_bf16 v[42:45], v[66:69], v[204:207], v[42:45]
	v_mfma_f32_16x16x32_bf16 v[30:33], v[58:61], v[212:215], v[30:33]
	v_mfma_f32_16x16x32_bf16 v[26:29], v[66:69], v[212:215], v[26:29]
	v_mfma_f32_16x16x32_bf16 v[14:17], v[58:61], v[240:243], v[14:17]
	v_mfma_f32_16x16x32_bf16 v[10:13], v[66:69], v[240:243], v[10:13]
	v_mfma_f32_16x16x32_bf16 v[94:97], v[62:65], v[200:203], v[94:97]
	v_mfma_f32_16x16x32_bf16 v[90:93], v[70:73], v[200:203], v[90:93]
	v_mfma_f32_16x16x32_bf16 v[54:57], v[62:65], v[208:211], v[54:57]
	v_mfma_f32_16x16x32_bf16 v[42:45], v[70:73], v[208:211], v[42:45]
	v_mfma_f32_16x16x32_bf16 v[30:33], v[62:65], v[236:239], v[30:33]
	v_mfma_f32_16x16x32_bf16 v[26:29], v[70:73], v[236:239], v[26:29]
	v_mfma_f32_16x16x32_bf16 v[14:17], v[62:65], v[244:247], v[14:17]
	v_mfma_f32_16x16x32_bf16 v[10:13], v[70:73], v[244:247], v[10:13]
	v_mfma_f32_16x16x32_bf16 v[46:49], v[74:77], v[192:195], v[46:49]
	v_mfma_f32_16x16x32_bf16 v[70:73], v[78:81], v[200:203], v[46:49]
	v_mfma_f32_16x16x32_bf16 v[46:49], v[82:85], v[192:195], v[50:53]
	v_mfma_f32_16x16x32_bf16 v[38:41], v[74:77], v[204:207], v[38:41]
	v_mfma_f32_16x16x32_bf16 v[34:37], v[82:85], v[204:207], v[34:37]
	v_mfma_f32_16x16x32_bf16 v[22:25], v[74:77], v[212:215], v[22:25]
	v_mfma_f32_16x16x32_bf16 v[18:21], v[82:85], v[212:215], v[18:21]
	v_mfma_f32_16x16x32_bf16 v[6:9], v[74:77], v[240:243], v[6:9]
	v_mfma_f32_16x16x32_bf16 v[2:5], v[82:85], v[240:243], v[2:5]
	v_mfma_f32_16x16x32_bf16 v[66:69], v[86:89], v[200:203], v[46:49]
	v_mfma_f32_16x16x32_bf16 v[38:41], v[78:81], v[208:211], v[38:41]
	v_mfma_f32_16x16x32_bf16 v[34:37], v[86:89], v[208:211], v[34:37]
	v_mfma_f32_16x16x32_bf16 v[22:25], v[78:81], v[236:239], v[22:25]
	v_mfma_f32_16x16x32_bf16 v[18:21], v[86:89], v[236:239], v[18:21]
	v_mfma_f32_16x16x32_bf16 v[6:9], v[78:81], v[244:247], v[6:9]
	v_mfma_f32_16x16x32_bf16 v[2:5], v[86:89], v[244:247], v[2:5]
	s_setprio 0
	s_barrier
	s_add_i32 vcc_hi, vcc_hi, 2
	s_add_u32 s40, s40, 0x100
	s_addc_u32 s41, s41, 0
	s_add_u32 s59, s59, 0x100
	s_addc_u32 vcc_lo, vcc_lo, 0
	s_cmp_gt_u32 vcc_hi, 13
	s_cbranch_scc0 .LBB0_357
	v_readlane_b32 s40, v253, 55
	v_readlane_b32 s41, v253, 56
	s_and_b64 vcc, exec, s[40:41]
	s_cbranch_vccz .LBB0_360
	s_barrier

.LBB0_397:
	s_add_u32 s52, s48, s50
	s_addc_u32 s53, s49, s51
	v_or_b32_e32 v146, 0x10000, v145
	v_add_u32_e32 v150, 0x10400, v145
	v_add_u32_e32 v154, 0x10800, v145
	v_add_u32_e32 v158, 0x10c00, v145
	v_or_b32_e32 v162, 0x14000, v145
	v_add_u32_e32 v166, 0x14400, v145
	v_add_u32_e32 v170, 0x14800, v145
	v_add_u32_e32 v174, 0x14c00, v145
	s_add_u32 s52, s52, 0x100
	ds_read_b128 v[146:149], v146
	ds_read_b128 v[150:153], v150
	ds_read_b128 v[154:157], v154
	ds_read_b128 v[158:161], v158
	ds_read_b128 v[162:165], v162
	ds_read_b128 v[166:169], v166
	ds_read_b128 v[170:173], v170
	ds_read_b128 v[174:177], v174
	s_addc_u32 s53, s53, 0
	s_add_u32 s93, s39, s50
	s_addc_u32 s94, s41, s51
	s_cmpk_eq_i32 s50, 0x700
	s_cselect_b32 s55, s90, s53
	s_cselect_b32 s54, s91, s52
	s_cselect_b32 s53, s45, s94
	s_cselect_b32 s52, s44, s93
	v_lshl_add_u64 v[194:195], v[140:141], 0, s[50:51]
	s_add_i32 m0, s57, 0xc000
	ds_read_b128 v[178:181], v144
	ds_read_b128 v[182:185], v144 offset:1024
	ds_read_b128 v[186:189], v144 offset:2048
	ds_read_b128 v[190:193], v144 offset:3072
	ds_read_b128 v[200:203], v144 offset:4096
	ds_read_b128 v[204:207], v144 offset:5120
	ds_read_b128 v[208:211], v144 offset:6144
	ds_read_b128 v[212:215], v144 offset:7168
	global_load_lds_dwordx4 v[194:195], off
	v_lshl_add_u64 v[194:195], v[142:143], 0, s[50:51]
	s_add_i32 m0, s57, 0xe000
	s_nop 0
	global_load_lds_dwordx4 v[194:195], off
	s_waitcnt vmcnt(8)
	s_waitcnt lgkmcnt(0)
	s_barrier
	s_setprio 1
	v_mfma_f32_16x16x32_bf16 v[126:129], v[146:149], v[178:181], v[126:129]
	v_mfma_f32_16x16x32_bf16 v[122:125], v[154:157], v[178:181], v[122:125]
	v_mfma_f32_16x16x32_bf16 v[110:113], v[146:149], v[186:189], v[110:113]
	v_mfma_f32_16x16x32_bf16 v[106:109], v[154:157], v[186:189], v[106:109]
	v_mfma_f32_16x16x32_bf16 v[94:97], v[146:149], v[200:203], v[94:97]
	v_mfma_f32_16x16x32_bf16 v[90:93], v[154:157], v[200:203], v[90:93]
	v_mfma_f32_16x16x32_bf16 v[78:81], v[146:149], v[208:211], v[78:81]
	v_mfma_f32_16x16x32_bf16 v[74:77], v[154:157], v[208:211], v[74:77]
	v_mfma_f32_16x16x32_bf16 v[126:129], v[150:153], v[182:185], v[126:129]
	v_mfma_f32_16x16x32_bf16 v[122:125], v[158:161], v[182:185], v[122:125]
	v_mfma_f32_16x16x32_bf16 v[110:113], v[150:153], v[190:193], v[110:113]
	v_mfma_f32_16x16x32_bf16 v[106:109], v[158:161], v[190:193], v[106:109]
	v_mfma_f32_16x16x32_bf16 v[94:97], v[150:153], v[204:207], v[94:97]
	v_mfma_f32_16x16x32_bf16 v[90:93], v[158:161], v[204:207], v[90:93]
	v_mfma_f32_16x16x32_bf16 v[78:81], v[150:153], v[212:215], v[78:81]
	v_mfma_f32_16x16x32_bf16 v[74:77], v[158:161], v[212:215], v[74:77]
	v_mfma_f32_16x16x32_bf16 v[118:121], v[162:165], v[178:181], v[118:121]
	v_mfma_f32_16x16x32_bf16 v[114:117], v[170:173], v[178:181], v[114:117]
	v_mfma_f32_16x16x32_bf16 v[102:105], v[162:165], v[186:189], v[102:105]
	v_mfma_f32_16x16x32_bf16 v[98:101], v[170:173], v[186:189], v[98:101]
	v_mfma_f32_16x16x32_bf16 v[86:89], v[162:165], v[200:203], v[86:89]
	v_mfma_f32_16x16x32_bf16 v[82:85], v[170:173], v[200:203], v[82:85]
	v_mfma_f32_16x16x32_bf16 v[70:73], v[162:165], v[208:211], v[70:73]
	v_mfma_f32_16x16x32_bf16 v[66:69], v[170:173], v[208:211], v[66:69]
	v_mfma_f32_16x16x32_bf16 v[118:121], v[166:169], v[182:185], v[118:121]
	v_mfma_f32_16x16x32_bf16 v[114:117], v[174:177], v[182:185], v[114:117]
	v_mfma_f32_16x16x32_bf16 v[102:105], v[166:169], v[190:193], v[102:105]
	v_mfma_f32_16x16x32_bf16 v[98:101], v[174:177], v[190:193], v[98:101]
	v_mfma_f32_16x16x32_bf16 v[86:89], v[166:169], v[204:207], v[86:89]
	v_mfma_f32_16x16x32_bf16 v[82:85], v[174:177], v[204:207], v[82:85]
	v_mfma_f32_16x16x32_bf16 v[70:73], v[166:169], v[212:215], v[70:73]
	v_mfma_f32_16x16x32_bf16 v[66:69], v[174:177], v[212:215], v[66:69]
	s_setprio 0
	s_barrier
	s_mov_b32 m0, s58
	v_lshl_add_u64 v[194:195], s[52:53], 0, v[0:1]
	s_add_u32 s94, s52, 0x40000
	ds_read_b128 v[178:181], v144 offset:16384
	ds_read_b128 v[182:185], v144 offset:17408
	ds_read_b128 v[186:189], v144 offset:18432
	ds_read_b128 v[190:193], v144 offset:19456
	ds_read_b128 v[200:203], v144 offset:20480
	ds_read_b128 v[204:207], v144 offset:21504
	ds_read_b128 v[208:211], v144 offset:22528
	ds_read_b128 v[212:215], v144 offset:23552
	global_load_lds_dwordx4 v0, s[52:53]
	v_lshl_add_u64 v[216:217], s[52:53], 0, v[130:131]
	s_mov_b32 m0, s59
	s_addc_u32 s95, s53, 0
	global_load_lds_dwordx4 v130, s[52:53]
	s_mov_b32 m0, s60
	v_lshl_add_u64 v[220:221], s[54:55], 0, v[132:133]
	global_load_lds_dwordx4 v0, s[94:95]
	s_mov_b32 m0, s61
	s_nop 0
	global_load_lds_dwordx4 v130, s[94:95]
	v_lshl_add_u64 v[218:219], s[54:55], 0, v[134:135]
	s_mov_b32 m0, s57
	s_nop 0
	global_load_lds_dwordx4 v134, s[54:55]
	s_mov_b32 m0, s64
	s_nop 0
	global_load_lds_dwordx4 v132, s[54:55]
	s_waitcnt vmcnt(8)
	s_waitcnt lgkmcnt(0)
	s_barrier
	s_setprio 1
	v_mfma_f32_16x16x32_bf16 v[62:65], v[146:149], v[178:181], v[62:65]
	v_mfma_f32_16x16x32_bf16 v[58:61], v[154:157], v[178:181], v[58:61]
	v_mfma_f32_16x16x32_bf16 v[46:49], v[146:149], v[186:189], v[46:49]
	v_mfma_f32_16x16x32_bf16 v[42:45], v[154:157], v[186:189], v[42:45]
	v_mfma_f32_16x16x32_bf16 v[30:33], v[146:149], v[200:203], v[30:33]
	v_mfma_f32_16x16x32_bf16 v[26:29], v[154:157], v[200:203], v[26:29]
	v_mfma_f32_16x16x32_bf16 v[14:17], v[146:149], v[208:211], v[14:17]
	v_mfma_f32_16x16x32_bf16 v[10:13], v[154:157], v[208:211], v[10:13]
	v_mfma_f32_16x16x32_bf16 v[62:65], v[150:153], v[182:185], v[62:65]
	v_mfma_f32_16x16x32_bf16 v[58:61], v[158:161], v[182:185], v[58:61]
	v_mfma_f32_16x16x32_bf16 v[46:49], v[150:153], v[190:193], v[46:49]
	v_mfma_f32_16x16x32_bf16 v[42:45], v[158:161], v[190:193], v[42:45]
	v_mfma_f32_16x16x32_bf16 v[30:33], v[150:153], v[204:207], v[30:33]
	v_mfma_f32_16x16x32_bf16 v[26:29], v[158:161], v[204:207], v[26:29]
	v_mfma_f32_16x16x32_bf16 v[14:17], v[150:153], v[212:215], v[14:17]
	v_mfma_f32_16x16x32_bf16 v[10:13], v[158:161], v[212:215], v[10:13]
	v_mfma_f32_16x16x32_bf16 v[54:57], v[162:165], v[178:181], v[54:57]
	v_mfma_f32_16x16x32_bf16 v[50:53], v[170:173], v[178:181], v[50:53]
	v_mfma_f32_16x16x32_bf16 v[38:41], v[162:165], v[186:189], v[38:41]
	v_mfma_f32_16x16x32_bf16 v[34:37], v[170:173], v[186:189], v[34:37]
	v_mfma_f32_16x16x32_bf16 v[22:25], v[162:165], v[200:203], v[22:25]
	v_mfma_f32_16x16x32_bf16 v[18:21], v[170:173], v[200:203], v[18:21]
	v_mfma_f32_16x16x32_bf16 v[6:9], v[162:165], v[208:211], v[6:9]
	v_mfma_f32_16x16x32_bf16 v[2:5], v[170:173], v[208:211], v[2:5]
	v_mfma_f32_16x16x32_bf16 v[54:57], v[166:169], v[182:185], v[54:57]
	v_mfma_f32_16x16x32_bf16 v[50:53], v[174:177], v[182:185], v[50:53]
	v_mfma_f32_16x16x32_bf16 v[38:41], v[166:169], v[190:193], v[38:41]
	v_mfma_f32_16x16x32_bf16 v[34:37], v[174:177], v[190:193], v[34:37]
	v_mfma_f32_16x16x32_bf16 v[22:25], v[166:169], v[204:207], v[22:25]
	v_mfma_f32_16x16x32_bf16 v[18:21], v[174:177], v[204:207], v[18:21]
	v_mfma_f32_16x16x32_bf16 v[6:9], v[166:169], v[212:215], v[6:9]
	v_mfma_f32_16x16x32_bf16 v[2:5], v[174:177], v[212:215], v[2:5]
	s_setprio 0
	s_barrier
	v_or_b32_e32 v146, 0x18000, v145
	v_add_u32_e32 v150, 0x18400, v145
	v_add_u32_e32 v154, 0x18800, v145
	v_add_u32_e32 v158, 0x18c00, v145
	v_or_b32_e32 v162, 0x1c000, v145
	v_add_u32_e32 v166, 0x1c400, v145
	v_add_u32_e32 v170, 0x1c800, v145
	v_add_u32_e32 v174, 0x1cc00, v145
	ds_read_b128 v[146:149], v146
	ds_read_b128 v[150:153], v150
	ds_read_b128 v[154:157], v154
	ds_read_b128 v[158:161], v158
	ds_read_b128 v[162:165], v162
	ds_read_b128 v[166:169], v166
	ds_read_b128 v[170:173], v170
	ds_read_b128 v[174:177], v174
	s_add_u32 s54, s54, 0x40000
	s_addc_u32 s55, s55, 0
	s_mov_b32 m0, s65
	ds_read_b128 v[178:181], v144 offset:32768
	ds_read_b128 v[182:185], v144 offset:33792
	ds_read_b128 v[186:189], v144 offset:34816
	ds_read_b128 v[190:193], v144 offset:35840
	ds_read_b128 v[200:203], v144 offset:36864
	ds_read_b128 v[204:207], v144 offset:37888
	ds_read_b128 v[208:211], v144 offset:38912
	ds_read_b128 v[212:215], v144 offset:39936
	global_load_lds_dwordx4 v134, s[54:55]
	s_mov_b32 m0, s66
	s_nop 0
	global_load_lds_dwordx4 v132, s[54:55]
	s_waitcnt vmcnt(8)
	s_waitcnt lgkmcnt(0)
	s_barrier
	s_setprio 1
	v_mfma_f32_16x16x32_bf16 v[126:129], v[146:149], v[178:181], v[126:129]
	v_mfma_f32_16x16x32_bf16 v[122:125], v[154:157], v[178:181], v[122:125]
	v_mfma_f32_16x16x32_bf16 v[110:113], v[146:149], v[186:189], v[110:113]
	v_mfma_f32_16x16x32_bf16 v[106:109], v[154:157], v[186:189], v[106:109]
	v_mfma_f32_16x16x32_bf16 v[94:97], v[146:149], v[200:203], v[94:97]
	v_mfma_f32_16x16x32_bf16 v[90:93], v[154:157], v[200:203], v[90:93]
	v_mfma_f32_16x16x32_bf16 v[78:81], v[146:149], v[208:211], v[78:81]
	v_mfma_f32_16x16x32_bf16 v[74:77], v[154:157], v[208:211], v[74:77]
	v_mfma_f32_16x16x32_bf16 v[126:129], v[150:153], v[182:185], v[126:129]
	v_mfma_f32_16x16x32_bf16 v[122:125], v[158:161], v[182:185], v[122:125]
	v_mfma_f32_16x16x32_bf16 v[110:113], v[150:153], v[190:193], v[110:113]
	v_mfma_f32_16x16x32_bf16 v[106:109], v[158:161], v[190:193], v[106:109]
	v_mfma_f32_16x16x32_bf16 v[94:97], v[150:153], v[204:207], v[94:97]
	v_mfma_f32_16x16x32_bf16 v[90:93], v[158:161], v[204:207], v[90:93]
	v_mfma_f32_16x16x32_bf16 v[78:81], v[150:153], v[212:215], v[78:81]
	v_mfma_f32_16x16x32_bf16 v[74:77], v[158:161], v[212:215], v[74:77]
	v_mfma_f32_16x16x32_bf16 v[118:121], v[162:165], v[178:181], v[118:121]
	v_mfma_f32_16x16x32_bf16 v[114:117], v[170:173], v[178:181], v[114:117]
	v_mfma_f32_16x16x32_bf16 v[102:105], v[162:165], v[186:189], v[102:105]
	v_mfma_f32_16x16x32_bf16 v[98:101], v[170:173], v[186:189], v[98:101]
	v_mfma_f32_16x16x32_bf16 v[86:89], v[162:165], v[200:203], v[86:89]
	v_mfma_f32_16x16x32_bf16 v[82:85], v[170:173], v[200:203], v[82:85]
	v_mfma_f32_16x16x32_bf16 v[70:73], v[162:165], v[208:211], v[70:73]
	v_mfma_f32_16x16x32_bf16 v[66:69], v[170:173], v[208:211], v[66:69]
	v_mfma_f32_16x16x32_bf16 v[118:121], v[166:169], v[182:185], v[118:121]
	v_mfma_f32_16x16x32_bf16 v[114:117], v[174:177], v[182:185], v[114:117]
	v_mfma_f32_16x16x32_bf16 v[102:105], v[166:169], v[190:193], v[102:105]
	v_mfma_f32_16x16x32_bf16 v[98:101], v[174:177], v[190:193], v[98:101]
	v_mfma_f32_16x16x32_bf16 v[86:89], v[166:169], v[204:207], v[86:89]
	v_mfma_f32_16x16x32_bf16 v[82:85], v[174:177], v[204:207], v[82:85]
	v_mfma_f32_16x16x32_bf16 v[70:73], v[166:169], v[212:215], v[70:73]
	v_mfma_f32_16x16x32_bf16 v[66:69], v[174:177], v[212:215], v[66:69]
	s_setprio 0
	s_barrier
	s_mov_b32 m0, s67
	v_lshl_add_u64 v[194:195], v[194:195], 0, s[18:19]
	s_add_u32 s52, s52, 0x40080
	ds_read_b128 v[178:181], v144 offset:49152
	ds_read_b128 v[182:185], v144 offset:50176
	ds_read_b128 v[186:189], v144 offset:51200
	ds_read_b128 v[190:193], v144 offset:52224
	ds_read_b128 v[200:203], v144 offset:53248
	ds_read_b128 v[204:207], v144 offset:54272
	ds_read_b128 v[208:211], v144 offset:55296
	ds_read_b128 v[212:215], v144 offset:56320
	global_load_lds_dwordx4 v[194:195], off
	v_lshl_add_u64 v[194:195], v[216:217], 0, s[18:19]
	s_mov_b32 m0, s80
	s_addc_u32 s53, s53, 0
	global_load_lds_dwordx4 v[194:195], off
	s_mov_b32 m0, s84
	s_nop 0
	global_load_lds_dwordx4 v0, s[52:53]
	s_mov_b32 m0, s85
	s_nop 0
	global_load_lds_dwordx4 v130, s[52:53]
	v_lshl_add_u64 v[194:195], v[218:219], 0, s[18:19]
	s_mov_b32 m0, s82
	s_nop 0
	global_load_lds_dwordx4 v[194:195], off
	v_lshl_add_u64 v[194:195], v[220:221], 0, s[18:19]
	s_mov_b32 m0, s83
	s_nop 0
	global_load_lds_dwordx4 v[194:195], off
	s_waitcnt vmcnt(8)
	s_waitcnt lgkmcnt(0)
	s_barrier
	s_setprio 1
	v_mfma_f32_16x16x32_bf16 v[62:65], v[146:149], v[178:181], v[62:65]
	v_mfma_f32_16x16x32_bf16 v[58:61], v[154:157], v[178:181], v[58:61]
	v_mfma_f32_16x16x32_bf16 v[46:49], v[146:149], v[186:189], v[46:49]
	v_mfma_f32_16x16x32_bf16 v[42:45], v[154:157], v[186:189], v[42:45]
	v_mfma_f32_16x16x32_bf16 v[30:33], v[146:149], v[200:203], v[30:33]
	v_mfma_f32_16x16x32_bf16 v[26:29], v[154:157], v[200:203], v[26:29]
	v_mfma_f32_16x16x32_bf16 v[14:17], v[146:149], v[208:211], v[14:17]
	v_mfma_f32_16x16x32_bf16 v[10:13], v[154:157], v[208:211], v[10:13]
	v_mfma_f32_16x16x32_bf16 v[62:65], v[150:153], v[182:185], v[62:65]
	v_mfma_f32_16x16x32_bf16 v[58:61], v[158:161], v[182:185], v[58:61]
	v_mfma_f32_16x16x32_bf16 v[46:49], v[150:153], v[190:193], v[46:49]
	v_mfma_f32_16x16x32_bf16 v[42:45], v[158:161], v[190:193], v[42:45]
	v_mfma_f32_16x16x32_bf16 v[30:33], v[150:153], v[204:207], v[30:33]
	v_mfma_f32_16x16x32_bf16 v[26:29], v[158:161], v[204:207], v[26:29]
	v_mfma_f32_16x16x32_bf16 v[14:17], v[150:153], v[212:215], v[14:17]
	v_mfma_f32_16x16x32_bf16 v[10:13], v[158:161], v[212:215], v[10:13]
	v_mfma_f32_16x16x32_bf16 v[54:57], v[162:165], v[178:181], v[54:57]
	v_mfma_f32_16x16x32_bf16 v[50:53], v[170:173], v[178:181], v[50:53]
	v_mfma_f32_16x16x32_bf16 v[38:41], v[162:165], v[186:189], v[38:41]
	v_mfma_f32_16x16x32_bf16 v[34:37], v[170:173], v[186:189], v[34:37]
	v_mfma_f32_16x16x32_bf16 v[22:25], v[162:165], v[200:203], v[22:25]
	v_mfma_f32_16x16x32_bf16 v[18:21], v[170:173], v[200:203], v[18:21]
	v_mfma_f32_16x16x32_bf16 v[6:9], v[162:165], v[208:211], v[6:9]
	v_mfma_f32_16x16x32_bf16 v[2:5], v[170:173], v[208:211], v[2:5]
	v_mfma_f32_16x16x32_bf16 v[54:57], v[166:169], v[182:185], v[54:57]
	v_mfma_f32_16x16x32_bf16 v[50:53], v[174:177], v[182:185], v[50:53]
	v_mfma_f32_16x16x32_bf16 v[38:41], v[166:169], v[190:193], v[38:41]
	v_mfma_f32_16x16x32_bf16 v[34:37], v[174:177], v[190:193], v[34:37]
	v_mfma_f32_16x16x32_bf16 v[22:25], v[166:169], v[204:207], v[22:25]
	v_mfma_f32_16x16x32_bf16 v[18:21], v[174:177], v[204:207], v[18:21]
	v_mfma_f32_16x16x32_bf16 v[6:9], v[166:169], v[212:215], v[6:9]
	v_mfma_f32_16x16x32_bf16 v[2:5], v[174:177], v[212:215], v[2:5]
	s_setprio 0
	s_barrier
	s_add_i32 s92, s92, 2
	s_add_u32 s50, s50, 0x100
	s_addc_u32 s51, s51, 0
	s_cmp_gt_u32 s92, 13
	s_cbranch_scc0 .LBB0_397
	s_and_b64 vcc, exec, s[14:15]
	s_cbranch_vccz .LBB0_400
	s_barrier

.LBB0_438:
	v_or_b32_e32 v163, 0x10000, v162
	v_add_u32_e32 v168, 0x10400, v162
	ds_read_b128 v[164:167], v163
	ds_read_b128 v[168:171], v168
	v_add_u32_e32 v163, 0x10800, v162
	v_add_u32_e32 v176, 0x10c00, v162
	s_add_u32 s50, s16, s48
	ds_read_b128 v[172:175], v163
	ds_read_b128 v[176:179], v176
	v_or_b32_e32 v163, 0x14000, v162
	v_add_u32_e32 v184, 0x14400, v162
	s_addc_u32 s51, s17, s49
	ds_read_b128 v[180:183], v163
	ds_read_b128 v[184:187], v184
	v_add_u32_e32 v163, 0x14800, v162
	v_add_u32_e32 v192, 0x14c00, v162
	s_add_u32 s50, s50, 0x100
	ds_read_b128 v[188:191], v163
	ds_read_b128 v[192:195], v192
	s_addc_u32 s51, s51, 0
	s_add_u32 s91, s41, s48
	s_addc_u32 s92, s89, s49
	s_cmpk_eq_i32 s48, 0x700
	s_cselect_b32 s53, s29, s51
	s_cselect_b32 s52, s39, s50
	s_cselect_b32 s51, s45, s92
	s_cselect_b32 s50, s44, s91
	v_lshl_add_u64 v[226:227], v[156:157], 0, s[48:49]
	s_add_i32 m0, s58, 0xc000
	ds_read_b128 v[200:203], v161
	ds_read_b128 v[204:207], v161 offset:1024
	ds_read_b128 v[208:211], v161 offset:2048
	ds_read_b128 v[212:215], v161 offset:3072
	ds_read_b128 v[216:219], v161 offset:4096
	ds_read_b128 v[220:223], v161 offset:5120
	ds_read_b128 v[236:239], v161 offset:6144
	ds_read_b128 v[240:243], v161 offset:7168
	global_load_lds_dwordx4 v[226:227], off
	v_lshl_add_u64 v[226:227], v[158:159], 0, s[48:49]
	s_add_i32 m0, s58, 0xe000
	s_nop 0
	global_load_lds_dwordx4 v[226:227], off
	s_waitcnt vmcnt(8)
	s_waitcnt lgkmcnt(0)
	s_barrier
	s_setprio 1
	v_mfma_f32_16x16x32_bf16 v[126:129], v[164:167], v[200:203], v[126:129]
	v_mfma_f32_16x16x32_bf16 v[122:125], v[172:175], v[200:203], v[122:125]
	v_mfma_f32_16x16x32_bf16 v[110:113], v[164:167], v[208:211], v[110:113]
	v_mfma_f32_16x16x32_bf16 v[106:109], v[172:175], v[208:211], v[106:109]
	v_mfma_f32_16x16x32_bf16 v[94:97], v[164:167], v[216:219], v[94:97]
	v_mfma_f32_16x16x32_bf16 v[90:93], v[172:175], v[216:219], v[90:93]
	v_mfma_f32_16x16x32_bf16 v[86:89], v[164:167], v[236:239], v[86:89]
	v_mfma_f32_16x16x32_bf16 v[78:81], v[172:175], v[236:239], v[78:81]
	v_mfma_f32_16x16x32_bf16 v[126:129], v[168:171], v[204:207], v[126:129]
	v_mfma_f32_16x16x32_bf16 v[122:125], v[176:179], v[204:207], v[122:125]
	v_mfma_f32_16x16x32_bf16 v[110:113], v[168:171], v[212:215], v[110:113]
	v_mfma_f32_16x16x32_bf16 v[106:109], v[176:179], v[212:215], v[106:109]
	v_mfma_f32_16x16x32_bf16 v[94:97], v[168:171], v[220:223], v[94:97]
	v_mfma_f32_16x16x32_bf16 v[90:93], v[176:179], v[220:223], v[90:93]
	v_mfma_f32_16x16x32_bf16 v[86:89], v[168:171], v[240:243], v[86:89]
	v_mfma_f32_16x16x32_bf16 v[78:81], v[176:179], v[240:243], v[78:81]
	v_mfma_f32_16x16x32_bf16 v[118:121], v[180:183], v[200:203], v[118:121]
	v_mfma_f32_16x16x32_bf16 v[114:117], v[188:191], v[200:203], v[114:117]
	v_mfma_f32_16x16x32_bf16 v[102:105], v[180:183], v[208:211], v[102:105]
	v_mfma_f32_16x16x32_bf16 v[98:101], v[188:191], v[208:211], v[98:101]
	v_mfma_f32_16x16x32_bf16 v[82:85], v[180:183], v[216:219], v[82:85]
	v_mfma_f32_16x16x32_bf16 v[74:77], v[188:191], v[216:219], v[74:77]
	v_mfma_f32_16x16x32_bf16 v[70:73], v[180:183], v[236:239], v[70:73]
	v_mfma_f32_16x16x32_bf16 v[66:69], v[188:191], v[236:239], v[66:69]
	v_mfma_f32_16x16x32_bf16 v[118:121], v[184:187], v[204:207], v[118:121]
	v_mfma_f32_16x16x32_bf16 v[114:117], v[192:195], v[204:207], v[114:117]
	v_mfma_f32_16x16x32_bf16 v[102:105], v[184:187], v[212:215], v[102:105]
	v_mfma_f32_16x16x32_bf16 v[98:101], v[192:195], v[212:215], v[98:101]
	v_mfma_f32_16x16x32_bf16 v[82:85], v[184:187], v[220:223], v[82:85]
	v_mfma_f32_16x16x32_bf16 v[74:77], v[192:195], v[220:223], v[74:77]
	v_mfma_f32_16x16x32_bf16 v[70:73], v[184:187], v[240:243], v[70:73]
	v_mfma_f32_16x16x32_bf16 v[66:69], v[192:195], v[240:243], v[66:69]
	s_setprio 0
	s_barrier
	s_mov_b32 m0, s59
	v_lshl_add_u64 v[226:227], s[50:51], 0, v[0:1]
	s_add_u32 s92, s50, 0x40000
	ds_read_b128 v[200:203], v161 offset:16384
	ds_read_b128 v[204:207], v161 offset:17408
	ds_read_b128 v[208:211], v161 offset:18432
	ds_read_b128 v[212:215], v161 offset:19456
	ds_read_b128 v[216:219], v161 offset:20480
	ds_read_b128 v[220:223], v161 offset:21504
	ds_read_b128 v[236:239], v161 offset:22528
	ds_read_b128 v[240:243], v161 offset:23552
	global_load_lds_dwordx4 v0, s[50:51]
	v_lshl_add_u64 v[244:245], s[50:51], 0, v[142:143]
	s_mov_b32 m0, s60
	s_addc_u32 s93, s51, 0
	global_load_lds_dwordx4 v142, s[50:51]
	s_mov_b32 m0, s61
	v_lshl_add_u64 v[248:249], s[52:53], 0, v[144:145]
	global_load_lds_dwordx4 v0, s[92:93]
	s_mov_b32 m0, s62
	s_nop 0
	global_load_lds_dwordx4 v142, s[92:93]
	v_lshl_add_u64 v[246:247], s[52:53], 0, v[148:149]
	s_mov_b32 m0, s58
	s_nop 0
	global_load_lds_dwordx4 v148, s[52:53]
	s_mov_b32 m0, s63
	s_nop 0
	global_load_lds_dwordx4 v144, s[52:53]
	s_waitcnt vmcnt(8)
	s_waitcnt lgkmcnt(0)
	s_barrier
	s_setprio 1
	v_mfma_f32_16x16x32_bf16 v[62:65], v[164:167], v[200:203], v[62:65]
	v_mfma_f32_16x16x32_bf16 v[58:61], v[172:175], v[200:203], v[58:61]
	v_mfma_f32_16x16x32_bf16 v[54:57], v[164:167], v[208:211], v[54:57]
	v_mfma_f32_16x16x32_bf16 v[46:49], v[172:175], v[208:211], v[46:49]
	v_mfma_f32_16x16x32_bf16 v[30:33], v[164:167], v[216:219], v[30:33]
	v_mfma_f32_16x16x32_bf16 v[26:29], v[172:175], v[216:219], v[26:29]
	v_mfma_f32_16x16x32_bf16 v[22:25], v[164:167], v[236:239], v[22:25]
	v_mfma_f32_16x16x32_bf16 v[14:17], v[172:175], v[236:239], v[14:17]
	v_mfma_f32_16x16x32_bf16 v[62:65], v[168:171], v[204:207], v[62:65]
	v_mfma_f32_16x16x32_bf16 v[58:61], v[176:179], v[204:207], v[58:61]
	v_mfma_f32_16x16x32_bf16 v[54:57], v[168:171], v[212:215], v[54:57]
	v_mfma_f32_16x16x32_bf16 v[46:49], v[176:179], v[212:215], v[46:49]
	v_mfma_f32_16x16x32_bf16 v[30:33], v[168:171], v[220:223], v[30:33]
	v_mfma_f32_16x16x32_bf16 v[26:29], v[176:179], v[220:223], v[26:29]
	v_mfma_f32_16x16x32_bf16 v[22:25], v[168:171], v[240:243], v[22:25]
	v_mfma_f32_16x16x32_bf16 v[14:17], v[176:179], v[240:243], v[14:17]
	v_mfma_f32_16x16x32_bf16 v[50:53], v[180:183], v[200:203], v[50:53]
	v_mfma_f32_16x16x32_bf16 v[42:45], v[188:191], v[200:203], v[42:45]
	v_mfma_f32_16x16x32_bf16 v[38:41], v[180:183], v[208:211], v[38:41]
	v_mfma_f32_16x16x32_bf16 v[34:37], v[188:191], v[208:211], v[34:37]
	v_mfma_f32_16x16x32_bf16 v[18:21], v[180:183], v[216:219], v[18:21]
	v_mfma_f32_16x16x32_bf16 v[10:13], v[188:191], v[216:219], v[10:13]
	v_mfma_f32_16x16x32_bf16 v[6:9], v[180:183], v[236:239], v[6:9]
	v_mfma_f32_16x16x32_bf16 v[2:5], v[188:191], v[236:239], v[2:5]
	v_mfma_f32_16x16x32_bf16 v[50:53], v[184:187], v[204:207], v[50:53]
	v_mfma_f32_16x16x32_bf16 v[42:45], v[192:195], v[204:207], v[42:45]
	v_mfma_f32_16x16x32_bf16 v[38:41], v[184:187], v[212:215], v[38:41]
	v_mfma_f32_16x16x32_bf16 v[34:37], v[192:195], v[212:215], v[34:37]
	v_mfma_f32_16x16x32_bf16 v[18:21], v[184:187], v[220:223], v[18:21]
	v_mfma_f32_16x16x32_bf16 v[10:13], v[192:195], v[220:223], v[10:13]
	v_mfma_f32_16x16x32_bf16 v[6:9], v[184:187], v[240:243], v[6:9]
	v_mfma_f32_16x16x32_bf16 v[2:5], v[192:195], v[240:243], v[2:5]
	s_setprio 0
	s_barrier
	v_or_b32_e32 v163, 0x18000, v162
	v_add_u32_e32 v168, 0x18400, v162
	ds_read_b128 v[164:167], v163
	ds_read_b128 v[168:171], v168
	v_add_u32_e32 v163, 0x18800, v162
	v_add_u32_e32 v176, 0x18c00, v162
	ds_read_b128 v[172:175], v163
	ds_read_b128 v[176:179], v176
	v_or_b32_e32 v163, 0x1c000, v162
	v_add_u32_e32 v184, 0x1c400, v162
	ds_read_b128 v[180:183], v163
	ds_read_b128 v[184:187], v184
	v_add_u32_e32 v163, 0x1c800, v162
	v_add_u32_e32 v192, 0x1cc00, v162
	ds_read_b128 v[188:191], v163
	ds_read_b128 v[192:195], v192
	s_add_u32 s52, s52, 0x40000
	s_addc_u32 s53, s53, 0
	s_mov_b32 m0, s64
	v_lshl_add_u64 v[228:229], s[52:53], 0, v[148:149]
	ds_read_b128 v[200:203], v161 offset:32768
	ds_read_b128 v[204:207], v161 offset:33792
	ds_read_b128 v[208:211], v161 offset:34816
	ds_read_b128 v[212:215], v161 offset:35840
	ds_read_b128 v[216:219], v161 offset:36864
	ds_read_b128 v[220:223], v161 offset:37888
	ds_read_b128 v[236:239], v161 offset:38912
	ds_read_b128 v[240:243], v161 offset:39936
	global_load_lds_dwordx4 v148, s[52:53]
	v_lshl_add_u64 v[228:229], s[52:53], 0, v[144:145]
	s_mov_b32 m0, s65
	s_nop 0
	global_load_lds_dwordx4 v144, s[52:53]
	s_waitcnt vmcnt(8)
	s_waitcnt lgkmcnt(0)
	s_barrier
	s_setprio 1
	v_mfma_f32_16x16x32_bf16 v[126:129], v[164:167], v[200:203], v[126:129]
	v_mfma_f32_16x16x32_bf16 v[122:125], v[172:175], v[200:203], v[122:125]
	v_mfma_f32_16x16x32_bf16 v[110:113], v[164:167], v[208:211], v[110:113]
	v_mfma_f32_16x16x32_bf16 v[106:109], v[172:175], v[208:211], v[106:109]
	v_mfma_f32_16x16x32_bf16 v[94:97], v[164:167], v[216:219], v[94:97]
	v_mfma_f32_16x16x32_bf16 v[90:93], v[172:175], v[216:219], v[90:93]
	v_mfma_f32_16x16x32_bf16 v[86:89], v[164:167], v[236:239], v[86:89]
	v_mfma_f32_16x16x32_bf16 v[78:81], v[172:175], v[236:239], v[78:81]
	v_mfma_f32_16x16x32_bf16 v[126:129], v[168:171], v[204:207], v[126:129]
	v_mfma_f32_16x16x32_bf16 v[122:125], v[176:179], v[204:207], v[122:125]
	v_mfma_f32_16x16x32_bf16 v[110:113], v[168:171], v[212:215], v[110:113]
	v_mfma_f32_16x16x32_bf16 v[106:109], v[176:179], v[212:215], v[106:109]
	v_mfma_f32_16x16x32_bf16 v[94:97], v[168:171], v[220:223], v[94:97]
	v_mfma_f32_16x16x32_bf16 v[90:93], v[176:179], v[220:223], v[90:93]
	v_mfma_f32_16x16x32_bf16 v[86:89], v[168:171], v[240:243], v[86:89]
	v_mfma_f32_16x16x32_bf16 v[78:81], v[176:179], v[240:243], v[78:81]
	v_mfma_f32_16x16x32_bf16 v[118:121], v[180:183], v[200:203], v[118:121]
	v_mfma_f32_16x16x32_bf16 v[114:117], v[188:191], v[200:203], v[114:117]
	v_mfma_f32_16x16x32_bf16 v[102:105], v[180:183], v[208:211], v[102:105]
	v_mfma_f32_16x16x32_bf16 v[98:101], v[188:191], v[208:211], v[98:101]
	v_mfma_f32_16x16x32_bf16 v[82:85], v[180:183], v[216:219], v[82:85]
	v_mfma_f32_16x16x32_bf16 v[74:77], v[188:191], v[216:219], v[74:77]
	v_mfma_f32_16x16x32_bf16 v[70:73], v[180:183], v[236:239], v[70:73]
	v_mfma_f32_16x16x32_bf16 v[66:69], v[188:191], v[236:239], v[66:69]
	v_mfma_f32_16x16x32_bf16 v[118:121], v[184:187], v[204:207], v[118:121]
	v_mfma_f32_16x16x32_bf16 v[114:117], v[192:195], v[204:207], v[114:117]
	v_mfma_f32_16x16x32_bf16 v[102:105], v[184:187], v[212:215], v[102:105]
	v_mfma_f32_16x16x32_bf16 v[98:101], v[192:195], v[212:215], v[98:101]
	v_mfma_f32_16x16x32_bf16 v[82:85], v[184:187], v[220:223], v[82:85]
	v_mfma_f32_16x16x32_bf16 v[74:77], v[192:195], v[220:223], v[74:77]
	v_mfma_f32_16x16x32_bf16 v[70:73], v[184:187], v[240:243], v[70:73]
	v_mfma_f32_16x16x32_bf16 v[66:69], v[192:195], v[240:243], v[66:69]
	s_setprio 0
	s_barrier
	s_mov_b32 m0, s66
	v_lshl_add_u64 v[226:227], v[226:227], 0, s[18:19]
	s_add_u32 s50, s50, 0x40080
	ds_read_b128 v[200:203], v161 offset:49152
	ds_read_b128 v[204:207], v161 offset:50176
	ds_read_b128 v[208:211], v161 offset:51200
	ds_read_b128 v[212:215], v161 offset:52224
	ds_read_b128 v[216:219], v161 offset:53248
	ds_read_b128 v[220:223], v161 offset:54272
	ds_read_b128 v[236:239], v161 offset:55296
	ds_read_b128 v[240:243], v161 offset:56320
	global_load_lds_dwordx4 v[226:227], off
	v_lshl_add_u64 v[226:227], v[244:245], 0, s[18:19]
	s_mov_b32 m0, s67
	s_addc_u32 s51, s51, 0
	global_load_lds_dwordx4 v[226:227], off
	s_mov_b32 m0, s83
	s_nop 0
	global_load_lds_dwordx4 v0, s[50:51]
	s_mov_b32 m0, s84
	s_nop 0
	global_load_lds_dwordx4 v142, s[50:51]
	v_lshl_add_u64 v[226:227], v[246:247], 0, s[18:19]
	s_mov_b32 m0, s80
	s_nop 0
	global_load_lds_dwordx4 v[226:227], off
	v_lshl_add_u64 v[226:227], v[248:249], 0, s[18:19]
	s_mov_b32 m0, s82
	s_nop 0
	global_load_lds_dwordx4 v[226:227], off
	s_waitcnt vmcnt(8)
	s_waitcnt lgkmcnt(0)
	s_barrier
	s_setprio 1
	v_mfma_f32_16x16x32_bf16 v[62:65], v[164:167], v[200:203], v[62:65]
	v_mfma_f32_16x16x32_bf16 v[58:61], v[172:175], v[200:203], v[58:61]
	v_mfma_f32_16x16x32_bf16 v[54:57], v[164:167], v[208:211], v[54:57]
	v_mfma_f32_16x16x32_bf16 v[46:49], v[172:175], v[208:211], v[46:49]
	v_mfma_f32_16x16x32_bf16 v[30:33], v[164:167], v[216:219], v[30:33]
	v_mfma_f32_16x16x32_bf16 v[26:29], v[172:175], v[216:219], v[26:29]
	v_mfma_f32_16x16x32_bf16 v[22:25], v[164:167], v[236:239], v[22:25]
	v_mfma_f32_16x16x32_bf16 v[14:17], v[172:175], v[236:239], v[14:17]
	v_mfma_f32_16x16x32_bf16 v[62:65], v[168:171], v[204:207], v[62:65]
	v_mfma_f32_16x16x32_bf16 v[58:61], v[176:179], v[204:207], v[58:61]
	v_mfma_f32_16x16x32_bf16 v[54:57], v[168:171], v[212:215], v[54:57]
	v_mfma_f32_16x16x32_bf16 v[46:49], v[176:179], v[212:215], v[46:49]
	v_mfma_f32_16x16x32_bf16 v[30:33], v[168:171], v[220:223], v[30:33]
	v_mfma_f32_16x16x32_bf16 v[26:29], v[176:179], v[220:223], v[26:29]
	v_mfma_f32_16x16x32_bf16 v[22:25], v[168:171], v[240:243], v[22:25]
	v_mfma_f32_16x16x32_bf16 v[14:17], v[176:179], v[240:243], v[14:17]
	v_mfma_f32_16x16x32_bf16 v[50:53], v[180:183], v[200:203], v[50:53]
	v_mfma_f32_16x16x32_bf16 v[42:45], v[188:191], v[200:203], v[42:45]
	v_mfma_f32_16x16x32_bf16 v[38:41], v[180:183], v[208:211], v[38:41]
	v_mfma_f32_16x16x32_bf16 v[34:37], v[188:191], v[208:211], v[34:37]
	v_mfma_f32_16x16x32_bf16 v[18:21], v[180:183], v[216:219], v[18:21]
	v_mfma_f32_16x16x32_bf16 v[10:13], v[188:191], v[216:219], v[10:13]
	v_mfma_f32_16x16x32_bf16 v[6:9], v[180:183], v[236:239], v[6:9]
	v_mfma_f32_16x16x32_bf16 v[2:5], v[188:191], v[236:239], v[2:5]
	v_mfma_f32_16x16x32_bf16 v[50:53], v[184:187], v[204:207], v[50:53]
	v_mfma_f32_16x16x32_bf16 v[42:45], v[192:195], v[204:207], v[42:45]
	v_mfma_f32_16x16x32_bf16 v[38:41], v[184:187], v[212:215], v[38:41]
	v_mfma_f32_16x16x32_bf16 v[34:37], v[192:195], v[212:215], v[34:37]
	v_mfma_f32_16x16x32_bf16 v[18:21], v[184:187], v[220:223], v[18:21]
	v_mfma_f32_16x16x32_bf16 v[10:13], v[192:195], v[220:223], v[10:13]
	v_mfma_f32_16x16x32_bf16 v[6:9], v[184:187], v[240:243], v[6:9]
	v_mfma_f32_16x16x32_bf16 v[2:5], v[192:195], v[240:243], v[2:5]
	s_setprio 0
	s_barrier
	s_add_i32 s90, s90, 2
	s_add_u32 s48, s48, 0x100
	s_addc_u32 s49, s49, 0
	s_cmp_gt_u32 s90, 13
	s_cbranch_scc0 .LBB0_438
	s_add_u32 s48, s41, 0xffffff00
	s_addc_u32 s49, s89, -1
	s_and_b64 vcc, exec, s[36:37]
	s_movk_i32 s90, 0xfea0
	s_cbranch_vccnz .LBB0_441
	v_lshl_add_u32 v2, s38, 8, v160
	v_ashrrev_i32_e32 v3, 31, v2
	v_lshl_add_u64 v[2:3], v[2:3], 3, s[14:15]
	global_load_dwordx2 v[150:151], v[2:3], off nt
	global_load_dwordx2 v[146:147], v[2:3], off offset:128 nt
	global_load_dwordx2 v[140:141], v[2:3], off offset:256 nt
	global_load_dwordx2 v[138:139], v[2:3], off offset:384 nt
	global_load_dwordx2 v[136:137], v[2:3], off offset:1024 nt
	global_load_dwordx2 v[134:135], v[2:3], off offset:1152 nt
	global_load_dwordx2 v[132:133], v[2:3], off offset:1280 nt
	global_load_dwordx2 v[130:131], v[2:3], off offset:1408 nt
	v_mov_b32_e32 v2, 0
	s_mov_b32 s0, s40
	s_mov_b32 s34, s38
	s_mov_b64 s[16:17], s[46:47]
	s_mov_b32 s85, s88
	v_mov_b32_e32 v3, v2
	v_mov_b64_e32 v[4:5], v[2:3]
	v_mov_b64_e32 v[6:7], v[2:3]
	v_mov_b64_e32 v[8:9], v[2:3]
	v_mov_b64_e32 v[10:11], v[2:3]
	v_mov_b64_e32 v[12:13], v[2:3]
	v_mov_b64_e32 v[14:15], v[2:3]
	v_mov_b64_e32 v[16:17], v[2:3]
	v_mov_b64_e32 v[18:19], v[2:3]
	v_mov_b64_e32 v[20:21], v[2:3]
	v_mov_b64_e32 v[22:23], v[2:3]
	v_mov_b64_e32 v[24:25], v[2:3]
	v_mov_b64_e32 v[26:27], v[2:3]
	v_mov_b64_e32 v[28:29], v[2:3]
	v_mov_b64_e32 v[30:31], v[2:3]
	v_mov_b64_e32 v[32:33], v[2:3]
	v_mov_b64_e32 v[34:35], v[2:3]
	v_mov_b64_e32 v[36:37], v[2:3]
	v_mov_b64_e32 v[38:39], v[2:3]
	v_mov_b64_e32 v[40:41], v[2:3]
	v_mov_b64_e32 v[42:43], v[2:3]
	v_mov_b64_e32 v[44:45], v[2:3]
	v_mov_b64_e32 v[46:47], v[2:3]
	v_mov_b64_e32 v[48:49], v[2:3]
	v_mov_b64_e32 v[50:51], v[2:3]
	v_mov_b64_e32 v[52:53], v[2:3]
	v_mov_b64_e32 v[54:55], v[2:3]
	v_mov_b64_e32 v[56:57], v[2:3]
	v_mov_b64_e32 v[58:59], v[2:3]
	v_mov_b64_e32 v[60:61], v[2:3]
	v_mov_b64_e32 v[62:63], v[2:3]
	v_mov_b64_e32 v[64:65], v[2:3]
	v_mov_b64_e32 v[66:67], v[2:3]
	v_mov_b64_e32 v[68:69], v[2:3]
	v_mov_b64_e32 v[70:71], v[2:3]
	v_mov_b64_e32 v[72:73], v[2:3]
	v_mov_b64_e32 v[74:75], v[2:3]
	v_mov_b64_e32 v[76:77], v[2:3]
	v_mov_b64_e32 v[78:79], v[2:3]
	v_mov_b64_e32 v[80:81], v[2:3]
	v_mov_b64_e32 v[82:83], v[2:3]
	v_mov_b64_e32 v[84:85], v[2:3]
	v_mov_b64_e32 v[86:87], v[2:3]
	v_mov_b64_e32 v[88:89], v[2:3]
	v_mov_b64_e32 v[90:91], v[2:3]
	v_mov_b64_e32 v[92:93], v[2:3]
	v_mov_b64_e32 v[94:95], v[2:3]
	v_mov_b64_e32 v[96:97], v[2:3]
	v_mov_b64_e32 v[98:99], v[2:3]
	v_mov_b64_e32 v[100:101], v[2:3]
	v_mov_b64_e32 v[102:103], v[2:3]
	v_mov_b64_e32 v[104:105], v[2:3]
	v_mov_b64_e32 v[106:107], v[2:3]
	v_mov_b64_e32 v[108:109], v[2:3]
	v_mov_b64_e32 v[110:111], v[2:3]
	v_mov_b64_e32 v[112:113], v[2:3]
	v_mov_b64_e32 v[114:115], v[2:3]
	v_mov_b64_e32 v[116:117], v[2:3]
	v_mov_b64_e32 v[118:119], v[2:3]
	v_mov_b64_e32 v[120:121], v[2:3]
	v_mov_b64_e32 v[122:123], v[2:3]
	v_mov_b64_e32 v[124:125], v[2:3]
	v_mov_b64_e32 v[126:127], v[2:3]
	v_mov_b64_e32 v[128:129], v[2:3]
	s_branch .LBB0_442

.LBB0_496:
	s_add_u32 s36, s48, s52
	s_addc_u32 s37, s49, s53
	v_or_b32_e32 v146, 0x10000, v145
	v_add_u32_e32 v150, 0x10400, v145
	v_add_u32_e32 v154, 0x10800, v145
	v_add_u32_e32 v158, 0x10c00, v145
	v_or_b32_e32 v162, 0x14000, v145
	v_add_u32_e32 v166, 0x14400, v145
	v_add_u32_e32 v170, 0x14800, v145
	v_add_u32_e32 v174, 0x14c00, v145
	s_add_u32 s36, s36, 0x100
	ds_read_b128 v[146:149], v146
	ds_read_b128 v[150:153], v150
	ds_read_b128 v[154:157], v154
	ds_read_b128 v[158:161], v158
	ds_read_b128 v[162:165], v162
	ds_read_b128 v[166:169], v166
	ds_read_b128 v[170:173], v170
	ds_read_b128 v[174:177], v174
	s_addc_u32 s37, s37, 0
	s_add_u32 s54, s92, s52
	s_addc_u32 s55, s93, s53
	s_cmpk_eq_i32 s52, 0x700
	s_cselect_b32 s57, s39, s37
	s_cselect_b32 s56, s94, s36
	s_cselect_b32 s55, s41, s55
	s_cselect_b32 s54, s95, s54
	v_lshl_add_u64 v[194:195], v[140:141], 0, s[52:53]
	s_add_i32 m0, s17, 0xc000
	ds_read_b128 v[178:181], v144
	ds_read_b128 v[182:185], v144 offset:1024
	ds_read_b128 v[186:189], v144 offset:2048
	ds_read_b128 v[190:193], v144 offset:3072
	ds_read_b128 v[200:203], v144 offset:4096
	ds_read_b128 v[204:207], v144 offset:5120
	ds_read_b128 v[208:211], v144 offset:6144
	ds_read_b128 v[212:215], v144 offset:7168
	global_load_lds_dwordx4 v[194:195], off
	v_lshl_add_u64 v[194:195], v[142:143], 0, s[52:53]
	s_add_i32 m0, s17, 0xe000
	s_nop 0
	global_load_lds_dwordx4 v[194:195], off
	s_waitcnt vmcnt(8)
	s_waitcnt lgkmcnt(0)
	s_barrier
	s_setprio 1
	v_mfma_f32_16x16x32_bf16 v[126:129], v[146:149], v[178:181], v[126:129]
	v_mfma_f32_16x16x32_bf16 v[122:125], v[154:157], v[178:181], v[122:125]
	v_mfma_f32_16x16x32_bf16 v[110:113], v[146:149], v[186:189], v[110:113]
	v_mfma_f32_16x16x32_bf16 v[106:109], v[154:157], v[186:189], v[106:109]
	v_mfma_f32_16x16x32_bf16 v[94:97], v[146:149], v[200:203], v[94:97]
	v_mfma_f32_16x16x32_bf16 v[90:93], v[154:157], v[200:203], v[90:93]
	v_mfma_f32_16x16x32_bf16 v[78:81], v[146:149], v[208:211], v[78:81]
	v_mfma_f32_16x16x32_bf16 v[74:77], v[154:157], v[208:211], v[74:77]
	v_mfma_f32_16x16x32_bf16 v[126:129], v[150:153], v[182:185], v[126:129]
	v_mfma_f32_16x16x32_bf16 v[122:125], v[158:161], v[182:185], v[122:125]
	v_mfma_f32_16x16x32_bf16 v[110:113], v[150:153], v[190:193], v[110:113]
	v_mfma_f32_16x16x32_bf16 v[106:109], v[158:161], v[190:193], v[106:109]
	v_mfma_f32_16x16x32_bf16 v[94:97], v[150:153], v[204:207], v[94:97]
	v_mfma_f32_16x16x32_bf16 v[90:93], v[158:161], v[204:207], v[90:93]
	v_mfma_f32_16x16x32_bf16 v[78:81], v[150:153], v[212:215], v[78:81]
	v_mfma_f32_16x16x32_bf16 v[74:77], v[158:161], v[212:215], v[74:77]
	v_mfma_f32_16x16x32_bf16 v[118:121], v[162:165], v[178:181], v[118:121]
	v_mfma_f32_16x16x32_bf16 v[114:117], v[170:173], v[178:181], v[114:117]
	v_mfma_f32_16x16x32_bf16 v[102:105], v[162:165], v[186:189], v[102:105]
	v_mfma_f32_16x16x32_bf16 v[98:101], v[170:173], v[186:189], v[98:101]
	v_mfma_f32_16x16x32_bf16 v[86:89], v[162:165], v[200:203], v[86:89]
	v_mfma_f32_16x16x32_bf16 v[82:85], v[170:173], v[200:203], v[82:85]
	v_mfma_f32_16x16x32_bf16 v[70:73], v[162:165], v[208:211], v[70:73]
	v_mfma_f32_16x16x32_bf16 v[66:69], v[170:173], v[208:211], v[66:69]
	v_mfma_f32_16x16x32_bf16 v[118:121], v[166:169], v[182:185], v[118:121]
	v_mfma_f32_16x16x32_bf16 v[114:117], v[174:177], v[182:185], v[114:117]
	v_mfma_f32_16x16x32_bf16 v[102:105], v[166:169], v[190:193], v[102:105]
	v_mfma_f32_16x16x32_bf16 v[98:101], v[174:177], v[190:193], v[98:101]
	v_mfma_f32_16x16x32_bf16 v[86:89], v[166:169], v[204:207], v[86:89]
	v_mfma_f32_16x16x32_bf16 v[82:85], v[174:177], v[204:207], v[82:85]
	v_mfma_f32_16x16x32_bf16 v[70:73], v[166:169], v[212:215], v[70:73]
	v_mfma_f32_16x16x32_bf16 v[66:69], v[174:177], v[212:215], v[66:69]
	s_setprio 0
	s_barrier
	s_mov_b32 m0, s60
	s_add_u32 s36, s54, 0x40000
	ds_read_b128 v[178:181], v144 offset:16384
	ds_read_b128 v[182:185], v144 offset:17408
	ds_read_b128 v[186:189], v144 offset:18432
	ds_read_b128 v[190:193], v144 offset:19456
	ds_read_b128 v[200:203], v144 offset:20480
	ds_read_b128 v[204:207], v144 offset:21504
	ds_read_b128 v[208:211], v144 offset:22528
	ds_read_b128 v[212:215], v144 offset:23552
	global_load_lds_dwordx4 v0, s[54:55]
	v_lshl_add_u64 v[216:217], s[54:55], 0, v[130:131]
	s_mov_b32 m0, s61
	s_addc_u32 s37, s55, 0
	global_load_lds_dwordx4 v130, s[54:55]
	s_mov_b32 m0, s62
	s_nop 0
	global_load_lds_dwordx4 v0, s[36:37]
	s_mov_b32 m0, s63
	s_nop 0
	global_load_lds_dwordx4 v130, s[36:37]
	s_mov_b32 m0, s17
	s_nop 0
	global_load_lds_dwordx4 v134, s[56:57]
	s_mov_b32 m0, s66
	s_nop 0
	global_load_lds_dwordx4 v132, s[56:57]
	s_waitcnt vmcnt(8)
	s_waitcnt lgkmcnt(0)
	s_barrier
	s_setprio 1
	v_mfma_f32_16x16x32_bf16 v[62:65], v[146:149], v[178:181], v[62:65]
	v_mfma_f32_16x16x32_bf16 v[58:61], v[154:157], v[178:181], v[58:61]
	v_mfma_f32_16x16x32_bf16 v[46:49], v[146:149], v[186:189], v[46:49]
	v_mfma_f32_16x16x32_bf16 v[42:45], v[154:157], v[186:189], v[42:45]
	v_mfma_f32_16x16x32_bf16 v[30:33], v[146:149], v[200:203], v[30:33]
	v_mfma_f32_16x16x32_bf16 v[26:29], v[154:157], v[200:203], v[26:29]
	v_mfma_f32_16x16x32_bf16 v[14:17], v[146:149], v[208:211], v[14:17]
	v_mfma_f32_16x16x32_bf16 v[10:13], v[154:157], v[208:211], v[10:13]
	v_mfma_f32_16x16x32_bf16 v[62:65], v[150:153], v[182:185], v[62:65]
	v_mfma_f32_16x16x32_bf16 v[58:61], v[158:161], v[182:185], v[58:61]
	v_mfma_f32_16x16x32_bf16 v[46:49], v[150:153], v[190:193], v[46:49]
	v_mfma_f32_16x16x32_bf16 v[42:45], v[158:161], v[190:193], v[42:45]
	v_mfma_f32_16x16x32_bf16 v[30:33], v[150:153], v[204:207], v[30:33]
	v_mfma_f32_16x16x32_bf16 v[26:29], v[158:161], v[204:207], v[26:29]
	v_mfma_f32_16x16x32_bf16 v[14:17], v[150:153], v[212:215], v[14:17]
	v_mfma_f32_16x16x32_bf16 v[10:13], v[158:161], v[212:215], v[10:13]
	v_mfma_f32_16x16x32_bf16 v[54:57], v[162:165], v[178:181], v[54:57]
	v_mfma_f32_16x16x32_bf16 v[50:53], v[170:173], v[178:181], v[50:53]
	v_mfma_f32_16x16x32_bf16 v[38:41], v[162:165], v[186:189], v[38:41]
	v_mfma_f32_16x16x32_bf16 v[34:37], v[170:173], v[186:189], v[34:37]
	v_mfma_f32_16x16x32_bf16 v[22:25], v[162:165], v[200:203], v[22:25]
	v_mfma_f32_16x16x32_bf16 v[18:21], v[170:173], v[200:203], v[18:21]
	v_mfma_f32_16x16x32_bf16 v[6:9], v[162:165], v[208:211], v[6:9]
	v_mfma_f32_16x16x32_bf16 v[2:5], v[170:173], v[208:211], v[2:5]
	v_mfma_f32_16x16x32_bf16 v[54:57], v[166:169], v[182:185], v[54:57]
	v_mfma_f32_16x16x32_bf16 v[50:53], v[174:177], v[182:185], v[50:53]
	v_mfma_f32_16x16x32_bf16 v[38:41], v[166:169], v[190:193], v[38:41]
	v_mfma_f32_16x16x32_bf16 v[34:37], v[174:177], v[190:193], v[34:37]
	v_mfma_f32_16x16x32_bf16 v[22:25], v[166:169], v[204:207], v[22:25]
	v_mfma_f32_16x16x32_bf16 v[18:21], v[174:177], v[204:207], v[18:21]
	v_mfma_f32_16x16x32_bf16 v[6:9], v[166:169], v[212:215], v[6:9]
	v_mfma_f32_16x16x32_bf16 v[2:5], v[174:177], v[212:215], v[2:5]
	s_setprio 0
	s_barrier
	v_or_b32_e32 v146, 0x18000, v145
	v_add_u32_e32 v150, 0x18400, v145
	v_add_u32_e32 v154, 0x18800, v145
	v_add_u32_e32 v158, 0x18c00, v145
	v_or_b32_e32 v162, 0x1c000, v145
	v_add_u32_e32 v166, 0x1c400, v145
	v_add_u32_e32 v170, 0x1c800, v145
	v_add_u32_e32 v174, 0x1cc00, v145
	ds_read_b128 v[146:149], v146
	ds_read_b128 v[150:153], v150
	ds_read_b128 v[154:157], v154
	ds_read_b128 v[158:161], v158
	ds_read_b128 v[162:165], v162
	ds_read_b128 v[166:169], v166
	ds_read_b128 v[170:173], v170
	ds_read_b128 v[174:177], v174
	s_add_u32 s36, s56, 0x40000
	s_addc_u32 s37, s57, 0
	s_mov_b32 m0, s67
	ds_read_b128 v[178:181], v144 offset:32768
	ds_read_b128 v[182:185], v144 offset:33792
	ds_read_b128 v[186:189], v144 offset:34816
	ds_read_b128 v[190:193], v144 offset:35840
	ds_read_b128 v[200:203], v144 offset:36864
	ds_read_b128 v[204:207], v144 offset:37888
	ds_read_b128 v[208:211], v144 offset:38912
	ds_read_b128 v[212:215], v144 offset:39936
	global_load_lds_dwordx4 v134, s[36:37]
	s_mov_b32 m0, s80
	s_nop 0
	global_load_lds_dwordx4 v132, s[36:37]
	s_waitcnt vmcnt(8)
	s_waitcnt lgkmcnt(0)
	s_barrier
	s_setprio 1
	v_mfma_f32_16x16x32_bf16 v[126:129], v[146:149], v[178:181], v[126:129]
	v_mfma_f32_16x16x32_bf16 v[122:125], v[154:157], v[178:181], v[122:125]
	v_mfma_f32_16x16x32_bf16 v[110:113], v[146:149], v[186:189], v[110:113]
	v_mfma_f32_16x16x32_bf16 v[106:109], v[154:157], v[186:189], v[106:109]
	v_mfma_f32_16x16x32_bf16 v[94:97], v[146:149], v[200:203], v[94:97]
	v_mfma_f32_16x16x32_bf16 v[90:93], v[154:157], v[200:203], v[90:93]
	v_mfma_f32_16x16x32_bf16 v[78:81], v[146:149], v[208:211], v[78:81]
	v_mfma_f32_16x16x32_bf16 v[74:77], v[154:157], v[208:211], v[74:77]
	v_mfma_f32_16x16x32_bf16 v[126:129], v[150:153], v[182:185], v[126:129]
	v_mfma_f32_16x16x32_bf16 v[122:125], v[158:161], v[182:185], v[122:125]
	v_mfma_f32_16x16x32_bf16 v[110:113], v[150:153], v[190:193], v[110:113]
	v_mfma_f32_16x16x32_bf16 v[106:109], v[158:161], v[190:193], v[106:109]
	v_mfma_f32_16x16x32_bf16 v[94:97], v[150:153], v[204:207], v[94:97]
	v_mfma_f32_16x16x32_bf16 v[90:93], v[158:161], v[204:207], v[90:93]
	v_mfma_f32_16x16x32_bf16 v[78:81], v[150:153], v[212:215], v[78:81]
	v_mfma_f32_16x16x32_bf16 v[74:77], v[158:161], v[212:215], v[74:77]
	v_mfma_f32_16x16x32_bf16 v[118:121], v[162:165], v[178:181], v[118:121]
	v_mfma_f32_16x16x32_bf16 v[114:117], v[170:173], v[178:181], v[114:117]
	v_mfma_f32_16x16x32_bf16 v[102:105], v[162:165], v[186:189], v[102:105]
	v_mfma_f32_16x16x32_bf16 v[98:101], v[170:173], v[186:189], v[98:101]
	v_mfma_f32_16x16x32_bf16 v[86:89], v[162:165], v[200:203], v[86:89]
	v_mfma_f32_16x16x32_bf16 v[82:85], v[170:173], v[200:203], v[82:85]
	v_mfma_f32_16x16x32_bf16 v[70:73], v[162:165], v[208:211], v[70:73]
	v_mfma_f32_16x16x32_bf16 v[66:69], v[170:173], v[208:211], v[66:69]
	v_mfma_f32_16x16x32_bf16 v[118:121], v[166:169], v[182:185], v[118:121]
	v_mfma_f32_16x16x32_bf16 v[114:117], v[174:177], v[182:185], v[114:117]
	v_mfma_f32_16x16x32_bf16 v[102:105], v[166:169], v[190:193], v[102:105]
	v_mfma_f32_16x16x32_bf16 v[98:101], v[174:177], v[190:193], v[98:101]
	v_mfma_f32_16x16x32_bf16 v[86:89], v[166:169], v[204:207], v[86:89]
	v_mfma_f32_16x16x32_bf16 v[82:85], v[174:177], v[204:207], v[82:85]
	v_mfma_f32_16x16x32_bf16 v[70:73], v[166:169], v[212:215], v[70:73]
	v_mfma_f32_16x16x32_bf16 v[66:69], v[174:177], v[212:215], v[66:69]
	s_setprio 0
	s_barrier
	s_add_i32 m0, s82, 0xffffff80
	s_add_u32 s36, s54, 0x40080
	ds_read_b128 v[178:181], v144 offset:49152
	ds_read_b128 v[182:185], v144 offset:50176
	ds_read_b128 v[186:189], v144 offset:51200
	ds_read_b128 v[190:193], v144 offset:52224
	ds_read_b128 v[200:203], v144 offset:53248
	ds_read_b128 v[204:207], v144 offset:54272
	ds_read_b128 v[208:211], v144 offset:55296
	ds_read_b128 v[212:215], v144 offset:56320
	global_load_lds_dwordx4 v0, s[54:55] offset:128
	v_lshl_add_u64 v[194:195], v[216:217], 0, s[18:19]
	s_mov_b32 m0, s83
	s_addc_u32 s37, s55, 0
	global_load_lds_dwordx4 v[194:195], off
	s_mov_b32 m0, s88
	s_nop 0
	global_load_lds_dwordx4 v0, s[36:37]
	s_mov_b32 m0, s89
	s_nop 0
	global_load_lds_dwordx4 v130, s[36:37]
	s_add_i32 m0, s84, 0xffffff80
	s_nop 0
	global_load_lds_dwordx4 v134, s[56:57] offset:128
	s_add_i32 m0, s85, 0xffffff80
	s_nop 0
	global_load_lds_dwordx4 v132, s[56:57] offset:128
	s_waitcnt vmcnt(8)
	s_waitcnt lgkmcnt(0)
	s_barrier
	s_setprio 1
	v_mfma_f32_16x16x32_bf16 v[62:65], v[146:149], v[178:181], v[62:65]
	v_mfma_f32_16x16x32_bf16 v[58:61], v[154:157], v[178:181], v[58:61]
	v_mfma_f32_16x16x32_bf16 v[46:49], v[146:149], v[186:189], v[46:49]
	v_mfma_f32_16x16x32_bf16 v[42:45], v[154:157], v[186:189], v[42:45]
	v_mfma_f32_16x16x32_bf16 v[30:33], v[146:149], v[200:203], v[30:33]
	v_mfma_f32_16x16x32_bf16 v[26:29], v[154:157], v[200:203], v[26:29]
	v_mfma_f32_16x16x32_bf16 v[14:17], v[146:149], v[208:211], v[14:17]
	v_mfma_f32_16x16x32_bf16 v[10:13], v[154:157], v[208:211], v[10:13]
	v_mfma_f32_16x16x32_bf16 v[62:65], v[150:153], v[182:185], v[62:65]
	v_mfma_f32_16x16x32_bf16 v[58:61], v[158:161], v[182:185], v[58:61]
	v_mfma_f32_16x16x32_bf16 v[46:49], v[150:153], v[190:193], v[46:49]
	v_mfma_f32_16x16x32_bf16 v[42:45], v[158:161], v[190:193], v[42:45]
	v_mfma_f32_16x16x32_bf16 v[30:33], v[150:153], v[204:207], v[30:33]
	v_mfma_f32_16x16x32_bf16 v[26:29], v[158:161], v[204:207], v[26:29]
	v_mfma_f32_16x16x32_bf16 v[14:17], v[150:153], v[212:215], v[14:17]
	v_mfma_f32_16x16x32_bf16 v[10:13], v[158:161], v[212:215], v[10:13]
	v_mfma_f32_16x16x32_bf16 v[54:57], v[162:165], v[178:181], v[54:57]
	v_mfma_f32_16x16x32_bf16 v[50:53], v[170:173], v[178:181], v[50:53]
	v_mfma_f32_16x16x32_bf16 v[38:41], v[162:165], v[186:189], v[38:41]
	v_mfma_f32_16x16x32_bf16 v[34:37], v[170:173], v[186:189], v[34:37]
	v_mfma_f32_16x16x32_bf16 v[22:25], v[162:165], v[200:203], v[22:25]
	v_mfma_f32_16x16x32_bf16 v[18:21], v[170:173], v[200:203], v[18:21]
	v_mfma_f32_16x16x32_bf16 v[6:9], v[162:165], v[208:211], v[6:9]
	v_mfma_f32_16x16x32_bf16 v[2:5], v[170:173], v[208:211], v[2:5]
	v_mfma_f32_16x16x32_bf16 v[54:57], v[166:169], v[182:185], v[54:57]
	v_mfma_f32_16x16x32_bf16 v[50:53], v[174:177], v[182:185], v[50:53]
	v_mfma_f32_16x16x32_bf16 v[38:41], v[166:169], v[190:193], v[38:41]
	v_mfma_f32_16x16x32_bf16 v[34:37], v[174:177], v[190:193], v[34:37]
	v_mfma_f32_16x16x32_bf16 v[22:25], v[166:169], v[204:207], v[22:25]
	v_mfma_f32_16x16x32_bf16 v[18:21], v[174:177], v[204:207], v[18:21]
	v_mfma_f32_16x16x32_bf16 v[6:9], v[166:169], v[212:215], v[6:9]
	v_mfma_f32_16x16x32_bf16 v[2:5], v[174:177], v[212:215], v[2:5]
	s_setprio 0
	s_barrier
	s_add_i32 vcc_lo, vcc_lo, 2
	s_add_u32 s52, s52, 0x100
	s_addc_u32 s53, s53, 0
	s_cmp_gt_u32 vcc_lo, 13
	s_cbranch_scc0 .LBB0_496
	s_and_b64 vcc, exec, s[14:15]
	s_cbranch_vccz .LBB0_499
	s_barrier

.LBB0_535:
	s_add_u32 s0, s42, s52
	s_addc_u32 s1, s43, s53
	v_or_b32_e32 v146, 0x10000, v145
	v_add_u32_e32 v150, 0x10400, v145
	v_add_u32_e32 v154, 0x10800, v145
	v_add_u32_e32 v158, 0x10c00, v145
	v_or_b32_e32 v162, 0x14000, v145
	v_add_u32_e32 v166, 0x14400, v145
	v_add_u32_e32 v170, 0x14800, v145
	v_add_u32_e32 v174, 0x14c00, v145
	s_add_u32 s0, s0, 0x100
	ds_read_b128 v[146:149], v146
	ds_read_b128 v[150:153], v150
	ds_read_b128 v[154:157], v154
	ds_read_b128 v[158:161], v158
	ds_read_b128 v[162:165], v162
	ds_read_b128 v[166:169], v166
	ds_read_b128 v[170:173], v170
	ds_read_b128 v[174:177], v174
	s_addc_u32 s1, s1, 0
	s_add_u32 s54, s29, s52
	s_addc_u32 s55, s93, s53
	s_cmpk_eq_i32 s52, 0x700
	s_cselect_b32 s57, s39, s1
	s_cselect_b32 s56, s94, s0
	s_cselect_b32 s55, s41, s55
	s_cselect_b32 s54, s95, s54
	v_lshl_add_u64 v[194:195], v[140:141], 0, s[52:53]
	s_add_i32 m0, s37, 0xc000
	ds_read_b128 v[178:181], v144
	ds_read_b128 v[182:185], v144 offset:1024
	ds_read_b128 v[186:189], v144 offset:2048
	ds_read_b128 v[190:193], v144 offset:3072
	ds_read_b128 v[200:203], v144 offset:4096
	ds_read_b128 v[204:207], v144 offset:5120
	ds_read_b128 v[208:211], v144 offset:6144
	ds_read_b128 v[212:215], v144 offset:7168
	global_load_lds_dwordx4 v[194:195], off
	v_lshl_add_u64 v[194:195], v[142:143], 0, s[52:53]
	s_add_i32 m0, s37, 0xe000
	s_nop 0
	global_load_lds_dwordx4 v[194:195], off
	s_waitcnt vmcnt(8)
	s_waitcnt lgkmcnt(0)
	s_barrier
	s_setprio 1
	v_mfma_f32_16x16x32_bf16 v[126:129], v[146:149], v[178:181], v[126:129]
	v_mfma_f32_16x16x32_bf16 v[122:125], v[154:157], v[178:181], v[122:125]
	v_mfma_f32_16x16x32_bf16 v[110:113], v[146:149], v[186:189], v[110:113]
	v_mfma_f32_16x16x32_bf16 v[106:109], v[154:157], v[186:189], v[106:109]
	v_mfma_f32_16x16x32_bf16 v[94:97], v[146:149], v[200:203], v[94:97]
	v_mfma_f32_16x16x32_bf16 v[90:93], v[154:157], v[200:203], v[90:93]
	v_mfma_f32_16x16x32_bf16 v[78:81], v[146:149], v[208:211], v[78:81]
	v_mfma_f32_16x16x32_bf16 v[74:77], v[154:157], v[208:211], v[74:77]
	v_mfma_f32_16x16x32_bf16 v[126:129], v[150:153], v[182:185], v[126:129]
	v_mfma_f32_16x16x32_bf16 v[122:125], v[158:161], v[182:185], v[122:125]
	v_mfma_f32_16x16x32_bf16 v[110:113], v[150:153], v[190:193], v[110:113]
	v_mfma_f32_16x16x32_bf16 v[106:109], v[158:161], v[190:193], v[106:109]
	v_mfma_f32_16x16x32_bf16 v[94:97], v[150:153], v[204:207], v[94:97]
	v_mfma_f32_16x16x32_bf16 v[90:93], v[158:161], v[204:207], v[90:93]
	v_mfma_f32_16x16x32_bf16 v[78:81], v[150:153], v[212:215], v[78:81]
	v_mfma_f32_16x16x32_bf16 v[74:77], v[158:161], v[212:215], v[74:77]
	v_mfma_f32_16x16x32_bf16 v[118:121], v[162:165], v[178:181], v[118:121]
	v_mfma_f32_16x16x32_bf16 v[114:117], v[170:173], v[178:181], v[114:117]
	v_mfma_f32_16x16x32_bf16 v[102:105], v[162:165], v[186:189], v[102:105]
	v_mfma_f32_16x16x32_bf16 v[98:101], v[170:173], v[186:189], v[98:101]
	v_mfma_f32_16x16x32_bf16 v[86:89], v[162:165], v[200:203], v[86:89]
	v_mfma_f32_16x16x32_bf16 v[82:85], v[170:173], v[200:203], v[82:85]
	v_mfma_f32_16x16x32_bf16 v[70:73], v[162:165], v[208:211], v[70:73]
	v_mfma_f32_16x16x32_bf16 v[66:69], v[170:173], v[208:211], v[66:69]
	v_mfma_f32_16x16x32_bf16 v[118:121], v[166:169], v[182:185], v[118:121]
	v_mfma_f32_16x16x32_bf16 v[114:117], v[174:177], v[182:185], v[114:117]
	v_mfma_f32_16x16x32_bf16 v[102:105], v[166:169], v[190:193], v[102:105]
	v_mfma_f32_16x16x32_bf16 v[98:101], v[174:177], v[190:193], v[98:101]
	v_mfma_f32_16x16x32_bf16 v[86:89], v[166:169], v[204:207], v[86:89]
	v_mfma_f32_16x16x32_bf16 v[82:85], v[174:177], v[204:207], v[82:85]
	v_mfma_f32_16x16x32_bf16 v[70:73], v[166:169], v[212:215], v[70:73]
	v_mfma_f32_16x16x32_bf16 v[66:69], v[174:177], v[212:215], v[66:69]
	s_setprio 0
	s_barrier
	s_mov_b32 m0, s62
	s_add_u32 s0, s54, 0x40000
	ds_read_b128 v[178:181], v144 offset:16384
	ds_read_b128 v[182:185], v144 offset:17408
	ds_read_b128 v[186:189], v144 offset:18432
	ds_read_b128 v[190:193], v144 offset:19456
	ds_read_b128 v[200:203], v144 offset:20480
	ds_read_b128 v[204:207], v144 offset:21504
	ds_read_b128 v[208:211], v144 offset:22528
	ds_read_b128 v[212:215], v144 offset:23552
	global_load_lds_dwordx4 v0, s[54:55]
	v_lshl_add_u64 v[216:217], s[54:55], 0, v[130:131]
	s_mov_b32 m0, s63
	s_addc_u32 s1, s55, 0
	global_load_lds_dwordx4 v130, s[54:55]
	s_mov_b32 m0, s64
	s_nop 0
	global_load_lds_dwordx4 v0, s[0:1]
	s_mov_b32 m0, s65
	s_nop 0
	global_load_lds_dwordx4 v130, s[0:1]
	s_mov_b32 m0, s37
	s_nop 0
	global_load_lds_dwordx4 v134, s[56:57]
	s_mov_b32 m0, s66
	s_nop 0
	global_load_lds_dwordx4 v132, s[56:57]
	s_waitcnt vmcnt(8)
	s_waitcnt lgkmcnt(0)
	s_barrier
	s_setprio 1
	v_mfma_f32_16x16x32_bf16 v[62:65], v[146:149], v[178:181], v[62:65]
	v_mfma_f32_16x16x32_bf16 v[58:61], v[154:157], v[178:181], v[58:61]
	v_mfma_f32_16x16x32_bf16 v[46:49], v[146:149], v[186:189], v[46:49]
	v_mfma_f32_16x16x32_bf16 v[42:45], v[154:157], v[186:189], v[42:45]
	v_mfma_f32_16x16x32_bf16 v[30:33], v[146:149], v[200:203], v[30:33]
	v_mfma_f32_16x16x32_bf16 v[26:29], v[154:157], v[200:203], v[26:29]
	v_mfma_f32_16x16x32_bf16 v[14:17], v[146:149], v[208:211], v[14:17]
	v_mfma_f32_16x16x32_bf16 v[10:13], v[154:157], v[208:211], v[10:13]
	v_mfma_f32_16x16x32_bf16 v[62:65], v[150:153], v[182:185], v[62:65]
	v_mfma_f32_16x16x32_bf16 v[58:61], v[158:161], v[182:185], v[58:61]
	v_mfma_f32_16x16x32_bf16 v[46:49], v[150:153], v[190:193], v[46:49]
	v_mfma_f32_16x16x32_bf16 v[42:45], v[158:161], v[190:193], v[42:45]
	v_mfma_f32_16x16x32_bf16 v[30:33], v[150:153], v[204:207], v[30:33]
	v_mfma_f32_16x16x32_bf16 v[26:29], v[158:161], v[204:207], v[26:29]
	v_mfma_f32_16x16x32_bf16 v[14:17], v[150:153], v[212:215], v[14:17]
	v_mfma_f32_16x16x32_bf16 v[10:13], v[158:161], v[212:215], v[10:13]
	v_mfma_f32_16x16x32_bf16 v[54:57], v[162:165], v[178:181], v[54:57]
	v_mfma_f32_16x16x32_bf16 v[50:53], v[170:173], v[178:181], v[50:53]
	v_mfma_f32_16x16x32_bf16 v[38:41], v[162:165], v[186:189], v[38:41]
	v_mfma_f32_16x16x32_bf16 v[34:37], v[170:173], v[186:189], v[34:37]
	v_mfma_f32_16x16x32_bf16 v[22:25], v[162:165], v[200:203], v[22:25]
	v_mfma_f32_16x16x32_bf16 v[18:21], v[170:173], v[200:203], v[18:21]
	v_mfma_f32_16x16x32_bf16 v[6:9], v[162:165], v[208:211], v[6:9]
	v_mfma_f32_16x16x32_bf16 v[2:5], v[170:173], v[208:211], v[2:5]
	v_mfma_f32_16x16x32_bf16 v[54:57], v[166:169], v[182:185], v[54:57]
	v_mfma_f32_16x16x32_bf16 v[50:53], v[174:177], v[182:185], v[50:53]
	v_mfma_f32_16x16x32_bf16 v[38:41], v[166:169], v[190:193], v[38:41]
	v_mfma_f32_16x16x32_bf16 v[34:37], v[174:177], v[190:193], v[34:37]
	v_mfma_f32_16x16x32_bf16 v[22:25], v[166:169], v[204:207], v[22:25]
	v_mfma_f32_16x16x32_bf16 v[18:21], v[174:177], v[204:207], v[18:21]
	v_mfma_f32_16x16x32_bf16 v[6:9], v[166:169], v[212:215], v[6:9]
	v_mfma_f32_16x16x32_bf16 v[2:5], v[174:177], v[212:215], v[2:5]
	s_setprio 0
	s_barrier
	v_or_b32_e32 v146, 0x18000, v145
	v_add_u32_e32 v150, 0x18400, v145
	v_add_u32_e32 v154, 0x18800, v145
	v_add_u32_e32 v158, 0x18c00, v145
	v_or_b32_e32 v162, 0x1c000, v145
	v_add_u32_e32 v166, 0x1c400, v145
	v_add_u32_e32 v170, 0x1c800, v145
	v_add_u32_e32 v174, 0x1cc00, v145
	ds_read_b128 v[146:149], v146
	ds_read_b128 v[150:153], v150
	ds_read_b128 v[154:157], v154
	ds_read_b128 v[158:161], v158
	ds_read_b128 v[162:165], v162
	ds_read_b128 v[166:169], v166
	ds_read_b128 v[170:173], v170
	ds_read_b128 v[174:177], v174
	s_add_u32 s0, s56, 0x40000
	s_addc_u32 s1, s57, 0
	s_mov_b32 m0, s67
	ds_read_b128 v[178:181], v144 offset:32768
	ds_read_b128 v[182:185], v144 offset:33792
	ds_read_b128 v[186:189], v144 offset:34816
	ds_read_b128 v[190:193], v144 offset:35840
	ds_read_b128 v[200:203], v144 offset:36864
	ds_read_b128 v[204:207], v144 offset:37888
	ds_read_b128 v[208:211], v144 offset:38912
	ds_read_b128 v[212:215], v144 offset:39936
	global_load_lds_dwordx4 v134, s[0:1]
	s_mov_b32 m0, s80
	s_nop 0
	global_load_lds_dwordx4 v132, s[0:1]
	s_waitcnt vmcnt(8)
	s_waitcnt lgkmcnt(0)
	s_barrier
	s_setprio 1
	v_mfma_f32_16x16x32_bf16 v[126:129], v[146:149], v[178:181], v[126:129]
	v_mfma_f32_16x16x32_bf16 v[122:125], v[154:157], v[178:181], v[122:125]
	v_mfma_f32_16x16x32_bf16 v[110:113], v[146:149], v[186:189], v[110:113]
	v_mfma_f32_16x16x32_bf16 v[106:109], v[154:157], v[186:189], v[106:109]
	v_mfma_f32_16x16x32_bf16 v[94:97], v[146:149], v[200:203], v[94:97]
	v_mfma_f32_16x16x32_bf16 v[90:93], v[154:157], v[200:203], v[90:93]
	v_mfma_f32_16x16x32_bf16 v[78:81], v[146:149], v[208:211], v[78:81]
	v_mfma_f32_16x16x32_bf16 v[74:77], v[154:157], v[208:211], v[74:77]
	v_mfma_f32_16x16x32_bf16 v[126:129], v[150:153], v[182:185], v[126:129]
	v_mfma_f32_16x16x32_bf16 v[122:125], v[158:161], v[182:185], v[122:125]
	v_mfma_f32_16x16x32_bf16 v[110:113], v[150:153], v[190:193], v[110:113]
	v_mfma_f32_16x16x32_bf16 v[106:109], v[158:161], v[190:193], v[106:109]
	v_mfma_f32_16x16x32_bf16 v[94:97], v[150:153], v[204:207], v[94:97]
	v_mfma_f32_16x16x32_bf16 v[90:93], v[158:161], v[204:207], v[90:93]
	v_mfma_f32_16x16x32_bf16 v[78:81], v[150:153], v[212:215], v[78:81]
	v_mfma_f32_16x16x32_bf16 v[74:77], v[158:161], v[212:215], v[74:77]
	v_mfma_f32_16x16x32_bf16 v[118:121], v[162:165], v[178:181], v[118:121]
	v_mfma_f32_16x16x32_bf16 v[114:117], v[170:173], v[178:181], v[114:117]
	v_mfma_f32_16x16x32_bf16 v[102:105], v[162:165], v[186:189], v[102:105]
	v_mfma_f32_16x16x32_bf16 v[98:101], v[170:173], v[186:189], v[98:101]
	v_mfma_f32_16x16x32_bf16 v[86:89], v[162:165], v[200:203], v[86:89]
	v_mfma_f32_16x16x32_bf16 v[82:85], v[170:173], v[200:203], v[82:85]
	v_mfma_f32_16x16x32_bf16 v[70:73], v[162:165], v[208:211], v[70:73]
	v_mfma_f32_16x16x32_bf16 v[66:69], v[170:173], v[208:211], v[66:69]
	v_mfma_f32_16x16x32_bf16 v[118:121], v[166:169], v[182:185], v[118:121]
	v_mfma_f32_16x16x32_bf16 v[114:117], v[174:177], v[182:185], v[114:117]
	v_mfma_f32_16x16x32_bf16 v[102:105], v[166:169], v[190:193], v[102:105]
	v_mfma_f32_16x16x32_bf16 v[98:101], v[174:177], v[190:193], v[98:101]
	v_mfma_f32_16x16x32_bf16 v[86:89], v[166:169], v[204:207], v[86:89]
	v_mfma_f32_16x16x32_bf16 v[82:85], v[174:177], v[204:207], v[82:85]
	v_mfma_f32_16x16x32_bf16 v[70:73], v[166:169], v[212:215], v[70:73]
	v_mfma_f32_16x16x32_bf16 v[66:69], v[174:177], v[212:215], v[66:69]
	s_setprio 0
	s_barrier
	s_add_i32 m0, s82, 0xffffff80
	s_add_u32 s0, s54, 0x40080
	ds_read_b128 v[178:181], v144 offset:49152
	ds_read_b128 v[182:185], v144 offset:50176
	ds_read_b128 v[186:189], v144 offset:51200
	ds_read_b128 v[190:193], v144 offset:52224
	ds_read_b128 v[200:203], v144 offset:53248
	ds_read_b128 v[204:207], v144 offset:54272
	ds_read_b128 v[208:211], v144 offset:55296
	ds_read_b128 v[212:215], v144 offset:56320
	global_load_lds_dwordx4 v0, s[54:55] offset:128
	v_lshl_add_u64 v[194:195], v[216:217], 0, s[18:19]
	s_mov_b32 m0, s83
	s_addc_u32 s1, s55, 0
	global_load_lds_dwordx4 v[194:195], off
	s_mov_b32 m0, s88
	s_nop 0
	global_load_lds_dwordx4 v0, s[0:1]
	s_mov_b32 m0, s89
	s_nop 0
	global_load_lds_dwordx4 v130, s[0:1]
	s_add_i32 m0, s84, 0xffffff80
	s_nop 0
	global_load_lds_dwordx4 v134, s[56:57] offset:128
	s_add_i32 m0, s85, 0xffffff80
	s_nop 0
	global_load_lds_dwordx4 v132, s[56:57] offset:128
	s_waitcnt vmcnt(8)
	s_waitcnt lgkmcnt(0)
	s_barrier
	s_setprio 1
	v_mfma_f32_16x16x32_bf16 v[62:65], v[146:149], v[178:181], v[62:65]
	v_mfma_f32_16x16x32_bf16 v[58:61], v[154:157], v[178:181], v[58:61]
	v_mfma_f32_16x16x32_bf16 v[46:49], v[146:149], v[186:189], v[46:49]
	v_mfma_f32_16x16x32_bf16 v[42:45], v[154:157], v[186:189], v[42:45]
	v_mfma_f32_16x16x32_bf16 v[30:33], v[146:149], v[200:203], v[30:33]
	v_mfma_f32_16x16x32_bf16 v[26:29], v[154:157], v[200:203], v[26:29]
	v_mfma_f32_16x16x32_bf16 v[14:17], v[146:149], v[208:211], v[14:17]
	v_mfma_f32_16x16x32_bf16 v[10:13], v[154:157], v[208:211], v[10:13]
	v_mfma_f32_16x16x32_bf16 v[62:65], v[150:153], v[182:185], v[62:65]
	v_mfma_f32_16x16x32_bf16 v[58:61], v[158:161], v[182:185], v[58:61]
	v_mfma_f32_16x16x32_bf16 v[46:49], v[150:153], v[190:193], v[46:49]
	v_mfma_f32_16x16x32_bf16 v[42:45], v[158:161], v[190:193], v[42:45]
	v_mfma_f32_16x16x32_bf16 v[30:33], v[150:153], v[204:207], v[30:33]
	v_mfma_f32_16x16x32_bf16 v[26:29], v[158:161], v[204:207], v[26:29]
	v_mfma_f32_16x16x32_bf16 v[14:17], v[150:153], v[212:215], v[14:17]
	v_mfma_f32_16x16x32_bf16 v[10:13], v[158:161], v[212:215], v[10:13]
	v_mfma_f32_16x16x32_bf16 v[54:57], v[162:165], v[178:181], v[54:57]
	v_mfma_f32_16x16x32_bf16 v[50:53], v[170:173], v[178:181], v[50:53]
	v_mfma_f32_16x16x32_bf16 v[38:41], v[162:165], v[186:189], v[38:41]
	v_mfma_f32_16x16x32_bf16 v[34:37], v[170:173], v[186:189], v[34:37]
	v_mfma_f32_16x16x32_bf16 v[22:25], v[162:165], v[200:203], v[22:25]
	v_mfma_f32_16x16x32_bf16 v[18:21], v[170:173], v[200:203], v[18:21]
	v_mfma_f32_16x16x32_bf16 v[6:9], v[162:165], v[208:211], v[6:9]
	v_mfma_f32_16x16x32_bf16 v[2:5], v[170:173], v[208:211], v[2:5]
	v_mfma_f32_16x16x32_bf16 v[54:57], v[166:169], v[182:185], v[54:57]
	v_mfma_f32_16x16x32_bf16 v[50:53], v[174:177], v[182:185], v[50:53]
	v_mfma_f32_16x16x32_bf16 v[38:41], v[166:169], v[190:193], v[38:41]
	v_mfma_f32_16x16x32_bf16 v[34:37], v[174:177], v[190:193], v[34:37]
	v_mfma_f32_16x16x32_bf16 v[22:25], v[166:169], v[204:207], v[22:25]
	v_mfma_f32_16x16x32_bf16 v[18:21], v[174:177], v[204:207], v[18:21]
	v_mfma_f32_16x16x32_bf16 v[6:9], v[166:169], v[212:215], v[6:9]
	v_mfma_f32_16x16x32_bf16 v[2:5], v[174:177], v[212:215], v[2:5]
	s_setprio 0
	s_barrier
	s_add_i32 vcc_lo, vcc_lo, 2
	s_add_u32 s52, s52, 0x100
	s_addc_u32 s53, s53, 0
	s_cmp_gt_u32 vcc_lo, 13
	s_cbranch_scc0 .LBB0_535
	s_and_b64 vcc, exec, s[16:17]
	s_cbranch_vccz .LBB0_538
	s_barrier

.LBB0_851:
	v_or_b32_e32 v0, 0x10000, v237
	v_add_u32_e32 v134, 0x10400, v237
	ds_read_b128 v[130:133], v0
	ds_read_b128 v[134:137], v134
	v_add_u32_e32 v0, 0x10800, v237
	v_add_u32_e32 v142, 0x10c00, v237
	ds_read_b128 v[138:141], v0
	ds_read_b128 v[142:145], v142
	v_or_b32_e32 v0, 0x14000, v237
	v_add_u32_e32 v150, 0x14400, v237
	ds_read_b128 v[146:149], v0
	ds_read_b128 v[150:153], v150
	v_add_u32_e32 v0, 0x14800, v237
	v_add_u32_e32 v158, 0x14c00, v237
	ds_read_b128 v[154:157], v0
	ds_read_b128 v[158:161], v158
	s_add_u32 s43, s54, 0xfffe0080
	s_addc_u32 s45, s55, -1
	s_cmp_eq_u32 s41, 4
	s_cselect_b32 s59, s49, s45
	s_cselect_b32 s58, s48, s43
	s_cselect_b32 s57, s51, s39
	s_cselect_b32 s56, s50, s29
	s_add_i32 m0, s61, 0xc000
	ds_read_b128 v[162:165], v236
	ds_read_b128 v[166:169], v236 offset:1024
	ds_read_b128 v[170:173], v236 offset:2048
	ds_read_b128 v[174:177], v236 offset:3072
	ds_read_b128 v[178:181], v236 offset:4096
	ds_read_b128 v[182:185], v236 offset:5120
	ds_read_b128 v[186:189], v236 offset:6144
	ds_read_b128 v[190:193], v236 offset:7168
	global_load_lds_dwordx4 v206, s[54:55]
	s_add_i32 m0, s61, 0xe000
	s_nop 0
	global_load_lds_dwordx4 v208, s[54:55]
	s_waitcnt vmcnt(8)
	s_waitcnt lgkmcnt(0)
	s_barrier
	s_setprio 1
	v_mfma_f32_16x16x32_bf16 v[126:129], v[130:133], v[162:165], v[126:129]
	v_mfma_f32_16x16x32_bf16 v[122:125], v[138:141], v[162:165], v[122:125]
	v_mfma_f32_16x16x32_bf16 v[118:121], v[130:133], v[170:173], v[118:121]
	v_mfma_f32_16x16x32_bf16 v[114:117], v[138:141], v[170:173], v[114:117]
	v_mfma_f32_16x16x32_bf16 v[110:113], v[130:133], v[178:181], v[110:113]
	v_mfma_f32_16x16x32_bf16 v[106:109], v[138:141], v[178:181], v[106:109]
	v_mfma_f32_16x16x32_bf16 v[102:105], v[130:133], v[186:189], v[102:105]
	v_mfma_f32_16x16x32_bf16 v[98:101], v[138:141], v[186:189], v[98:101]
	v_mfma_f32_16x16x32_bf16 v[126:129], v[134:137], v[166:169], v[126:129]
	v_mfma_f32_16x16x32_bf16 v[122:125], v[142:145], v[166:169], v[122:125]
	v_mfma_f32_16x16x32_bf16 v[118:121], v[134:137], v[174:177], v[118:121]
	v_mfma_f32_16x16x32_bf16 v[114:117], v[142:145], v[174:177], v[114:117]
	v_mfma_f32_16x16x32_bf16 v[110:113], v[134:137], v[182:185], v[110:113]
	v_mfma_f32_16x16x32_bf16 v[106:109], v[142:145], v[182:185], v[106:109]
	v_mfma_f32_16x16x32_bf16 v[102:105], v[134:137], v[190:193], v[102:105]
	v_mfma_f32_16x16x32_bf16 v[98:101], v[142:145], v[190:193], v[98:101]
	v_mfma_f32_16x16x32_bf16 v[94:97], v[146:149], v[162:165], v[94:97]
	v_mfma_f32_16x16x32_bf16 v[90:93], v[154:157], v[162:165], v[90:93]
	v_mfma_f32_16x16x32_bf16 v[86:89], v[146:149], v[170:173], v[86:89]
	v_mfma_f32_16x16x32_bf16 v[82:85], v[154:157], v[170:173], v[82:85]
	v_mfma_f32_16x16x32_bf16 v[78:81], v[146:149], v[178:181], v[78:81]
	v_mfma_f32_16x16x32_bf16 v[74:77], v[154:157], v[178:181], v[74:77]
	v_mfma_f32_16x16x32_bf16 v[70:73], v[146:149], v[186:189], v[70:73]
	v_mfma_f32_16x16x32_bf16 v[66:69], v[154:157], v[186:189], v[66:69]
	v_mfma_f32_16x16x32_bf16 v[94:97], v[150:153], v[166:169], v[94:97]
	v_mfma_f32_16x16x32_bf16 v[90:93], v[158:161], v[166:169], v[90:93]
	v_mfma_f32_16x16x32_bf16 v[86:89], v[150:153], v[174:177], v[86:89]
	v_mfma_f32_16x16x32_bf16 v[82:85], v[158:161], v[174:177], v[82:85]
	v_mfma_f32_16x16x32_bf16 v[78:81], v[150:153], v[182:185], v[78:81]
	v_mfma_f32_16x16x32_bf16 v[74:77], v[158:161], v[182:185], v[74:77]
	v_mfma_f32_16x16x32_bf16 v[70:73], v[150:153], v[190:193], v[70:73]
	v_mfma_f32_16x16x32_bf16 v[66:69], v[158:161], v[190:193], v[66:69]
	s_setprio 0
	s_barrier
	s_mov_b32 m0, s62
	v_lshl_add_u64 v[210:211], s[56:57], 0, v[200:201]
	s_add_u32 vcc_lo, s56, 0x20000
	ds_read_b128 v[162:165], v236 offset:16384
	ds_read_b128 v[166:169], v236 offset:17408
	ds_read_b128 v[170:173], v236 offset:18432
	ds_read_b128 v[174:177], v236 offset:19456
	ds_read_b128 v[178:181], v236 offset:20480
	ds_read_b128 v[182:185], v236 offset:21504
	ds_read_b128 v[186:189], v236 offset:22528
	ds_read_b128 v[190:193], v236 offset:23552
	global_load_lds_dwordx4 v200, s[56:57]
	v_lshl_add_u64 v[212:213], s[56:57], 0, v[204:205]
	s_mov_b32 m0, s63
	s_addc_u32 vcc_hi, s57, 0
	global_load_lds_dwordx4 v204, s[56:57]
	v_lshl_add_u64 v[214:215], vcc, 0, v[200:201]
	s_mov_b32 m0, s64
	v_lshl_add_u64 v[216:217], s[58:59], 0, v[202:203]
	global_load_lds_dwordx4 v200, vcc
	v_lshl_add_u64 v[214:215], vcc, 0, v[204:205]
	s_mov_b32 m0, s65
	s_nop 0
	global_load_lds_dwordx4 v204, vcc
	v_lshl_add_u64 v[214:215], s[58:59], 0, v[194:195]
	s_mov_b32 m0, s61
	s_nop 0
	global_load_lds_dwordx4 v194, s[58:59]
	s_mov_b32 m0, s66
	s_nop 0
	global_load_lds_dwordx4 v202, s[58:59]
	s_waitcnt vmcnt(8)
	s_waitcnt lgkmcnt(0)
	s_barrier
	s_setprio 1
	v_mfma_f32_16x16x32_bf16 v[62:65], v[130:133], v[162:165], v[62:65]
	v_mfma_f32_16x16x32_bf16 v[58:61], v[138:141], v[162:165], v[58:61]
	v_mfma_f32_16x16x32_bf16 v[54:57], v[130:133], v[170:173], v[54:57]
	v_mfma_f32_16x16x32_bf16 v[50:53], v[138:141], v[170:173], v[50:53]
	v_mfma_f32_16x16x32_bf16 v[46:49], v[130:133], v[178:181], v[46:49]
	v_mfma_f32_16x16x32_bf16 v[42:45], v[138:141], v[178:181], v[42:45]
	v_mfma_f32_16x16x32_bf16 v[38:41], v[130:133], v[186:189], v[38:41]
	v_mfma_f32_16x16x32_bf16 v[34:37], v[138:141], v[186:189], v[34:37]
	v_mfma_f32_16x16x32_bf16 v[62:65], v[134:137], v[166:169], v[62:65]
	v_mfma_f32_16x16x32_bf16 v[58:61], v[142:145], v[166:169], v[58:61]
	v_mfma_f32_16x16x32_bf16 v[54:57], v[134:137], v[174:177], v[54:57]
	v_mfma_f32_16x16x32_bf16 v[50:53], v[142:145], v[174:177], v[50:53]
	v_mfma_f32_16x16x32_bf16 v[46:49], v[134:137], v[182:185], v[46:49]
	v_mfma_f32_16x16x32_bf16 v[42:45], v[142:145], v[182:185], v[42:45]
	v_mfma_f32_16x16x32_bf16 v[38:41], v[134:137], v[190:193], v[38:41]
	v_mfma_f32_16x16x32_bf16 v[34:37], v[142:145], v[190:193], v[34:37]
	v_mfma_f32_16x16x32_bf16 v[30:33], v[146:149], v[162:165], v[30:33]
	v_mfma_f32_16x16x32_bf16 v[26:29], v[154:157], v[162:165], v[26:29]
	v_mfma_f32_16x16x32_bf16 v[22:25], v[146:149], v[170:173], v[22:25]
	v_mfma_f32_16x16x32_bf16 v[18:21], v[154:157], v[170:173], v[18:21]
	v_mfma_f32_16x16x32_bf16 v[14:17], v[146:149], v[178:181], v[14:17]
	v_mfma_f32_16x16x32_bf16 v[10:13], v[154:157], v[178:181], v[10:13]
	v_mfma_f32_16x16x32_bf16 v[6:9], v[146:149], v[186:189], v[6:9]
	v_mfma_f32_16x16x32_bf16 v[2:5], v[154:157], v[186:189], v[2:5]
	v_mfma_f32_16x16x32_bf16 v[30:33], v[150:153], v[166:169], v[30:33]
	v_mfma_f32_16x16x32_bf16 v[26:29], v[158:161], v[166:169], v[26:29]
	v_mfma_f32_16x16x32_bf16 v[22:25], v[150:153], v[174:177], v[22:25]
	v_mfma_f32_16x16x32_bf16 v[18:21], v[158:161], v[174:177], v[18:21]
	v_mfma_f32_16x16x32_bf16 v[14:17], v[150:153], v[182:185], v[14:17]
	v_mfma_f32_16x16x32_bf16 v[10:13], v[158:161], v[182:185], v[10:13]
	v_mfma_f32_16x16x32_bf16 v[6:9], v[150:153], v[190:193], v[6:9]
	v_mfma_f32_16x16x32_bf16 v[2:5], v[158:161], v[190:193], v[2:5]
	s_setprio 0
	s_barrier
	v_or_b32_e32 v0, 0x18000, v237
	v_add_u32_e32 v134, 0x18400, v237
	ds_read_b128 v[130:133], v0
	ds_read_b128 v[134:137], v134
	v_add_u32_e32 v0, 0x18800, v237
	v_add_u32_e32 v142, 0x18c00, v237
	ds_read_b128 v[138:141], v0
	ds_read_b128 v[142:145], v142
	v_or_b32_e32 v0, 0x1c000, v237
	v_add_u32_e32 v150, 0x1c400, v237
	ds_read_b128 v[146:149], v0
	ds_read_b128 v[150:153], v150
	v_add_u32_e32 v0, 0x1c800, v237
	v_add_u32_e32 v158, 0x1cc00, v237
	ds_read_b128 v[154:157], v0
	ds_read_b128 v[158:161], v158
	s_add_u32 s58, s58, 0x20000
	s_addc_u32 s59, s59, 0
	s_mov_b32 m0, s67
	v_lshl_add_u64 v[218:219], s[58:59], 0, v[194:195]
	ds_read_b128 v[162:165], v236 offset:32768
	ds_read_b128 v[166:169], v236 offset:33792
	ds_read_b128 v[170:173], v236 offset:34816
	ds_read_b128 v[174:177], v236 offset:35840
	ds_read_b128 v[178:181], v236 offset:36864
	ds_read_b128 v[182:185], v236 offset:37888
	ds_read_b128 v[186:189], v236 offset:38912
	ds_read_b128 v[190:193], v236 offset:39936
	global_load_lds_dwordx4 v194, s[58:59]
	v_lshl_add_u64 v[218:219], s[58:59], 0, v[202:203]
	s_mov_b32 m0, s82
	s_nop 0
	global_load_lds_dwordx4 v202, s[58:59]
	s_waitcnt vmcnt(8)
	s_waitcnt lgkmcnt(0)
	s_barrier
	s_setprio 1
	v_mfma_f32_16x16x32_bf16 v[126:129], v[130:133], v[162:165], v[126:129]
	v_mfma_f32_16x16x32_bf16 v[122:125], v[138:141], v[162:165], v[122:125]
	v_mfma_f32_16x16x32_bf16 v[118:121], v[130:133], v[170:173], v[118:121]
	v_mfma_f32_16x16x32_bf16 v[114:117], v[138:141], v[170:173], v[114:117]
	v_mfma_f32_16x16x32_bf16 v[110:113], v[130:133], v[178:181], v[110:113]
	v_mfma_f32_16x16x32_bf16 v[106:109], v[138:141], v[178:181], v[106:109]
	v_mfma_f32_16x16x32_bf16 v[102:105], v[130:133], v[186:189], v[102:105]
	v_mfma_f32_16x16x32_bf16 v[98:101], v[138:141], v[186:189], v[98:101]
	v_mfma_f32_16x16x32_bf16 v[126:129], v[134:137], v[166:169], v[126:129]
	v_mfma_f32_16x16x32_bf16 v[122:125], v[142:145], v[166:169], v[122:125]
	v_mfma_f32_16x16x32_bf16 v[118:121], v[134:137], v[174:177], v[118:121]
	v_mfma_f32_16x16x32_bf16 v[114:117], v[142:145], v[174:177], v[114:117]
	v_mfma_f32_16x16x32_bf16 v[110:113], v[134:137], v[182:185], v[110:113]
	v_mfma_f32_16x16x32_bf16 v[106:109], v[142:145], v[182:185], v[106:109]
	v_mfma_f32_16x16x32_bf16 v[102:105], v[134:137], v[190:193], v[102:105]
	v_mfma_f32_16x16x32_bf16 v[98:101], v[142:145], v[190:193], v[98:101]
	v_mfma_f32_16x16x32_bf16 v[94:97], v[146:149], v[162:165], v[94:97]
	v_mfma_f32_16x16x32_bf16 v[90:93], v[154:157], v[162:165], v[90:93]
	v_mfma_f32_16x16x32_bf16 v[86:89], v[146:149], v[170:173], v[86:89]
	v_mfma_f32_16x16x32_bf16 v[82:85], v[154:157], v[170:173], v[82:85]
	v_mfma_f32_16x16x32_bf16 v[78:81], v[146:149], v[178:181], v[78:81]
	v_mfma_f32_16x16x32_bf16 v[74:77], v[154:157], v[178:181], v[74:77]
	v_mfma_f32_16x16x32_bf16 v[70:73], v[146:149], v[186:189], v[70:73]
	v_mfma_f32_16x16x32_bf16 v[66:69], v[154:157], v[186:189], v[66:69]
	v_mfma_f32_16x16x32_bf16 v[94:97], v[150:153], v[166:169], v[94:97]
	v_mfma_f32_16x16x32_bf16 v[90:93], v[158:161], v[166:169], v[90:93]
	v_mfma_f32_16x16x32_bf16 v[86:89], v[150:153], v[174:177], v[86:89]
	v_mfma_f32_16x16x32_bf16 v[82:85], v[158:161], v[174:177], v[82:85]
	v_mfma_f32_16x16x32_bf16 v[78:81], v[150:153], v[182:185], v[78:81]
	v_mfma_f32_16x16x32_bf16 v[74:77], v[158:161], v[182:185], v[74:77]
	v_mfma_f32_16x16x32_bf16 v[70:73], v[150:153], v[190:193], v[70:73]
	v_mfma_f32_16x16x32_bf16 v[66:69], v[158:161], v[190:193], v[66:69]
	s_setprio 0
	s_barrier
	s_mov_b32 m0, s88
	v_lshl_add_u64 v[210:211], v[210:211], 0, s[18:19]
	s_add_u32 s56, s56, 0x20080
	ds_read_b128 v[162:165], v236 offset:49152
	ds_read_b128 v[166:169], v236 offset:50176
	ds_read_b128 v[170:173], v236 offset:51200
	ds_read_b128 v[174:177], v236 offset:52224
	ds_read_b128 v[178:181], v236 offset:53248
	ds_read_b128 v[182:185], v236 offset:54272
	ds_read_b128 v[186:189], v236 offset:55296
	ds_read_b128 v[190:193], v236 offset:56320
	global_load_lds_dwordx4 v[210:211], off
	v_lshl_add_u64 v[210:211], v[212:213], 0, s[18:19]
	s_mov_b32 m0, s89
	s_addc_u32 s57, s57, 0
	global_load_lds_dwordx4 v[210:211], off
	s_mov_b32 m0, s92
	s_nop 0
	global_load_lds_dwordx4 v200, s[56:57]
	s_mov_b32 m0, s93
	s_nop 0
	global_load_lds_dwordx4 v204, s[56:57]
	v_lshl_add_u64 v[210:211], v[214:215], 0, s[18:19]
	s_mov_b32 m0, s90
	s_nop 0
	global_load_lds_dwordx4 v[210:211], off
	v_lshl_add_u64 v[210:211], v[216:217], 0, s[18:19]
	s_mov_b32 m0, s91
	s_nop 0
	global_load_lds_dwordx4 v[210:211], off
	s_waitcnt vmcnt(8)
	s_waitcnt lgkmcnt(0)
	s_barrier
	s_setprio 1
	v_mfma_f32_16x16x32_bf16 v[62:65], v[130:133], v[162:165], v[62:65]
	v_mfma_f32_16x16x32_bf16 v[58:61], v[138:141], v[162:165], v[58:61]
	v_mfma_f32_16x16x32_bf16 v[54:57], v[130:133], v[170:173], v[54:57]
	v_mfma_f32_16x16x32_bf16 v[50:53], v[138:141], v[170:173], v[50:53]
	v_mfma_f32_16x16x32_bf16 v[46:49], v[130:133], v[178:181], v[46:49]
	v_mfma_f32_16x16x32_bf16 v[42:45], v[138:141], v[178:181], v[42:45]
	v_mfma_f32_16x16x32_bf16 v[38:41], v[130:133], v[186:189], v[38:41]
	v_mfma_f32_16x16x32_bf16 v[34:37], v[138:141], v[186:189], v[34:37]
	v_mfma_f32_16x16x32_bf16 v[62:65], v[134:137], v[166:169], v[62:65]
	v_mfma_f32_16x16x32_bf16 v[58:61], v[142:145], v[166:169], v[58:61]
	v_mfma_f32_16x16x32_bf16 v[54:57], v[134:137], v[174:177], v[54:57]
	v_mfma_f32_16x16x32_bf16 v[50:53], v[142:145], v[174:177], v[50:53]
	v_mfma_f32_16x16x32_bf16 v[46:49], v[134:137], v[182:185], v[46:49]
	v_mfma_f32_16x16x32_bf16 v[42:45], v[142:145], v[182:185], v[42:45]
	v_mfma_f32_16x16x32_bf16 v[38:41], v[134:137], v[190:193], v[38:41]
	v_mfma_f32_16x16x32_bf16 v[34:37], v[142:145], v[190:193], v[34:37]
	v_mfma_f32_16x16x32_bf16 v[30:33], v[146:149], v[162:165], v[30:33]
	v_mfma_f32_16x16x32_bf16 v[26:29], v[154:157], v[162:165], v[26:29]
	v_mfma_f32_16x16x32_bf16 v[22:25], v[146:149], v[170:173], v[22:25]
	v_mfma_f32_16x16x32_bf16 v[18:21], v[154:157], v[170:173], v[18:21]
	v_mfma_f32_16x16x32_bf16 v[14:17], v[146:149], v[178:181], v[14:17]
	v_mfma_f32_16x16x32_bf16 v[10:13], v[154:157], v[178:181], v[10:13]
	v_mfma_f32_16x16x32_bf16 v[6:9], v[146:149], v[186:189], v[6:9]
	v_mfma_f32_16x16x32_bf16 v[2:5], v[154:157], v[186:189], v[2:5]
	v_mfma_f32_16x16x32_bf16 v[30:33], v[150:153], v[166:169], v[30:33]
	v_mfma_f32_16x16x32_bf16 v[26:29], v[158:161], v[166:169], v[26:29]
	v_mfma_f32_16x16x32_bf16 v[22:25], v[150:153], v[174:177], v[22:25]
	v_mfma_f32_16x16x32_bf16 v[18:21], v[158:161], v[174:177], v[18:21]
	v_mfma_f32_16x16x32_bf16 v[14:17], v[150:153], v[182:185], v[14:17]
	v_mfma_f32_16x16x32_bf16 v[10:13], v[158:161], v[182:185], v[10:13]
	v_mfma_f32_16x16x32_bf16 v[6:9], v[150:153], v[190:193], v[6:9]
	v_mfma_f32_16x16x32_bf16 v[2:5], v[158:161], v[190:193], v[2:5]
	s_setprio 0
	s_barrier
	s_add_i32 s41, s41, 2
	s_add_u32 s54, s54, 0x100
	s_addc_u32 s55, s55, 0
	s_add_u32 s29, s29, 0x100
	s_addc_u32 s39, s39, 0
	s_cmp_gt_u32 s41, 5
	s_cbranch_scc0 .LBB0_851
	s_and_b64 vcc, exec, s[16:17]
	s_cbranch_vccz .LBB0_854
	s_barrier

.LBB0_1058:
	v_or_b32_e32 v0, 0x10000, v162
	v_add_u32_e32 v158, 0x10400, v162
	ds_read_b128 v[164:167], v0
	ds_read_b128 v[168:171], v158
	v_add_u32_e32 v0, 0x10800, v162
	v_add_u32_e32 v158, 0x10c00, v162
	ds_read_b128 v[172:175], v0
	ds_read_b128 v[176:179], v158
	v_or_b32_e32 v0, 0x14000, v162
	v_add_u32_e32 v158, 0x14400, v162
	ds_read_b128 v[180:183], v0
	ds_read_b128 v[184:187], v158
	v_add_u32_e32 v0, 0x14800, v162
	v_add_u32_e32 v158, 0x14c00, v162
	ds_read_b128 v[188:191], v0
	ds_read_b128 v[192:195], v158
	s_add_u32 s48, s36, 0xfffc0080
	s_addc_u32 s49, s37, -1
	s_cmp_eq_u32 s90, 12
	s_cselect_b32 s51, s29, s49
	s_cselect_b32 s50, s39, s48
	s_cselect_b32 s49, s41, s89
	s_cselect_b32 s48, s85, s88
	v_lshl_add_u64 v[158:159], s[36:37], 0, v[138:139]
	s_add_i32 m0, s35, 0xc000
	ds_read_b128 v[200:203], v161
	ds_read_b128 v[204:207], v161 offset:1024
	ds_read_b128 v[208:211], v161 offset:2048
	ds_read_b128 v[212:215], v161 offset:3072
	ds_read_b128 v[216:219], v161 offset:4096
	ds_read_b128 v[220:223], v161 offset:5120
	ds_read_b128 v[236:239], v161 offset:6144
	ds_read_b128 v[240:243], v161 offset:7168
	global_load_lds_dwordx4 v138, s[36:37]
	v_lshl_add_u64 v[158:159], s[36:37], 0, v[140:141]
	s_add_i32 m0, s35, 0xe000
	s_nop 0
	global_load_lds_dwordx4 v140, s[36:37]
	s_waitcnt vmcnt(8)
	s_waitcnt lgkmcnt(0)
	s_barrier
	s_setprio 1
	v_mfma_f32_16x16x32_bf16 v[126:129], v[164:167], v[200:203], v[126:129]
	v_mfma_f32_16x16x32_bf16 v[122:125], v[172:175], v[200:203], v[122:125]
	v_mfma_f32_16x16x32_bf16 v[110:113], v[164:167], v[208:211], v[110:113]
	v_mfma_f32_16x16x32_bf16 v[106:109], v[172:175], v[208:211], v[106:109]
	v_mfma_f32_16x16x32_bf16 v[94:97], v[164:167], v[216:219], v[94:97]
	v_mfma_f32_16x16x32_bf16 v[90:93], v[172:175], v[216:219], v[90:93]
	v_mfma_f32_16x16x32_bf16 v[78:81], v[164:167], v[236:239], v[78:81]
	v_mfma_f32_16x16x32_bf16 v[74:77], v[172:175], v[236:239], v[74:77]
	v_mfma_f32_16x16x32_bf16 v[126:129], v[168:171], v[204:207], v[126:129]
	v_mfma_f32_16x16x32_bf16 v[122:125], v[176:179], v[204:207], v[122:125]
	v_mfma_f32_16x16x32_bf16 v[110:113], v[168:171], v[212:215], v[110:113]
	v_mfma_f32_16x16x32_bf16 v[106:109], v[176:179], v[212:215], v[106:109]
	v_mfma_f32_16x16x32_bf16 v[94:97], v[168:171], v[220:223], v[94:97]
	v_mfma_f32_16x16x32_bf16 v[90:93], v[176:179], v[220:223], v[90:93]
	v_mfma_f32_16x16x32_bf16 v[78:81], v[168:171], v[240:243], v[78:81]
	v_mfma_f32_16x16x32_bf16 v[74:77], v[176:179], v[240:243], v[74:77]
	v_mfma_f32_16x16x32_bf16 v[118:121], v[180:183], v[200:203], v[118:121]
	v_mfma_f32_16x16x32_bf16 v[114:117], v[188:191], v[200:203], v[114:117]
	v_mfma_f32_16x16x32_bf16 v[102:105], v[180:183], v[208:211], v[102:105]
	v_mfma_f32_16x16x32_bf16 v[98:101], v[188:191], v[208:211], v[98:101]
	v_mfma_f32_16x16x32_bf16 v[86:89], v[180:183], v[216:219], v[86:89]
	v_mfma_f32_16x16x32_bf16 v[82:85], v[188:191], v[216:219], v[82:85]
	v_mfma_f32_16x16x32_bf16 v[70:73], v[180:183], v[236:239], v[70:73]
	v_mfma_f32_16x16x32_bf16 v[66:69], v[188:191], v[236:239], v[66:69]
	v_mfma_f32_16x16x32_bf16 v[118:121], v[184:187], v[204:207], v[118:121]
	v_mfma_f32_16x16x32_bf16 v[114:117], v[192:195], v[204:207], v[114:117]
	v_mfma_f32_16x16x32_bf16 v[102:105], v[184:187], v[212:215], v[102:105]
	v_mfma_f32_16x16x32_bf16 v[98:101], v[192:195], v[212:215], v[98:101]
	v_mfma_f32_16x16x32_bf16 v[86:89], v[184:187], v[220:223], v[86:89]
	v_mfma_f32_16x16x32_bf16 v[82:85], v[192:195], v[220:223], v[82:85]
	v_mfma_f32_16x16x32_bf16 v[70:73], v[184:187], v[240:243], v[70:73]
	v_mfma_f32_16x16x32_bf16 v[66:69], v[192:195], v[240:243], v[66:69]
	s_setprio 0
	s_barrier
	s_mov_b32 m0, s53
	v_lshl_add_u64 v[158:159], s[48:49], 0, v[134:135]
	s_add_u32 s92, s48, 0x40000
	ds_read_b128 v[200:203], v161 offset:16384
	ds_read_b128 v[204:207], v161 offset:17408
	ds_read_b128 v[208:211], v161 offset:18432
	ds_read_b128 v[212:215], v161 offset:19456
	ds_read_b128 v[216:219], v161 offset:20480
	ds_read_b128 v[220:223], v161 offset:21504
	ds_read_b128 v[236:239], v161 offset:22528
	ds_read_b128 v[240:243], v161 offset:23552
	global_load_lds_dwordx4 v134, s[48:49]
	v_lshl_add_u64 v[226:227], s[48:49], 0, v[130:131]
	s_mov_b32 m0, s54
	s_addc_u32 s93, s49, 0
	global_load_lds_dwordx4 v130, s[48:49]
	s_mov_b32 m0, s55
	v_lshl_add_u64 v[246:247], s[50:51], 0, v[132:133]
	global_load_lds_dwordx4 v134, s[92:93]
	s_mov_b32 m0, s56
	s_nop 0
	global_load_lds_dwordx4 v130, s[92:93]
	v_lshl_add_u64 v[244:245], s[50:51], 0, v[136:137]
	s_mov_b32 m0, s35
	s_nop 0
	global_load_lds_dwordx4 v136, s[50:51]
	s_mov_b32 m0, s57
	s_nop 0
	global_load_lds_dwordx4 v132, s[50:51]
	s_waitcnt vmcnt(8)
	s_waitcnt lgkmcnt(0)
	s_barrier
	s_setprio 1
	v_mfma_f32_16x16x32_bf16 v[62:65], v[164:167], v[200:203], v[62:65]
	v_mfma_f32_16x16x32_bf16 v[58:61], v[172:175], v[200:203], v[58:61]
	v_mfma_f32_16x16x32_bf16 v[46:49], v[164:167], v[208:211], v[46:49]
	v_mfma_f32_16x16x32_bf16 v[42:45], v[172:175], v[208:211], v[42:45]
	v_mfma_f32_16x16x32_bf16 v[30:33], v[164:167], v[216:219], v[30:33]
	v_mfma_f32_16x16x32_bf16 v[26:29], v[172:175], v[216:219], v[26:29]
	v_mfma_f32_16x16x32_bf16 v[14:17], v[164:167], v[236:239], v[14:17]
	v_mfma_f32_16x16x32_bf16 v[10:13], v[172:175], v[236:239], v[10:13]
	v_mfma_f32_16x16x32_bf16 v[62:65], v[168:171], v[204:207], v[62:65]
	v_mfma_f32_16x16x32_bf16 v[58:61], v[176:179], v[204:207], v[58:61]
	v_mfma_f32_16x16x32_bf16 v[46:49], v[168:171], v[212:215], v[46:49]
	v_mfma_f32_16x16x32_bf16 v[42:45], v[176:179], v[212:215], v[42:45]
	v_mfma_f32_16x16x32_bf16 v[30:33], v[168:171], v[220:223], v[30:33]
	v_mfma_f32_16x16x32_bf16 v[26:29], v[176:179], v[220:223], v[26:29]
	v_mfma_f32_16x16x32_bf16 v[14:17], v[168:171], v[240:243], v[14:17]
	v_mfma_f32_16x16x32_bf16 v[10:13], v[176:179], v[240:243], v[10:13]
	v_mfma_f32_16x16x32_bf16 v[54:57], v[180:183], v[200:203], v[54:57]
	v_mfma_f32_16x16x32_bf16 v[50:53], v[188:191], v[200:203], v[50:53]
	v_mfma_f32_16x16x32_bf16 v[38:41], v[180:183], v[208:211], v[38:41]
	v_mfma_f32_16x16x32_bf16 v[34:37], v[188:191], v[208:211], v[34:37]
	v_mfma_f32_16x16x32_bf16 v[22:25], v[180:183], v[216:219], v[22:25]
	v_mfma_f32_16x16x32_bf16 v[18:21], v[188:191], v[216:219], v[18:21]
	v_mfma_f32_16x16x32_bf16 v[6:9], v[180:183], v[236:239], v[6:9]
	v_mfma_f32_16x16x32_bf16 v[2:5], v[188:191], v[236:239], v[2:5]
	v_mfma_f32_16x16x32_bf16 v[54:57], v[184:187], v[204:207], v[54:57]
	v_mfma_f32_16x16x32_bf16 v[50:53], v[192:195], v[204:207], v[50:53]
	v_mfma_f32_16x16x32_bf16 v[38:41], v[184:187], v[212:215], v[38:41]
	v_mfma_f32_16x16x32_bf16 v[34:37], v[192:195], v[212:215], v[34:37]
	v_mfma_f32_16x16x32_bf16 v[22:25], v[184:187], v[220:223], v[22:25]
	v_mfma_f32_16x16x32_bf16 v[18:21], v[192:195], v[220:223], v[18:21]
	v_mfma_f32_16x16x32_bf16 v[6:9], v[184:187], v[240:243], v[6:9]
	v_mfma_f32_16x16x32_bf16 v[2:5], v[192:195], v[240:243], v[2:5]
	s_setprio 0
	s_barrier
	v_or_b32_e32 v0, 0x18000, v162
	v_add_u32_e32 v163, 0x18400, v162
	ds_read_b128 v[164:167], v0
	ds_read_b128 v[168:171], v163
	v_add_u32_e32 v0, 0x18800, v162
	v_add_u32_e32 v163, 0x18c00, v162
	ds_read_b128 v[172:175], v0
	ds_read_b128 v[176:179], v163
	v_or_b32_e32 v0, 0x1c000, v162
	v_add_u32_e32 v163, 0x1c400, v162
	ds_read_b128 v[180:183], v0
	ds_read_b128 v[184:187], v163
	v_add_u32_e32 v0, 0x1c800, v162
	v_add_u32_e32 v163, 0x1cc00, v162
	ds_read_b128 v[188:191], v0
	ds_read_b128 v[192:195], v163
	s_add_u32 s50, s50, 0x40000
	s_addc_u32 s51, s51, 0
	s_mov_b32 m0, s58
	ds_read_b128 v[200:203], v161 offset:32768
	ds_read_b128 v[204:207], v161 offset:33792
	ds_read_b128 v[208:211], v161 offset:34816
	ds_read_b128 v[212:215], v161 offset:35840
	ds_read_b128 v[216:219], v161 offset:36864
	ds_read_b128 v[220:223], v161 offset:37888
	ds_read_b128 v[236:239], v161 offset:38912
	ds_read_b128 v[240:243], v161 offset:39936
	global_load_lds_dwordx4 v136, s[50:51]
	s_mov_b32 m0, s59
	s_nop 0
	global_load_lds_dwordx4 v132, s[50:51]
	s_waitcnt vmcnt(8)
	s_waitcnt lgkmcnt(0)
	s_barrier
	s_setprio 1
	v_mfma_f32_16x16x32_bf16 v[126:129], v[164:167], v[200:203], v[126:129]
	v_mfma_f32_16x16x32_bf16 v[122:125], v[172:175], v[200:203], v[122:125]
	v_mfma_f32_16x16x32_bf16 v[110:113], v[164:167], v[208:211], v[110:113]
	v_mfma_f32_16x16x32_bf16 v[106:109], v[172:175], v[208:211], v[106:109]
	v_mfma_f32_16x16x32_bf16 v[94:97], v[164:167], v[216:219], v[94:97]
	v_mfma_f32_16x16x32_bf16 v[90:93], v[172:175], v[216:219], v[90:93]
	v_mfma_f32_16x16x32_bf16 v[78:81], v[164:167], v[236:239], v[78:81]
	v_mfma_f32_16x16x32_bf16 v[74:77], v[172:175], v[236:239], v[74:77]
	v_mfma_f32_16x16x32_bf16 v[126:129], v[168:171], v[204:207], v[126:129]
	v_mfma_f32_16x16x32_bf16 v[122:125], v[176:179], v[204:207], v[122:125]
	v_mfma_f32_16x16x32_bf16 v[110:113], v[168:171], v[212:215], v[110:113]
	v_mfma_f32_16x16x32_bf16 v[106:109], v[176:179], v[212:215], v[106:109]
	v_mfma_f32_16x16x32_bf16 v[94:97], v[168:171], v[220:223], v[94:97]
	v_mfma_f32_16x16x32_bf16 v[90:93], v[176:179], v[220:223], v[90:93]
	v_mfma_f32_16x16x32_bf16 v[78:81], v[168:171], v[240:243], v[78:81]
	v_mfma_f32_16x16x32_bf16 v[74:77], v[176:179], v[240:243], v[74:77]
	v_mfma_f32_16x16x32_bf16 v[118:121], v[180:183], v[200:203], v[118:121]
	v_mfma_f32_16x16x32_bf16 v[114:117], v[188:191], v[200:203], v[114:117]
	v_mfma_f32_16x16x32_bf16 v[102:105], v[180:183], v[208:211], v[102:105]
	v_mfma_f32_16x16x32_bf16 v[98:101], v[188:191], v[208:211], v[98:101]
	v_mfma_f32_16x16x32_bf16 v[86:89], v[180:183], v[216:219], v[86:89]
	v_mfma_f32_16x16x32_bf16 v[82:85], v[188:191], v[216:219], v[82:85]
	v_mfma_f32_16x16x32_bf16 v[70:73], v[180:183], v[236:239], v[70:73]
	v_mfma_f32_16x16x32_bf16 v[66:69], v[188:191], v[236:239], v[66:69]
	v_mfma_f32_16x16x32_bf16 v[118:121], v[184:187], v[204:207], v[118:121]
	v_mfma_f32_16x16x32_bf16 v[114:117], v[192:195], v[204:207], v[114:117]
	v_mfma_f32_16x16x32_bf16 v[102:105], v[184:187], v[212:215], v[102:105]
	v_mfma_f32_16x16x32_bf16 v[98:101], v[192:195], v[212:215], v[98:101]
	v_mfma_f32_16x16x32_bf16 v[86:89], v[184:187], v[220:223], v[86:89]
	v_mfma_f32_16x16x32_bf16 v[82:85], v[192:195], v[220:223], v[82:85]
	v_mfma_f32_16x16x32_bf16 v[70:73], v[184:187], v[240:243], v[70:73]
	v_mfma_f32_16x16x32_bf16 v[66:69], v[192:195], v[240:243], v[66:69]
	s_setprio 0
	s_barrier
	s_mov_b32 m0, s62
	v_lshl_add_u64 v[158:159], v[158:159], 0, s[18:19]
	s_add_u32 s48, s48, 0x40080
	ds_read_b128 v[200:203], v161 offset:49152
	ds_read_b128 v[204:207], v161 offset:50176
	ds_read_b128 v[208:211], v161 offset:51200
	ds_read_b128 v[212:215], v161 offset:52224
	ds_read_b128 v[216:219], v161 offset:53248
	ds_read_b128 v[220:223], v161 offset:54272
	ds_read_b128 v[236:239], v161 offset:55296
	ds_read_b128 v[240:243], v161 offset:56320
	global_load_lds_dwordx4 v[158:159], off
	v_lshl_add_u64 v[158:159], v[226:227], 0, s[18:19]
	s_mov_b32 m0, s63
	s_addc_u32 s49, s49, 0
	global_load_lds_dwordx4 v[158:159], off
	v_lshl_add_u64 v[158:159], s[48:49], 0, v[134:135]
	s_mov_b32 m0, s66
	s_nop 0
	global_load_lds_dwordx4 v134, s[48:49]
	v_lshl_add_u64 v[158:159], s[48:49], 0, v[130:131]
	s_mov_b32 m0, s67
	s_nop 0
	global_load_lds_dwordx4 v130, s[48:49]
	v_lshl_add_u64 v[158:159], v[244:245], 0, s[18:19]
	s_mov_b32 m0, s64
	s_nop 0
	global_load_lds_dwordx4 v[158:159], off
	v_lshl_add_u64 v[158:159], v[246:247], 0, s[18:19]
	s_mov_b32 m0, s65
	s_nop 0
	global_load_lds_dwordx4 v[158:159], off
	s_waitcnt vmcnt(8)
	s_waitcnt lgkmcnt(0)
	s_barrier
	s_setprio 1
	v_mfma_f32_16x16x32_bf16 v[62:65], v[164:167], v[200:203], v[62:65]
	v_mfma_f32_16x16x32_bf16 v[58:61], v[172:175], v[200:203], v[58:61]
	v_mfma_f32_16x16x32_bf16 v[46:49], v[164:167], v[208:211], v[46:49]
	v_mfma_f32_16x16x32_bf16 v[42:45], v[172:175], v[208:211], v[42:45]
	v_mfma_f32_16x16x32_bf16 v[30:33], v[164:167], v[216:219], v[30:33]
	v_mfma_f32_16x16x32_bf16 v[26:29], v[172:175], v[216:219], v[26:29]
	v_mfma_f32_16x16x32_bf16 v[14:17], v[164:167], v[236:239], v[14:17]
	v_mfma_f32_16x16x32_bf16 v[10:13], v[172:175], v[236:239], v[10:13]
	v_mfma_f32_16x16x32_bf16 v[62:65], v[168:171], v[204:207], v[62:65]
	v_mfma_f32_16x16x32_bf16 v[58:61], v[176:179], v[204:207], v[58:61]
	v_mfma_f32_16x16x32_bf16 v[46:49], v[168:171], v[212:215], v[46:49]
	v_mfma_f32_16x16x32_bf16 v[42:45], v[176:179], v[212:215], v[42:45]
	v_mfma_f32_16x16x32_bf16 v[30:33], v[168:171], v[220:223], v[30:33]
	v_mfma_f32_16x16x32_bf16 v[26:29], v[176:179], v[220:223], v[26:29]
	v_mfma_f32_16x16x32_bf16 v[14:17], v[168:171], v[240:243], v[14:17]
	v_mfma_f32_16x16x32_bf16 v[10:13], v[176:179], v[240:243], v[10:13]
	v_mfma_f32_16x16x32_bf16 v[54:57], v[180:183], v[200:203], v[54:57]
	v_mfma_f32_16x16x32_bf16 v[50:53], v[188:191], v[200:203], v[50:53]
	v_mfma_f32_16x16x32_bf16 v[38:41], v[180:183], v[208:211], v[38:41]
	v_mfma_f32_16x16x32_bf16 v[34:37], v[188:191], v[208:211], v[34:37]
	v_mfma_f32_16x16x32_bf16 v[22:25], v[180:183], v[216:219], v[22:25]
	v_mfma_f32_16x16x32_bf16 v[18:21], v[188:191], v[216:219], v[18:21]
	v_mfma_f32_16x16x32_bf16 v[6:9], v[180:183], v[236:239], v[6:9]
	v_mfma_f32_16x16x32_bf16 v[2:5], v[188:191], v[236:239], v[2:5]
	v_mfma_f32_16x16x32_bf16 v[54:57], v[184:187], v[204:207], v[54:57]
	v_mfma_f32_16x16x32_bf16 v[50:53], v[192:195], v[204:207], v[50:53]
	v_mfma_f32_16x16x32_bf16 v[38:41], v[184:187], v[212:215], v[38:41]
	v_mfma_f32_16x16x32_bf16 v[34:37], v[192:195], v[212:215], v[34:37]
	v_mfma_f32_16x16x32_bf16 v[22:25], v[184:187], v[220:223], v[22:25]
	v_mfma_f32_16x16x32_bf16 v[18:21], v[192:195], v[220:223], v[18:21]
	v_mfma_f32_16x16x32_bf16 v[6:9], v[184:187], v[240:243], v[6:9]
	v_mfma_f32_16x16x32_bf16 v[2:5], v[192:195], v[240:243], v[2:5]
	s_setprio 0
	s_barrier
	s_add_i32 s90, s90, 2
	s_add_u32 s36, s36, 0x100
	s_addc_u32 s37, s37, 0
	s_add_u32 s88, s88, 0x100
	s_addc_u32 s89, s89, 0
	s_cmp_gt_u32 s90, 13
	s_cbranch_scc0 .LBB0_1058
	s_and_b64 vcc, exec, s[16:17]
	s_cbranch_vccz .LBB0_1061
	s_barrier

.LBB0_1195:
	s_add_u32 s58, s44, s52
	s_addc_u32 s59, s45, s53
	s_add_u32 s56, s58, 0x100
	s_addc_u32 s57, s59, 0
	s_and_b64 s[54:55], s[50:51], exec
	s_cselect_b32 s55, s17, s57
	s_cselect_b32 s54, s29, s56
	s_add_u32 s52, s42, s52
	s_addc_u32 s53, s43, s53
	v_or_b32_e32 v0, 0x10000, v141
	s_add_u32 s52, s52, 0x100
	ds_read_b128 v[142:145], v0
	v_add_u32_e32 v0, 0x10400, v141
	s_addc_u32 s53, s53, 0
	ds_read_b128 v[146:149], v0
	v_add_u32_e32 v0, 0x10800, v141
	s_and_b64 s[50:51], s[50:51], exec
	ds_read_b128 v[150:153], v0
	v_add_u32_e32 v0, 0x10c00, v141
	s_cselect_b32 s57, s39, s53
	s_cselect_b32 s56, s38, s52
	s_add_u32 s60, s58, 0x80080
	ds_read_b128 v[154:157], v0
	v_or_b32_e32 v0, 0x14000, v141
	s_addc_u32 s61, s59, 0
	s_add_i32 m0, s63, 0xc000
	s_add_i32 vcc_lo, s63, 0xe000
	ds_read_b128 v[158:161], v0
	v_add_u32_e32 v0, 0x14400, v141
	s_add_u32 s58, s56, 0x40000
	ds_read_b128 v[162:165], v0
	v_add_u32_e32 v0, 0x14800, v141
	s_addc_u32 s59, s57, 0
	ds_read_b128 v[166:169], v0
	v_add_u32_e32 v0, 0x14c00, v141
	s_add_u32 s52, s54, 0x80000
	ds_read_b128 v[170:173], v0
	s_addc_u32 s53, s55, 0
	s_add_u32 s50, s56, 0x40080
	s_addc_u32 s51, s57, 0
	v_lshl_add_u64 v[138:139], s[60:61], 0, v[136:137]
	ds_read_b128 v[174:177], v140
	ds_read_b128 v[178:181], v140 offset:1024
	ds_read_b128 v[182:185], v140 offset:2048
	ds_read_b128 v[186:189], v140 offset:3072
	ds_read_b128 v[190:193], v140 offset:4096
	ds_read_b128 v[200:203], v140 offset:5120
	ds_read_b128 v[204:207], v140 offset:6144
	ds_read_b128 v[208:211], v140 offset:7168
	global_load_lds_dwordx4 v136, s[60:61]
	v_lshl_add_u64 v[138:139], s[60:61], 0, v[132:133]
	s_mov_b32 m0, vcc_lo
	s_nop 0
	global_load_lds_dwordx4 v132, s[60:61]
	s_waitcnt vmcnt(8)
	s_waitcnt lgkmcnt(0)
	s_barrier
	s_setprio 1
	v_mfma_f32_16x16x32_bf16 v[126:129], v[142:145], v[174:177], v[126:129]
	v_mfma_f32_16x16x32_bf16 v[122:125], v[150:153], v[174:177], v[122:125]
	v_mfma_f32_16x16x32_bf16 v[118:121], v[142:145], v[182:185], v[118:121]
	v_mfma_f32_16x16x32_bf16 v[110:113], v[150:153], v[182:185], v[110:113]
	v_mfma_f32_16x16x32_bf16 v[102:105], v[142:145], v[190:193], v[102:105]
	v_mfma_f32_16x16x32_bf16 v[94:97], v[150:153], v[190:193], v[94:97]
	v_mfma_f32_16x16x32_bf16 v[86:89], v[142:145], v[204:207], v[86:89]
	v_mfma_f32_16x16x32_bf16 v[78:81], v[150:153], v[204:207], v[78:81]
	v_mfma_f32_16x16x32_bf16 v[126:129], v[146:149], v[178:181], v[126:129]
	v_mfma_f32_16x16x32_bf16 v[122:125], v[154:157], v[178:181], v[122:125]
	v_mfma_f32_16x16x32_bf16 v[118:121], v[146:149], v[186:189], v[118:121]
	v_mfma_f32_16x16x32_bf16 v[110:113], v[154:157], v[186:189], v[110:113]
	v_mfma_f32_16x16x32_bf16 v[102:105], v[146:149], v[200:203], v[102:105]
	v_mfma_f32_16x16x32_bf16 v[94:97], v[154:157], v[200:203], v[94:97]
	v_mfma_f32_16x16x32_bf16 v[86:89], v[146:149], v[208:211], v[86:89]
	v_mfma_f32_16x16x32_bf16 v[78:81], v[154:157], v[208:211], v[78:81]
	v_mfma_f32_16x16x32_bf16 v[114:117], v[158:161], v[174:177], v[114:117]
	v_mfma_f32_16x16x32_bf16 v[106:109], v[166:169], v[174:177], v[106:109]
	v_mfma_f32_16x16x32_bf16 v[98:101], v[158:161], v[182:185], v[98:101]
	v_mfma_f32_16x16x32_bf16 v[90:93], v[166:169], v[182:185], v[90:93]
	v_mfma_f32_16x16x32_bf16 v[82:85], v[158:161], v[190:193], v[82:85]
	v_mfma_f32_16x16x32_bf16 v[74:77], v[166:169], v[190:193], v[74:77]
	v_mfma_f32_16x16x32_bf16 v[70:73], v[158:161], v[204:207], v[70:73]
	v_mfma_f32_16x16x32_bf16 v[66:69], v[166:169], v[204:207], v[66:69]
	v_mfma_f32_16x16x32_bf16 v[114:117], v[162:165], v[178:181], v[114:117]
	v_mfma_f32_16x16x32_bf16 v[106:109], v[170:173], v[178:181], v[106:109]
	v_mfma_f32_16x16x32_bf16 v[98:101], v[162:165], v[186:189], v[98:101]
	v_mfma_f32_16x16x32_bf16 v[90:93], v[170:173], v[186:189], v[90:93]
	v_mfma_f32_16x16x32_bf16 v[82:85], v[162:165], v[200:203], v[82:85]
	v_mfma_f32_16x16x32_bf16 v[74:77], v[170:173], v[200:203], v[74:77]
	v_mfma_f32_16x16x32_bf16 v[70:73], v[162:165], v[208:211], v[70:73]
	v_mfma_f32_16x16x32_bf16 v[66:69], v[170:173], v[208:211], v[66:69]
	s_setprio 0
	s_barrier
	s_mov_b32 m0, s64
	v_lshl_add_u64 v[138:139], s[56:57], 0, v[134:135]
	ds_read_b128 v[174:177], v140 offset:16384
	ds_read_b128 v[178:181], v140 offset:17408
	ds_read_b128 v[182:185], v140 offset:18432
	ds_read_b128 v[186:189], v140 offset:19456
	ds_read_b128 v[190:193], v140 offset:20480
	ds_read_b128 v[200:203], v140 offset:21504
	ds_read_b128 v[204:207], v140 offset:22528
	ds_read_b128 v[208:211], v140 offset:23552
	global_load_lds_dwordx4 v134, s[56:57]
	v_lshl_add_u64 v[194:195], s[56:57], 0, v[130:131]
	s_mov_b32 m0, s65
	s_nop 0
	global_load_lds_dwordx4 v130, s[56:57]
	s_mov_b32 m0, s66
	v_lshl_add_u64 v[214:215], s[54:55], 0, v[132:133]
	global_load_lds_dwordx4 v134, s[58:59]
	s_mov_b32 m0, s67
	s_nop 0
	global_load_lds_dwordx4 v130, s[58:59]
	v_lshl_add_u64 v[212:213], s[54:55], 0, v[136:137]
	s_mov_b32 m0, s63
	s_nop 0
	global_load_lds_dwordx4 v136, s[54:55]
	s_mov_b32 m0, s80
	s_nop 0
	global_load_lds_dwordx4 v132, s[54:55]
	s_waitcnt vmcnt(8)
	s_waitcnt lgkmcnt(0)
	s_barrier
	s_setprio 1
	v_mfma_f32_16x16x32_bf16 v[62:65], v[142:145], v[174:177], v[62:65]
	v_mfma_f32_16x16x32_bf16 v[58:61], v[150:153], v[174:177], v[58:61]
	v_mfma_f32_16x16x32_bf16 v[54:57], v[142:145], v[182:185], v[54:57]
	v_mfma_f32_16x16x32_bf16 v[46:49], v[150:153], v[182:185], v[46:49]
	v_mfma_f32_16x16x32_bf16 v[38:41], v[142:145], v[190:193], v[38:41]
	v_mfma_f32_16x16x32_bf16 v[30:33], v[150:153], v[190:193], v[30:33]
	v_mfma_f32_16x16x32_bf16 v[22:25], v[142:145], v[204:207], v[22:25]
	v_mfma_f32_16x16x32_bf16 v[14:17], v[150:153], v[204:207], v[14:17]
	v_mfma_f32_16x16x32_bf16 v[62:65], v[146:149], v[178:181], v[62:65]
	v_mfma_f32_16x16x32_bf16 v[58:61], v[154:157], v[178:181], v[58:61]
	v_mfma_f32_16x16x32_bf16 v[54:57], v[146:149], v[186:189], v[54:57]
	v_mfma_f32_16x16x32_bf16 v[46:49], v[154:157], v[186:189], v[46:49]
	v_mfma_f32_16x16x32_bf16 v[38:41], v[146:149], v[200:203], v[38:41]
	v_mfma_f32_16x16x32_bf16 v[30:33], v[154:157], v[200:203], v[30:33]
	v_mfma_f32_16x16x32_bf16 v[22:25], v[146:149], v[208:211], v[22:25]
	v_mfma_f32_16x16x32_bf16 v[14:17], v[154:157], v[208:211], v[14:17]
	v_mfma_f32_16x16x32_bf16 v[50:53], v[158:161], v[174:177], v[50:53]
	v_mfma_f32_16x16x32_bf16 v[42:45], v[166:169], v[174:177], v[42:45]
	v_mfma_f32_16x16x32_bf16 v[34:37], v[158:161], v[182:185], v[34:37]
	v_mfma_f32_16x16x32_bf16 v[26:29], v[166:169], v[182:185], v[26:29]
	v_mfma_f32_16x16x32_bf16 v[18:21], v[158:161], v[190:193], v[18:21]
	v_mfma_f32_16x16x32_bf16 v[10:13], v[166:169], v[190:193], v[10:13]
	v_mfma_f32_16x16x32_bf16 v[6:9], v[158:161], v[204:207], v[6:9]
	v_mfma_f32_16x16x32_bf16 v[2:5], v[166:169], v[204:207], v[2:5]
	v_mfma_f32_16x16x32_bf16 v[50:53], v[162:165], v[178:181], v[50:53]
	v_mfma_f32_16x16x32_bf16 v[42:45], v[170:173], v[178:181], v[42:45]
	v_mfma_f32_16x16x32_bf16 v[34:37], v[162:165], v[186:189], v[34:37]
	v_mfma_f32_16x16x32_bf16 v[26:29], v[170:173], v[186:189], v[26:29]
	v_mfma_f32_16x16x32_bf16 v[18:21], v[162:165], v[200:203], v[18:21]
	v_mfma_f32_16x16x32_bf16 v[10:13], v[170:173], v[200:203], v[10:13]
	v_mfma_f32_16x16x32_bf16 v[6:9], v[162:165], v[208:211], v[6:9]
	v_mfma_f32_16x16x32_bf16 v[2:5], v[170:173], v[208:211], v[2:5]
	s_setprio 0
	s_barrier
	v_or_b32_e32 v0, 0x18000, v141
	v_add_u32_e32 v146, 0x18400, v141
	ds_read_b128 v[142:145], v0
	ds_read_b128 v[146:149], v146
	v_add_u32_e32 v0, 0x18800, v141
	v_add_u32_e32 v154, 0x18c00, v141
	ds_read_b128 v[150:153], v0
	ds_read_b128 v[154:157], v154
	v_or_b32_e32 v0, 0x1c000, v141
	v_add_u32_e32 v162, 0x1c400, v141
	ds_read_b128 v[158:161], v0
	ds_read_b128 v[162:165], v162
	v_add_u32_e32 v0, 0x1c800, v141
	v_add_u32_e32 v170, 0x1cc00, v141
	ds_read_b128 v[166:169], v0
	ds_read_b128 v[170:173], v170
	s_mov_b32 m0, s82
	ds_read_b128 v[174:177], v140 offset:32768
	ds_read_b128 v[178:181], v140 offset:33792
	ds_read_b128 v[182:185], v140 offset:34816
	ds_read_b128 v[186:189], v140 offset:35840
	ds_read_b128 v[190:193], v140 offset:36864
	ds_read_b128 v[200:203], v140 offset:37888
	ds_read_b128 v[204:207], v140 offset:38912
	ds_read_b128 v[208:211], v140 offset:39936
	global_load_lds_dwordx4 v136, s[52:53]
	s_mov_b32 m0, s83
	s_nop 0
	global_load_lds_dwordx4 v132, s[52:53]
	s_waitcnt vmcnt(8)
	s_waitcnt lgkmcnt(0)
	s_barrier
	s_setprio 1
	v_mfma_f32_16x16x32_bf16 v[126:129], v[142:145], v[174:177], v[126:129]
	v_mfma_f32_16x16x32_bf16 v[122:125], v[150:153], v[174:177], v[122:125]
	v_mfma_f32_16x16x32_bf16 v[118:121], v[142:145], v[182:185], v[118:121]
	v_mfma_f32_16x16x32_bf16 v[110:113], v[150:153], v[182:185], v[110:113]
	v_mfma_f32_16x16x32_bf16 v[102:105], v[142:145], v[190:193], v[102:105]
	v_mfma_f32_16x16x32_bf16 v[94:97], v[150:153], v[190:193], v[94:97]
	v_mfma_f32_16x16x32_bf16 v[86:89], v[142:145], v[204:207], v[86:89]
	v_mfma_f32_16x16x32_bf16 v[78:81], v[150:153], v[204:207], v[78:81]
	v_mfma_f32_16x16x32_bf16 v[126:129], v[146:149], v[178:181], v[126:129]
	v_mfma_f32_16x16x32_bf16 v[122:125], v[154:157], v[178:181], v[122:125]
	v_mfma_f32_16x16x32_bf16 v[118:121], v[146:149], v[186:189], v[118:121]
	v_mfma_f32_16x16x32_bf16 v[110:113], v[154:157], v[186:189], v[110:113]
	v_mfma_f32_16x16x32_bf16 v[102:105], v[146:149], v[200:203], v[102:105]
	v_mfma_f32_16x16x32_bf16 v[94:97], v[154:157], v[200:203], v[94:97]
	v_mfma_f32_16x16x32_bf16 v[86:89], v[146:149], v[208:211], v[86:89]
	v_mfma_f32_16x16x32_bf16 v[78:81], v[154:157], v[208:211], v[78:81]
	v_mfma_f32_16x16x32_bf16 v[114:117], v[158:161], v[174:177], v[114:117]
	v_mfma_f32_16x16x32_bf16 v[106:109], v[166:169], v[174:177], v[106:109]
	v_mfma_f32_16x16x32_bf16 v[98:101], v[158:161], v[182:185], v[98:101]
	v_mfma_f32_16x16x32_bf16 v[90:93], v[166:169], v[182:185], v[90:93]
	v_mfma_f32_16x16x32_bf16 v[82:85], v[158:161], v[190:193], v[82:85]
	v_mfma_f32_16x16x32_bf16 v[74:77], v[166:169], v[190:193], v[74:77]
	v_mfma_f32_16x16x32_bf16 v[70:73], v[158:161], v[204:207], v[70:73]
	v_mfma_f32_16x16x32_bf16 v[66:69], v[166:169], v[204:207], v[66:69]
	v_mfma_f32_16x16x32_bf16 v[114:117], v[162:165], v[178:181], v[114:117]
	v_mfma_f32_16x16x32_bf16 v[106:109], v[170:173], v[178:181], v[106:109]
	v_mfma_f32_16x16x32_bf16 v[98:101], v[162:165], v[186:189], v[98:101]
	v_mfma_f32_16x16x32_bf16 v[90:93], v[170:173], v[186:189], v[90:93]
	v_mfma_f32_16x16x32_bf16 v[82:85], v[162:165], v[200:203], v[82:85]
	v_mfma_f32_16x16x32_bf16 v[74:77], v[170:173], v[200:203], v[74:77]
	v_mfma_f32_16x16x32_bf16 v[70:73], v[162:165], v[208:211], v[70:73]
	v_mfma_f32_16x16x32_bf16 v[66:69], v[170:173], v[208:211], v[66:69]
	s_setprio 0
	s_barrier
	s_add_i32 m0, s85, 0xffffff80
	v_lshl_add_u64 v[138:139], v[138:139], 0, s[18:19]
	ds_read_b128 v[174:177], v140 offset:49152
	ds_read_b128 v[178:181], v140 offset:50176
	ds_read_b128 v[182:185], v140 offset:51200
	ds_read_b128 v[186:189], v140 offset:52224
	ds_read_b128 v[190:193], v140 offset:53248
	ds_read_b128 v[200:203], v140 offset:54272
	ds_read_b128 v[204:207], v140 offset:55296
	ds_read_b128 v[208:211], v140 offset:56320
	global_load_lds_dwordx4 v134, s[56:57] offset:128
	v_lshl_add_u64 v[138:139], v[194:195], 0, s[18:19]
	s_add_i32 m0, s88, 0xffffff80
	s_nop 0
	global_load_lds_dwordx4 v130, s[56:57] offset:128
	v_lshl_add_u64 v[138:139], s[50:51], 0, v[134:135]
	s_mov_b32 m0, s91
	s_nop 0
	global_load_lds_dwordx4 v134, s[50:51]
	v_lshl_add_u64 v[138:139], s[50:51], 0, v[130:131]
	s_mov_b32 m0, s92
	s_nop 0
	global_load_lds_dwordx4 v130, s[50:51]
	v_lshl_add_u64 v[138:139], v[212:213], 0, s[18:19]
	s_add_i32 m0, s89, 0xffffff80
	s_nop 0
	global_load_lds_dwordx4 v136, s[54:55] offset:128
	v_lshl_add_u64 v[138:139], v[214:215], 0, s[18:19]
	s_add_i32 m0, s90, 0xffffff80
	s_nop 0
	global_load_lds_dwordx4 v132, s[54:55] offset:128
	s_waitcnt vmcnt(8)
	s_waitcnt lgkmcnt(0)
	s_barrier
	s_setprio 1
	v_mfma_f32_16x16x32_bf16 v[62:65], v[142:145], v[174:177], v[62:65]
	v_mfma_f32_16x16x32_bf16 v[58:61], v[150:153], v[174:177], v[58:61]
	v_mfma_f32_16x16x32_bf16 v[54:57], v[142:145], v[182:185], v[54:57]
	v_mfma_f32_16x16x32_bf16 v[46:49], v[150:153], v[182:185], v[46:49]
	v_mfma_f32_16x16x32_bf16 v[38:41], v[142:145], v[190:193], v[38:41]
	v_mfma_f32_16x16x32_bf16 v[30:33], v[150:153], v[190:193], v[30:33]
	v_mfma_f32_16x16x32_bf16 v[22:25], v[142:145], v[204:207], v[22:25]
	v_mfma_f32_16x16x32_bf16 v[14:17], v[150:153], v[204:207], v[14:17]
	v_mfma_f32_16x16x32_bf16 v[62:65], v[146:149], v[178:181], v[62:65]
	v_mfma_f32_16x16x32_bf16 v[58:61], v[154:157], v[178:181], v[58:61]
	v_mfma_f32_16x16x32_bf16 v[54:57], v[146:149], v[186:189], v[54:57]
	v_mfma_f32_16x16x32_bf16 v[46:49], v[154:157], v[186:189], v[46:49]
	v_mfma_f32_16x16x32_bf16 v[38:41], v[146:149], v[200:203], v[38:41]
	v_mfma_f32_16x16x32_bf16 v[30:33], v[154:157], v[200:203], v[30:33]
	v_mfma_f32_16x16x32_bf16 v[22:25], v[146:149], v[208:211], v[22:25]
	v_mfma_f32_16x16x32_bf16 v[14:17], v[154:157], v[208:211], v[14:17]
	v_mfma_f32_16x16x32_bf16 v[50:53], v[158:161], v[174:177], v[50:53]
	v_mfma_f32_16x16x32_bf16 v[42:45], v[166:169], v[174:177], v[42:45]
	v_mfma_f32_16x16x32_bf16 v[34:37], v[158:161], v[182:185], v[34:37]
	v_mfma_f32_16x16x32_bf16 v[26:29], v[166:169], v[182:185], v[26:29]
	v_mfma_f32_16x16x32_bf16 v[18:21], v[158:161], v[190:193], v[18:21]
	v_mfma_f32_16x16x32_bf16 v[10:13], v[166:169], v[190:193], v[10:13]
	v_mfma_f32_16x16x32_bf16 v[6:9], v[158:161], v[204:207], v[6:9]
	v_mfma_f32_16x16x32_bf16 v[2:5], v[166:169], v[204:207], v[2:5]
	v_mfma_f32_16x16x32_bf16 v[50:53], v[162:165], v[178:181], v[50:53]
	v_mfma_f32_16x16x32_bf16 v[42:45], v[170:173], v[178:181], v[42:45]
	v_mfma_f32_16x16x32_bf16 v[34:37], v[162:165], v[186:189], v[34:37]
	v_mfma_f32_16x16x32_bf16 v[26:29], v[170:173], v[186:189], v[26:29]
	v_mfma_f32_16x16x32_bf16 v[18:21], v[162:165], v[200:203], v[18:21]
	v_mfma_f32_16x16x32_bf16 v[10:13], v[170:173], v[200:203], v[10:13]
	v_mfma_f32_16x16x32_bf16 v[6:9], v[162:165], v[208:211], v[6:9]
	v_mfma_f32_16x16x32_bf16 v[2:5], v[170:173], v[208:211], v[2:5]
	s_setprio 0
	s_barrier
	s_andn2_b64 vcc, exec, s[48:49]
	s_mov_b64 s[50:51], -1
	s_mov_b64 s[48:49], 0
	s_mov_b64 s[52:53], 0x100
	s_cbranch_vccz .LBB0_1195
	s_and_b64 vcc, exec, s[14:15]
	s_cbranch_vccz .LBB0_1198
	s_barrier

.LBB0_1213:
	s_add_u32 s58, s40, s52
	s_addc_u32 s59, s41, s53
	s_add_u32 s56, s58, 0x100
	s_addc_u32 s57, s59, 0
	s_and_b64 s[54:55], s[50:51], exec
	s_cselect_b32 s55, s43, s57
	s_cselect_b32 s54, s42, s56
	s_add_u32 s52, s38, s52
	s_addc_u32 s53, s39, s53
	v_or_b32_e32 v0, 0x10000, v139
	s_add_u32 s52, s52, 0x100
	ds_read_b128 v[140:143], v0
	v_add_u32_e32 v0, 0x10400, v139
	s_addc_u32 s53, s53, 0
	ds_read_b128 v[144:147], v0
	v_add_u32_e32 v0, 0x10800, v139
	s_and_b64 s[50:51], s[50:51], exec
	ds_read_b128 v[148:151], v0
	v_add_u32_e32 v0, 0x10c00, v139
	s_cselect_b32 s57, s37, s53
	s_cselect_b32 s56, s29, s52
	s_add_u32 s60, s58, 0x40080
	ds_read_b128 v[152:155], v0
	v_or_b32_e32 v0, 0x14000, v139
	s_addc_u32 s61, s59, 0
	s_add_i32 m0, s63, 0xc000
	s_add_i32 vcc_lo, s63, 0xe000
	ds_read_b128 v[156:159], v0
	v_add_u32_e32 v0, 0x14400, v139
	s_add_u32 s58, s56, 0x80000
	ds_read_b128 v[160:163], v0
	v_add_u32_e32 v0, 0x14800, v139
	s_addc_u32 s59, s57, 0
	ds_read_b128 v[164:167], v0
	v_add_u32_e32 v0, 0x14c00, v139
	s_add_u32 s52, s54, 0x40000
	ds_read_b128 v[168:171], v0
	s_addc_u32 s53, s55, 0
	s_add_u32 s50, s56, 0x80080
	s_addc_u32 s51, s57, 0
	ds_read_b128 v[172:175], v138
	ds_read_b128 v[176:179], v138 offset:1024
	ds_read_b128 v[180:183], v138 offset:2048
	ds_read_b128 v[184:187], v138 offset:3072
	ds_read_b128 v[188:191], v138 offset:4096
	ds_read_b128 v[192:195], v138 offset:5120
	ds_read_b128 v[200:203], v138 offset:6144
	ds_read_b128 v[204:207], v138 offset:7168
	global_load_lds_dwordx4 v136, s[60:61]
	s_mov_b32 m0, vcc_lo
	s_nop 0
	global_load_lds_dwordx4 v132, s[60:61]
	s_waitcnt vmcnt(8)
	s_waitcnt lgkmcnt(0)
	s_barrier
	s_setprio 1
	v_mfma_f32_16x16x32_bf16 v[126:129], v[140:143], v[172:175], v[126:129]
	v_mfma_f32_16x16x32_bf16 v[122:125], v[148:151], v[172:175], v[122:125]
	v_mfma_f32_16x16x32_bf16 v[118:121], v[140:143], v[180:183], v[118:121]
	v_mfma_f32_16x16x32_bf16 v[114:117], v[148:151], v[180:183], v[114:117]
	v_mfma_f32_16x16x32_bf16 v[102:105], v[140:143], v[188:191], v[102:105]
	v_mfma_f32_16x16x32_bf16 v[98:101], v[148:151], v[188:191], v[98:101]
	v_mfma_f32_16x16x32_bf16 v[86:89], v[140:143], v[200:203], v[86:89]
	v_mfma_f32_16x16x32_bf16 v[82:85], v[148:151], v[200:203], v[82:85]
	v_mfma_f32_16x16x32_bf16 v[126:129], v[144:147], v[176:179], v[126:129]
	v_mfma_f32_16x16x32_bf16 v[122:125], v[152:155], v[176:179], v[122:125]
	v_mfma_f32_16x16x32_bf16 v[118:121], v[144:147], v[184:187], v[118:121]
	v_mfma_f32_16x16x32_bf16 v[114:117], v[152:155], v[184:187], v[114:117]
	v_mfma_f32_16x16x32_bf16 v[102:105], v[144:147], v[192:195], v[102:105]
	v_mfma_f32_16x16x32_bf16 v[98:101], v[152:155], v[192:195], v[98:101]
	v_mfma_f32_16x16x32_bf16 v[86:89], v[144:147], v[204:207], v[86:89]
	v_mfma_f32_16x16x32_bf16 v[82:85], v[152:155], v[204:207], v[82:85]
	v_mfma_f32_16x16x32_bf16 v[110:113], v[156:159], v[172:175], v[110:113]
	v_mfma_f32_16x16x32_bf16 v[106:109], v[164:167], v[172:175], v[106:109]
	v_mfma_f32_16x16x32_bf16 v[94:97], v[156:159], v[180:183], v[94:97]
	v_mfma_f32_16x16x32_bf16 v[90:93], v[164:167], v[180:183], v[90:93]
	v_mfma_f32_16x16x32_bf16 v[78:81], v[156:159], v[188:191], v[78:81]
	v_mfma_f32_16x16x32_bf16 v[74:77], v[164:167], v[188:191], v[74:77]
	v_mfma_f32_16x16x32_bf16 v[70:73], v[156:159], v[200:203], v[70:73]
	v_mfma_f32_16x16x32_bf16 v[66:69], v[164:167], v[200:203], v[66:69]
	v_mfma_f32_16x16x32_bf16 v[110:113], v[160:163], v[176:179], v[110:113]
	v_mfma_f32_16x16x32_bf16 v[106:109], v[168:171], v[176:179], v[106:109]
	v_mfma_f32_16x16x32_bf16 v[94:97], v[160:163], v[184:187], v[94:97]
	v_mfma_f32_16x16x32_bf16 v[90:93], v[168:171], v[184:187], v[90:93]
	v_mfma_f32_16x16x32_bf16 v[78:81], v[160:163], v[192:195], v[78:81]
	v_mfma_f32_16x16x32_bf16 v[74:77], v[168:171], v[192:195], v[74:77]
	v_mfma_f32_16x16x32_bf16 v[70:73], v[160:163], v[204:207], v[70:73]
	v_mfma_f32_16x16x32_bf16 v[66:69], v[168:171], v[204:207], v[66:69]
	s_setprio 0
	s_barrier
	s_mov_b32 m0, s64
	ds_read_b128 v[172:175], v138 offset:16384
	ds_read_b128 v[176:179], v138 offset:17408
	ds_read_b128 v[180:183], v138 offset:18432
	ds_read_b128 v[184:187], v138 offset:19456
	ds_read_b128 v[188:191], v138 offset:20480
	ds_read_b128 v[192:195], v138 offset:21504
	ds_read_b128 v[200:203], v138 offset:22528
	ds_read_b128 v[204:207], v138 offset:23552
	global_load_lds_dwordx4 v134, s[56:57]
	s_mov_b32 m0, s65
	s_nop 0
	global_load_lds_dwordx4 v130, s[56:57]
	s_mov_b32 m0, s66
	s_nop 0
	global_load_lds_dwordx4 v134, s[58:59]
	s_mov_b32 m0, s67
	s_nop 0
	global_load_lds_dwordx4 v130, s[58:59]
	s_mov_b32 m0, s63
	s_nop 0
	global_load_lds_dwordx4 v136, s[54:55]
	s_mov_b32 m0, s80
	s_nop 0
	global_load_lds_dwordx4 v132, s[54:55]
	s_waitcnt vmcnt(8)
	s_waitcnt lgkmcnt(0)
	s_barrier
	s_setprio 1
	v_mfma_f32_16x16x32_bf16 v[62:65], v[140:143], v[172:175], v[62:65]
	v_mfma_f32_16x16x32_bf16 v[58:61], v[148:151], v[172:175], v[58:61]
	v_mfma_f32_16x16x32_bf16 v[54:57], v[140:143], v[180:183], v[54:57]
	v_mfma_f32_16x16x32_bf16 v[50:53], v[148:151], v[180:183], v[50:53]
	v_mfma_f32_16x16x32_bf16 v[38:41], v[140:143], v[188:191], v[38:41]
	v_mfma_f32_16x16x32_bf16 v[34:37], v[148:151], v[188:191], v[34:37]
	v_mfma_f32_16x16x32_bf16 v[22:25], v[140:143], v[200:203], v[22:25]
	v_mfma_f32_16x16x32_bf16 v[18:21], v[148:151], v[200:203], v[18:21]
	v_mfma_f32_16x16x32_bf16 v[62:65], v[144:147], v[176:179], v[62:65]
	v_mfma_f32_16x16x32_bf16 v[58:61], v[152:155], v[176:179], v[58:61]
	v_mfma_f32_16x16x32_bf16 v[54:57], v[144:147], v[184:187], v[54:57]
	v_mfma_f32_16x16x32_bf16 v[50:53], v[152:155], v[184:187], v[50:53]
	v_mfma_f32_16x16x32_bf16 v[38:41], v[144:147], v[192:195], v[38:41]
	v_mfma_f32_16x16x32_bf16 v[34:37], v[152:155], v[192:195], v[34:37]
	v_mfma_f32_16x16x32_bf16 v[22:25], v[144:147], v[204:207], v[22:25]
	v_mfma_f32_16x16x32_bf16 v[18:21], v[152:155], v[204:207], v[18:21]
	v_mfma_f32_16x16x32_bf16 v[46:49], v[156:159], v[172:175], v[46:49]
	v_mfma_f32_16x16x32_bf16 v[42:45], v[164:167], v[172:175], v[42:45]
	v_mfma_f32_16x16x32_bf16 v[30:33], v[156:159], v[180:183], v[30:33]
	v_mfma_f32_16x16x32_bf16 v[26:29], v[164:167], v[180:183], v[26:29]
	v_mfma_f32_16x16x32_bf16 v[14:17], v[156:159], v[188:191], v[14:17]
	v_mfma_f32_16x16x32_bf16 v[10:13], v[164:167], v[188:191], v[10:13]
	v_mfma_f32_16x16x32_bf16 v[6:9], v[156:159], v[200:203], v[6:9]
	v_mfma_f32_16x16x32_bf16 v[2:5], v[164:167], v[200:203], v[2:5]
	v_mfma_f32_16x16x32_bf16 v[46:49], v[160:163], v[176:179], v[46:49]
	v_mfma_f32_16x16x32_bf16 v[42:45], v[168:171], v[176:179], v[42:45]
	v_mfma_f32_16x16x32_bf16 v[30:33], v[160:163], v[184:187], v[30:33]
	v_mfma_f32_16x16x32_bf16 v[26:29], v[168:171], v[184:187], v[26:29]
	v_mfma_f32_16x16x32_bf16 v[14:17], v[160:163], v[192:195], v[14:17]
	v_mfma_f32_16x16x32_bf16 v[10:13], v[168:171], v[192:195], v[10:13]
	v_mfma_f32_16x16x32_bf16 v[6:9], v[160:163], v[204:207], v[6:9]
	v_mfma_f32_16x16x32_bf16 v[2:5], v[168:171], v[204:207], v[2:5]
	s_setprio 0
	s_barrier
	v_or_b32_e32 v0, 0x18000, v139
	v_add_u32_e32 v144, 0x18400, v139
	ds_read_b128 v[140:143], v0
	ds_read_b128 v[144:147], v144
	v_add_u32_e32 v0, 0x18800, v139
	v_add_u32_e32 v152, 0x18c00, v139
	ds_read_b128 v[148:151], v0
	ds_read_b128 v[152:155], v152
	v_or_b32_e32 v0, 0x1c000, v139
	v_add_u32_e32 v160, 0x1c400, v139
	ds_read_b128 v[156:159], v0
	ds_read_b128 v[160:163], v160
	v_add_u32_e32 v0, 0x1c800, v139
	v_add_u32_e32 v168, 0x1cc00, v139
	ds_read_b128 v[164:167], v0
	ds_read_b128 v[168:171], v168
	s_mov_b32 m0, s82
	ds_read_b128 v[172:175], v138 offset:32768
	ds_read_b128 v[176:179], v138 offset:33792
	ds_read_b128 v[180:183], v138 offset:34816
	ds_read_b128 v[184:187], v138 offset:35840
	ds_read_b128 v[188:191], v138 offset:36864
	ds_read_b128 v[192:195], v138 offset:37888
	ds_read_b128 v[200:203], v138 offset:38912
	ds_read_b128 v[204:207], v138 offset:39936
	global_load_lds_dwordx4 v136, s[52:53]
	s_mov_b32 m0, s83
	s_nop 0
	global_load_lds_dwordx4 v132, s[52:53]
	s_waitcnt vmcnt(8)
	s_waitcnt lgkmcnt(0)
	s_barrier
	s_setprio 1
	v_mfma_f32_16x16x32_bf16 v[126:129], v[140:143], v[172:175], v[126:129]
	v_mfma_f32_16x16x32_bf16 v[122:125], v[148:151], v[172:175], v[122:125]
	v_mfma_f32_16x16x32_bf16 v[118:121], v[140:143], v[180:183], v[118:121]
	v_mfma_f32_16x16x32_bf16 v[114:117], v[148:151], v[180:183], v[114:117]
	v_mfma_f32_16x16x32_bf16 v[102:105], v[140:143], v[188:191], v[102:105]
	v_mfma_f32_16x16x32_bf16 v[98:101], v[148:151], v[188:191], v[98:101]
	v_mfma_f32_16x16x32_bf16 v[86:89], v[140:143], v[200:203], v[86:89]
	v_mfma_f32_16x16x32_bf16 v[82:85], v[148:151], v[200:203], v[82:85]
	v_mfma_f32_16x16x32_bf16 v[126:129], v[144:147], v[176:179], v[126:129]
	v_mfma_f32_16x16x32_bf16 v[122:125], v[152:155], v[176:179], v[122:125]
	v_mfma_f32_16x16x32_bf16 v[118:121], v[144:147], v[184:187], v[118:121]
	v_mfma_f32_16x16x32_bf16 v[114:117], v[152:155], v[184:187], v[114:117]
	v_mfma_f32_16x16x32_bf16 v[102:105], v[144:147], v[192:195], v[102:105]
	v_mfma_f32_16x16x32_bf16 v[98:101], v[152:155], v[192:195], v[98:101]
	v_mfma_f32_16x16x32_bf16 v[86:89], v[144:147], v[204:207], v[86:89]
	v_mfma_f32_16x16x32_bf16 v[82:85], v[152:155], v[204:207], v[82:85]
	v_mfma_f32_16x16x32_bf16 v[110:113], v[156:159], v[172:175], v[110:113]
	v_mfma_f32_16x16x32_bf16 v[106:109], v[164:167], v[172:175], v[106:109]
	v_mfma_f32_16x16x32_bf16 v[94:97], v[156:159], v[180:183], v[94:97]
	v_mfma_f32_16x16x32_bf16 v[90:93], v[164:167], v[180:183], v[90:93]
	v_mfma_f32_16x16x32_bf16 v[78:81], v[156:159], v[188:191], v[78:81]
	v_mfma_f32_16x16x32_bf16 v[74:77], v[164:167], v[188:191], v[74:77]
	v_mfma_f32_16x16x32_bf16 v[70:73], v[156:159], v[200:203], v[70:73]
	v_mfma_f32_16x16x32_bf16 v[66:69], v[164:167], v[200:203], v[66:69]
	v_mfma_f32_16x16x32_bf16 v[110:113], v[160:163], v[176:179], v[110:113]
	v_mfma_f32_16x16x32_bf16 v[106:109], v[168:171], v[176:179], v[106:109]
	v_mfma_f32_16x16x32_bf16 v[94:97], v[160:163], v[184:187], v[94:97]
	v_mfma_f32_16x16x32_bf16 v[90:93], v[168:171], v[184:187], v[90:93]
	v_mfma_f32_16x16x32_bf16 v[78:81], v[160:163], v[192:195], v[78:81]
	v_mfma_f32_16x16x32_bf16 v[74:77], v[168:171], v[192:195], v[74:77]
	v_mfma_f32_16x16x32_bf16 v[70:73], v[160:163], v[204:207], v[70:73]
	v_mfma_f32_16x16x32_bf16 v[66:69], v[168:171], v[204:207], v[66:69]
	s_setprio 0
	s_barrier
	s_add_i32 m0, s85, 0xffffff80
	ds_read_b128 v[172:175], v138 offset:49152
	ds_read_b128 v[176:179], v138 offset:50176
	ds_read_b128 v[180:183], v138 offset:51200
	ds_read_b128 v[184:187], v138 offset:52224
	ds_read_b128 v[188:191], v138 offset:53248
	ds_read_b128 v[192:195], v138 offset:54272
	ds_read_b128 v[200:203], v138 offset:55296
	ds_read_b128 v[204:207], v138 offset:56320
	global_load_lds_dwordx4 v134, s[56:57] offset:128
	s_add_i32 m0, s88, 0xffffff80
	s_nop 0
	global_load_lds_dwordx4 v130, s[56:57] offset:128
	s_mov_b32 m0, s91
	s_nop 0
	global_load_lds_dwordx4 v134, s[50:51]
	s_mov_b32 m0, s92
	s_nop 0
	global_load_lds_dwordx4 v130, s[50:51]
	s_add_i32 m0, s89, 0xffffff80
	s_nop 0
	global_load_lds_dwordx4 v136, s[54:55] offset:128
	s_add_i32 m0, s90, 0xffffff80
	s_nop 0
	global_load_lds_dwordx4 v132, s[54:55] offset:128
	s_waitcnt vmcnt(8)
	s_waitcnt lgkmcnt(0)
	s_barrier
	s_setprio 1
	v_mfma_f32_16x16x32_bf16 v[62:65], v[140:143], v[172:175], v[62:65]
	v_mfma_f32_16x16x32_bf16 v[58:61], v[148:151], v[172:175], v[58:61]
	v_mfma_f32_16x16x32_bf16 v[54:57], v[140:143], v[180:183], v[54:57]
	v_mfma_f32_16x16x32_bf16 v[50:53], v[148:151], v[180:183], v[50:53]
	v_mfma_f32_16x16x32_bf16 v[38:41], v[140:143], v[188:191], v[38:41]
	v_mfma_f32_16x16x32_bf16 v[34:37], v[148:151], v[188:191], v[34:37]
	v_mfma_f32_16x16x32_bf16 v[22:25], v[140:143], v[200:203], v[22:25]
	v_mfma_f32_16x16x32_bf16 v[18:21], v[148:151], v[200:203], v[18:21]
	v_mfma_f32_16x16x32_bf16 v[62:65], v[144:147], v[176:179], v[62:65]
	v_mfma_f32_16x16x32_bf16 v[58:61], v[152:155], v[176:179], v[58:61]
	v_mfma_f32_16x16x32_bf16 v[54:57], v[144:147], v[184:187], v[54:57]
	v_mfma_f32_16x16x32_bf16 v[50:53], v[152:155], v[184:187], v[50:53]
	v_mfma_f32_16x16x32_bf16 v[38:41], v[144:147], v[192:195], v[38:41]
	v_mfma_f32_16x16x32_bf16 v[34:37], v[152:155], v[192:195], v[34:37]
	v_mfma_f32_16x16x32_bf16 v[22:25], v[144:147], v[204:207], v[22:25]
	v_mfma_f32_16x16x32_bf16 v[18:21], v[152:155], v[204:207], v[18:21]
	v_mfma_f32_16x16x32_bf16 v[46:49], v[156:159], v[172:175], v[46:49]
	v_mfma_f32_16x16x32_bf16 v[42:45], v[164:167], v[172:175], v[42:45]
	v_mfma_f32_16x16x32_bf16 v[30:33], v[156:159], v[180:183], v[30:33]
	v_mfma_f32_16x16x32_bf16 v[26:29], v[164:167], v[180:183], v[26:29]
	v_mfma_f32_16x16x32_bf16 v[14:17], v[156:159], v[188:191], v[14:17]
	v_mfma_f32_16x16x32_bf16 v[10:13], v[164:167], v[188:191], v[10:13]
	v_mfma_f32_16x16x32_bf16 v[6:9], v[156:159], v[200:203], v[6:9]
	v_mfma_f32_16x16x32_bf16 v[2:5], v[164:167], v[200:203], v[2:5]
	v_mfma_f32_16x16x32_bf16 v[46:49], v[160:163], v[176:179], v[46:49]
	v_mfma_f32_16x16x32_bf16 v[42:45], v[168:171], v[176:179], v[42:45]
	v_mfma_f32_16x16x32_bf16 v[30:33], v[160:163], v[184:187], v[30:33]
	v_mfma_f32_16x16x32_bf16 v[26:29], v[168:171], v[184:187], v[26:29]
	v_mfma_f32_16x16x32_bf16 v[14:17], v[160:163], v[192:195], v[14:17]
	v_mfma_f32_16x16x32_bf16 v[10:13], v[168:171], v[192:195], v[10:13]
	v_mfma_f32_16x16x32_bf16 v[6:9], v[160:163], v[204:207], v[6:9]
	v_mfma_f32_16x16x32_bf16 v[2:5], v[168:171], v[204:207], v[2:5]
	s_setprio 0
	s_barrier
	s_andn2_b64 vcc, exec, s[48:49]
	s_mov_b64 s[50:51], -1
	s_mov_b64 s[48:49], 0
	s_mov_b64 s[52:53], 0x100
	s_cbranch_vccz .LBB0_1213
	s_and_b64 vcc, exec, s[14:15]
	s_cbranch_vccz .LBB0_1216
	s_barrier

.LBB0_2006:
	v_or_b32_e32 v0, 0x10000, v164
	v_add_u32_e32 v165, 0x10400, v164
	ds_read_b128 v[158:161], v0
	ds_read_b128 v[166:169], v165
	v_add_u32_e32 v0, 0x10800, v164
	v_add_u32_e32 v165, 0x10c00, v164
	ds_read_b128 v[170:173], v0
	ds_read_b128 v[174:177], v165
	v_or_b32_e32 v0, 0x14000, v164
	v_add_u32_e32 v165, 0x14400, v164
	ds_read_b128 v[178:181], v0
	ds_read_b128 v[182:185], v165
	v_add_u32_e32 v0, 0x14800, v164
	v_add_u32_e32 v165, 0x14c00, v164
	ds_read_b128 v[186:189], v0
	ds_read_b128 v[190:193], v165
	s_add_u32 s40, s36, 0xfffc0080
	s_addc_u32 s41, s37, -1
	s_cmp_eq_u32 vcc_lo, 12
	s_cselect_b32 s63, s29, s41
	s_cselect_b32 s62, s47, s40
	s_cselect_b32 s61, s49, s95
	s_cselect_b32 s60, s59, s80
	s_add_i32 m0, s31, 0xc000
	ds_read_b128 v[200:203], v163
	ds_read_b128 v[204:207], v163 offset:1024
	ds_read_b128 v[208:211], v163 offset:2048
	ds_read_b128 v[212:215], v163 offset:3072
	ds_read_b128 v[216:219], v163 offset:4096
	ds_read_b128 v[220:223], v163 offset:5120
	ds_read_b128 v[236:239], v163 offset:6144
	ds_read_b128 v[240:243], v163 offset:7168
	global_load_lds_dwordx4 v138, s[36:37]
	s_add_i32 m0, s31, 0xe000
	s_nop 0
	global_load_lds_dwordx4 v140, s[36:37]
	s_waitcnt vmcnt(8)
	s_waitcnt lgkmcnt(0)
	s_barrier
	s_setprio 1
	v_mfma_f32_16x16x32_bf16 v[126:129], v[158:161], v[200:203], v[126:129]
	v_mfma_f32_16x16x32_bf16 v[122:125], v[170:173], v[200:203], v[122:125]
	v_mfma_f32_16x16x32_bf16 v[114:117], v[158:161], v[208:211], v[114:117]
	v_mfma_f32_16x16x32_bf16 v[106:109], v[170:173], v[208:211], v[106:109]
	v_mfma_f32_16x16x32_bf16 v[98:101], v[158:161], v[216:219], v[98:101]
	v_mfma_f32_16x16x32_bf16 v[90:93], v[170:173], v[216:219], v[90:93]
	v_mfma_f32_16x16x32_bf16 v[82:85], v[158:161], v[236:239], v[82:85]
	v_mfma_f32_16x16x32_bf16 v[74:77], v[170:173], v[236:239], v[74:77]
	v_mfma_f32_16x16x32_bf16 v[126:129], v[166:169], v[204:207], v[126:129]
	v_mfma_f32_16x16x32_bf16 v[122:125], v[174:177], v[204:207], v[122:125]
	v_mfma_f32_16x16x32_bf16 v[114:117], v[166:169], v[212:215], v[114:117]
	v_mfma_f32_16x16x32_bf16 v[106:109], v[174:177], v[212:215], v[106:109]
	v_mfma_f32_16x16x32_bf16 v[98:101], v[166:169], v[220:223], v[98:101]
	v_mfma_f32_16x16x32_bf16 v[90:93], v[174:177], v[220:223], v[90:93]
	v_mfma_f32_16x16x32_bf16 v[82:85], v[166:169], v[240:243], v[82:85]
	v_mfma_f32_16x16x32_bf16 v[74:77], v[174:177], v[240:243], v[74:77]
	v_mfma_f32_16x16x32_bf16 v[118:121], v[178:181], v[200:203], v[118:121]
	v_mfma_f32_16x16x32_bf16 v[110:113], v[186:189], v[200:203], v[110:113]
	v_mfma_f32_16x16x32_bf16 v[102:105], v[178:181], v[208:211], v[102:105]
	v_mfma_f32_16x16x32_bf16 v[94:97], v[186:189], v[208:211], v[94:97]
	v_mfma_f32_16x16x32_bf16 v[86:89], v[178:181], v[216:219], v[86:89]
	v_mfma_f32_16x16x32_bf16 v[78:81], v[186:189], v[216:219], v[78:81]
	v_mfma_f32_16x16x32_bf16 v[70:73], v[178:181], v[236:239], v[70:73]
	v_mfma_f32_16x16x32_bf16 v[66:69], v[186:189], v[236:239], v[66:69]
	v_mfma_f32_16x16x32_bf16 v[118:121], v[182:185], v[204:207], v[118:121]
	v_mfma_f32_16x16x32_bf16 v[110:113], v[190:193], v[204:207], v[110:113]
	v_mfma_f32_16x16x32_bf16 v[102:105], v[182:185], v[212:215], v[102:105]
	v_mfma_f32_16x16x32_bf16 v[94:97], v[190:193], v[212:215], v[94:97]
	v_mfma_f32_16x16x32_bf16 v[86:89], v[182:185], v[220:223], v[86:89]
	v_mfma_f32_16x16x32_bf16 v[78:81], v[190:193], v[220:223], v[78:81]
	v_mfma_f32_16x16x32_bf16 v[70:73], v[182:185], v[240:243], v[70:73]
	v_mfma_f32_16x16x32_bf16 v[66:69], v[190:193], v[240:243], v[66:69]
	s_setprio 0
	s_barrier
	s_mov_b32 m0, s51
	s_add_u32 s40, s60, 0x40000
	ds_read_b128 v[200:203], v163 offset:16384
	ds_read_b128 v[204:207], v163 offset:17408
	ds_read_b128 v[208:211], v163 offset:18432
	ds_read_b128 v[212:215], v163 offset:19456
	ds_read_b128 v[216:219], v163 offset:20480
	ds_read_b128 v[220:223], v163 offset:21504
	ds_read_b128 v[236:239], v163 offset:22528
	ds_read_b128 v[240:243], v163 offset:23552
	global_load_lds_dwordx4 v132, s[60:61]
	v_lshl_add_u64 v[226:227], s[60:61], 0, v[136:137]
	s_mov_b32 m0, s65
	s_addc_u32 s41, s61, 0
	global_load_lds_dwordx4 v136, s[60:61]
	s_mov_b32 m0, s66
	s_nop 0
	global_load_lds_dwordx4 v132, s[40:41]
	s_mov_b32 m0, s67
	s_nop 0
	global_load_lds_dwordx4 v136, s[40:41]
	s_mov_b32 m0, s31
	s_nop 0
	global_load_lds_dwordx4 v130, s[62:63]
	s_mov_b32 m0, s82
	s_nop 0
	global_load_lds_dwordx4 v134, s[62:63]
	s_waitcnt vmcnt(8)
	s_waitcnt lgkmcnt(0)
	s_barrier
	s_setprio 1
	v_mfma_f32_16x16x32_bf16 v[62:65], v[158:161], v[200:203], v[62:65]
	v_mfma_f32_16x16x32_bf16 v[58:61], v[170:173], v[200:203], v[58:61]
	v_mfma_f32_16x16x32_bf16 v[54:57], v[158:161], v[208:211], v[54:57]
	v_mfma_f32_16x16x32_bf16 v[46:49], v[170:173], v[208:211], v[46:49]
	v_mfma_f32_16x16x32_bf16 v[38:41], v[158:161], v[216:219], v[38:41]
	v_mfma_f32_16x16x32_bf16 v[30:33], v[170:173], v[216:219], v[30:33]
	v_mfma_f32_16x16x32_bf16 v[22:25], v[158:161], v[236:239], v[22:25]
	v_mfma_f32_16x16x32_bf16 v[14:17], v[170:173], v[236:239], v[14:17]
	v_mfma_f32_16x16x32_bf16 v[62:65], v[166:169], v[204:207], v[62:65]
	v_mfma_f32_16x16x32_bf16 v[58:61], v[174:177], v[204:207], v[58:61]
	v_mfma_f32_16x16x32_bf16 v[54:57], v[166:169], v[212:215], v[54:57]
	v_mfma_f32_16x16x32_bf16 v[46:49], v[174:177], v[212:215], v[46:49]
	v_mfma_f32_16x16x32_bf16 v[38:41], v[166:169], v[220:223], v[38:41]
	v_mfma_f32_16x16x32_bf16 v[30:33], v[174:177], v[220:223], v[30:33]
	v_mfma_f32_16x16x32_bf16 v[22:25], v[166:169], v[240:243], v[22:25]
	v_mfma_f32_16x16x32_bf16 v[14:17], v[174:177], v[240:243], v[14:17]
	v_mfma_f32_16x16x32_bf16 v[50:53], v[178:181], v[200:203], v[50:53]
	v_mfma_f32_16x16x32_bf16 v[42:45], v[186:189], v[200:203], v[42:45]
	v_mfma_f32_16x16x32_bf16 v[34:37], v[178:181], v[208:211], v[34:37]
	v_mfma_f32_16x16x32_bf16 v[26:29], v[186:189], v[208:211], v[26:29]
	v_mfma_f32_16x16x32_bf16 v[18:21], v[178:181], v[216:219], v[18:21]
	v_mfma_f32_16x16x32_bf16 v[10:13], v[186:189], v[216:219], v[10:13]
	v_mfma_f32_16x16x32_bf16 v[6:9], v[178:181], v[236:239], v[6:9]
	v_mfma_f32_16x16x32_bf16 v[2:5], v[186:189], v[236:239], v[2:5]
	v_mfma_f32_16x16x32_bf16 v[50:53], v[182:185], v[204:207], v[50:53]
	v_mfma_f32_16x16x32_bf16 v[42:45], v[190:193], v[204:207], v[42:45]
	v_mfma_f32_16x16x32_bf16 v[34:37], v[182:185], v[212:215], v[34:37]
	v_mfma_f32_16x16x32_bf16 v[26:29], v[190:193], v[212:215], v[26:29]
	v_mfma_f32_16x16x32_bf16 v[18:21], v[182:185], v[220:223], v[18:21]
	v_mfma_f32_16x16x32_bf16 v[10:13], v[190:193], v[220:223], v[10:13]
	v_mfma_f32_16x16x32_bf16 v[6:9], v[182:185], v[240:243], v[6:9]
	v_mfma_f32_16x16x32_bf16 v[2:5], v[190:193], v[240:243], v[2:5]
	s_setprio 0
	s_barrier
	v_or_b32_e32 v0, 0x18000, v164
	v_add_u32_e32 v165, 0x18400, v164
	ds_read_b128 v[158:161], v0
	ds_read_b128 v[166:169], v165
	v_add_u32_e32 v0, 0x18800, v164
	v_add_u32_e32 v165, 0x18c00, v164
	ds_read_b128 v[170:173], v0
	ds_read_b128 v[174:177], v165
	v_or_b32_e32 v0, 0x1c000, v164
	v_add_u32_e32 v165, 0x1c400, v164
	ds_read_b128 v[178:181], v0
	ds_read_b128 v[182:185], v165
	v_add_u32_e32 v0, 0x1c800, v164
	v_add_u32_e32 v165, 0x1cc00, v164
	ds_read_b128 v[186:189], v0
	ds_read_b128 v[190:193], v165
	s_add_u32 s40, s62, 0x40000
	s_addc_u32 s41, s63, 0
	s_mov_b32 m0, s83
	ds_read_b128 v[200:203], v163 offset:32768
	ds_read_b128 v[204:207], v163 offset:33792
	ds_read_b128 v[208:211], v163 offset:34816
	ds_read_b128 v[212:215], v163 offset:35840
	ds_read_b128 v[216:219], v163 offset:36864
	ds_read_b128 v[220:223], v163 offset:37888
	ds_read_b128 v[236:239], v163 offset:38912
	ds_read_b128 v[240:243], v163 offset:39936
	global_load_lds_dwordx4 v130, s[40:41]
	s_mov_b32 m0, s84
	s_nop 0
	global_load_lds_dwordx4 v134, s[40:41]
	s_waitcnt vmcnt(8)
	s_waitcnt lgkmcnt(0)
	s_barrier
	s_setprio 1
	v_mfma_f32_16x16x32_bf16 v[126:129], v[158:161], v[200:203], v[126:129]
	v_mfma_f32_16x16x32_bf16 v[122:125], v[170:173], v[200:203], v[122:125]
	v_mfma_f32_16x16x32_bf16 v[114:117], v[158:161], v[208:211], v[114:117]
	v_mfma_f32_16x16x32_bf16 v[106:109], v[170:173], v[208:211], v[106:109]
	v_mfma_f32_16x16x32_bf16 v[98:101], v[158:161], v[216:219], v[98:101]
	v_mfma_f32_16x16x32_bf16 v[90:93], v[170:173], v[216:219], v[90:93]
	v_mfma_f32_16x16x32_bf16 v[82:85], v[158:161], v[236:239], v[82:85]
	v_mfma_f32_16x16x32_bf16 v[74:77], v[170:173], v[236:239], v[74:77]
	v_mfma_f32_16x16x32_bf16 v[126:129], v[166:169], v[204:207], v[126:129]
	v_mfma_f32_16x16x32_bf16 v[122:125], v[174:177], v[204:207], v[122:125]
	v_mfma_f32_16x16x32_bf16 v[114:117], v[166:169], v[212:215], v[114:117]
	v_mfma_f32_16x16x32_bf16 v[106:109], v[174:177], v[212:215], v[106:109]
	v_mfma_f32_16x16x32_bf16 v[98:101], v[166:169], v[220:223], v[98:101]
	v_mfma_f32_16x16x32_bf16 v[90:93], v[174:177], v[220:223], v[90:93]
	v_mfma_f32_16x16x32_bf16 v[82:85], v[166:169], v[240:243], v[82:85]
	v_mfma_f32_16x16x32_bf16 v[74:77], v[174:177], v[240:243], v[74:77]
	v_mfma_f32_16x16x32_bf16 v[118:121], v[178:181], v[200:203], v[118:121]
	v_mfma_f32_16x16x32_bf16 v[110:113], v[186:189], v[200:203], v[110:113]
	v_mfma_f32_16x16x32_bf16 v[102:105], v[178:181], v[208:211], v[102:105]
	v_mfma_f32_16x16x32_bf16 v[94:97], v[186:189], v[208:211], v[94:97]
	v_mfma_f32_16x16x32_bf16 v[86:89], v[178:181], v[216:219], v[86:89]
	v_mfma_f32_16x16x32_bf16 v[78:81], v[186:189], v[216:219], v[78:81]
	v_mfma_f32_16x16x32_bf16 v[70:73], v[178:181], v[236:239], v[70:73]
	v_mfma_f32_16x16x32_bf16 v[66:69], v[186:189], v[236:239], v[66:69]
	v_mfma_f32_16x16x32_bf16 v[118:121], v[182:185], v[204:207], v[118:121]
	v_mfma_f32_16x16x32_bf16 v[110:113], v[190:193], v[204:207], v[110:113]
	v_mfma_f32_16x16x32_bf16 v[102:105], v[182:185], v[212:215], v[102:105]
	v_mfma_f32_16x16x32_bf16 v[94:97], v[190:193], v[212:215], v[94:97]
	v_mfma_f32_16x16x32_bf16 v[86:89], v[182:185], v[220:223], v[86:89]
	v_mfma_f32_16x16x32_bf16 v[78:81], v[190:193], v[220:223], v[78:81]
	v_mfma_f32_16x16x32_bf16 v[70:73], v[182:185], v[240:243], v[70:73]
	v_mfma_f32_16x16x32_bf16 v[66:69], v[190:193], v[240:243], v[66:69]
	s_setprio 0
	s_barrier
	s_add_i32 m0, s88, 0xffffff80
	s_add_u32 s40, s60, 0x40080
	ds_read_b128 v[200:203], v163 offset:49152
	ds_read_b128 v[204:207], v163 offset:50176
	ds_read_b128 v[208:211], v163 offset:51200
	ds_read_b128 v[212:215], v163 offset:52224
	ds_read_b128 v[216:219], v163 offset:53248
	ds_read_b128 v[220:223], v163 offset:54272
	ds_read_b128 v[236:239], v163 offset:55296
	ds_read_b128 v[240:243], v163 offset:56320
	global_load_lds_dwordx4 v132, s[60:61] offset:128
	v_lshl_add_u64 v[194:195], v[226:227], 0, s[18:19]
	s_mov_b32 m0, s89
	s_addc_u32 s41, s61, 0
	global_load_lds_dwordx4 v[194:195], off
	s_mov_b32 m0, s92
	s_nop 0
	global_load_lds_dwordx4 v132, s[40:41]
	s_mov_b32 m0, s93
	s_nop 0
	global_load_lds_dwordx4 v136, s[40:41]
	s_add_i32 m0, s90, 0xffffff80
	s_nop 0
	global_load_lds_dwordx4 v130, s[62:63] offset:128
	s_add_i32 m0, s91, 0xffffff80
	s_nop 0
	global_load_lds_dwordx4 v134, s[62:63] offset:128
	s_waitcnt vmcnt(8)
	s_waitcnt lgkmcnt(0)
	s_barrier
	s_setprio 1
	v_mfma_f32_16x16x32_bf16 v[62:65], v[158:161], v[200:203], v[62:65]
	v_mfma_f32_16x16x32_bf16 v[58:61], v[170:173], v[200:203], v[58:61]
	v_mfma_f32_16x16x32_bf16 v[54:57], v[158:161], v[208:211], v[54:57]
	v_mfma_f32_16x16x32_bf16 v[46:49], v[170:173], v[208:211], v[46:49]
	v_mfma_f32_16x16x32_bf16 v[38:41], v[158:161], v[216:219], v[38:41]
	v_mfma_f32_16x16x32_bf16 v[30:33], v[170:173], v[216:219], v[30:33]
	v_mfma_f32_16x16x32_bf16 v[22:25], v[158:161], v[236:239], v[22:25]
	v_mfma_f32_16x16x32_bf16 v[14:17], v[170:173], v[236:239], v[14:17]
	v_mfma_f32_16x16x32_bf16 v[62:65], v[166:169], v[204:207], v[62:65]
	v_mfma_f32_16x16x32_bf16 v[58:61], v[174:177], v[204:207], v[58:61]
	v_mfma_f32_16x16x32_bf16 v[54:57], v[166:169], v[212:215], v[54:57]
	v_mfma_f32_16x16x32_bf16 v[46:49], v[174:177], v[212:215], v[46:49]
	v_mfma_f32_16x16x32_bf16 v[38:41], v[166:169], v[220:223], v[38:41]
	v_mfma_f32_16x16x32_bf16 v[30:33], v[174:177], v[220:223], v[30:33]
	v_mfma_f32_16x16x32_bf16 v[22:25], v[166:169], v[240:243], v[22:25]
	v_mfma_f32_16x16x32_bf16 v[14:17], v[174:177], v[240:243], v[14:17]
	v_mfma_f32_16x16x32_bf16 v[50:53], v[178:181], v[200:203], v[50:53]
	v_mfma_f32_16x16x32_bf16 v[42:45], v[186:189], v[200:203], v[42:45]
	v_mfma_f32_16x16x32_bf16 v[34:37], v[178:181], v[208:211], v[34:37]
	v_mfma_f32_16x16x32_bf16 v[26:29], v[186:189], v[208:211], v[26:29]
	v_mfma_f32_16x16x32_bf16 v[18:21], v[178:181], v[216:219], v[18:21]
	v_mfma_f32_16x16x32_bf16 v[10:13], v[186:189], v[216:219], v[10:13]
	v_mfma_f32_16x16x32_bf16 v[6:9], v[178:181], v[236:239], v[6:9]
	v_mfma_f32_16x16x32_bf16 v[2:5], v[186:189], v[236:239], v[2:5]
	v_mfma_f32_16x16x32_bf16 v[50:53], v[182:185], v[204:207], v[50:53]
	v_mfma_f32_16x16x32_bf16 v[42:45], v[190:193], v[204:207], v[42:45]
	v_mfma_f32_16x16x32_bf16 v[34:37], v[182:185], v[212:215], v[34:37]
	v_mfma_f32_16x16x32_bf16 v[26:29], v[190:193], v[212:215], v[26:29]
	v_mfma_f32_16x16x32_bf16 v[18:21], v[182:185], v[220:223], v[18:21]
	v_mfma_f32_16x16x32_bf16 v[10:13], v[190:193], v[220:223], v[10:13]
	v_mfma_f32_16x16x32_bf16 v[6:9], v[182:185], v[240:243], v[6:9]
	v_mfma_f32_16x16x32_bf16 v[2:5], v[190:193], v[240:243], v[2:5]
	s_setprio 0
	s_barrier
	s_add_i32 vcc_lo, vcc_lo, 2
	s_add_u32 s36, s36, 0x100
	s_addc_u32 s37, s37, 0
	s_add_u32 s80, s80, 0x100
	s_addc_u32 s95, s95, 0
	s_cmp_gt_u32 vcc_lo, 13
	s_cbranch_scc0 .LBB0_2006
	s_and_b64 vcc, exec, s[16:17]
	s_cbranch_vccz .LBB0_2009
	s_barrier

.LBB0_2067:
	v_or_b32_e32 v0, 0x10000, v143
	v_add_u32_e32 v148, 0x10400, v143
	ds_read_b128 v[144:147], v0
	ds_read_b128 v[148:151], v148
	v_add_u32_e32 v0, 0x10800, v143
	v_add_u32_e32 v156, 0x10c00, v143
	ds_read_b128 v[152:155], v0
	ds_read_b128 v[156:159], v156
	v_or_b32_e32 v0, 0x14000, v143
	v_add_u32_e32 v164, 0x14400, v143
	ds_read_b128 v[160:163], v0
	ds_read_b128 v[164:167], v164
	v_add_u32_e32 v0, 0x14800, v143
	v_add_u32_e32 v172, 0x14c00, v143
	ds_read_b128 v[168:171], v0
	ds_read_b128 v[172:175], v172
	s_add_u32 s41, s52, 0xfffc0080
	s_addc_u32 s43, s53, -1
	s_cmp_eq_u32 s39, 12
	s_cselect_b32 s57, s47, s43
	s_cselect_b32 s56, s46, s41
	s_cselect_b32 s55, s49, s29
	s_cselect_b32 s54, s48, s17
	s_add_i32 m0, s59, 0xc000
	ds_read_b128 v[176:179], v142
	ds_read_b128 v[180:183], v142 offset:1024
	ds_read_b128 v[184:187], v142 offset:2048
	ds_read_b128 v[188:191], v142 offset:3072
	ds_read_b128 v[192:195], v142 offset:4096
	ds_read_b128 v[200:203], v142 offset:5120
	ds_read_b128 v[204:207], v142 offset:6144
	ds_read_b128 v[208:211], v142 offset:7168
	global_load_lds_dwordx4 v138, s[52:53]
	s_add_i32 m0, s59, 0xe000
	s_nop 0
	global_load_lds_dwordx4 v140, s[52:53]
	s_waitcnt vmcnt(8)
	s_waitcnt lgkmcnt(0)
	s_barrier
	s_setprio 1
	v_mfma_f32_16x16x32_bf16 v[126:129], v[144:147], v[176:179], v[126:129]
	v_mfma_f32_16x16x32_bf16 v[122:125], v[152:155], v[176:179], v[122:125]
	v_mfma_f32_16x16x32_bf16 v[118:121], v[144:147], v[184:187], v[118:121]
	v_mfma_f32_16x16x32_bf16 v[114:117], v[152:155], v[184:187], v[114:117]
	v_mfma_f32_16x16x32_bf16 v[102:105], v[144:147], v[192:195], v[102:105]
	v_mfma_f32_16x16x32_bf16 v[98:101], v[152:155], v[192:195], v[98:101]
	v_mfma_f32_16x16x32_bf16 v[86:89], v[144:147], v[204:207], v[86:89]
	v_mfma_f32_16x16x32_bf16 v[82:85], v[152:155], v[204:207], v[82:85]
	v_mfma_f32_16x16x32_bf16 v[126:129], v[148:151], v[180:183], v[126:129]
	v_mfma_f32_16x16x32_bf16 v[122:125], v[156:159], v[180:183], v[122:125]
	v_mfma_f32_16x16x32_bf16 v[118:121], v[148:151], v[188:191], v[118:121]
	v_mfma_f32_16x16x32_bf16 v[114:117], v[156:159], v[188:191], v[114:117]
	v_mfma_f32_16x16x32_bf16 v[102:105], v[148:151], v[200:203], v[102:105]
	v_mfma_f32_16x16x32_bf16 v[98:101], v[156:159], v[200:203], v[98:101]
	v_mfma_f32_16x16x32_bf16 v[86:89], v[148:151], v[208:211], v[86:89]
	v_mfma_f32_16x16x32_bf16 v[82:85], v[156:159], v[208:211], v[82:85]
	v_mfma_f32_16x16x32_bf16 v[110:113], v[160:163], v[176:179], v[110:113]
	v_mfma_f32_16x16x32_bf16 v[106:109], v[168:171], v[176:179], v[106:109]
	v_mfma_f32_16x16x32_bf16 v[94:97], v[160:163], v[184:187], v[94:97]
	v_mfma_f32_16x16x32_bf16 v[90:93], v[168:171], v[184:187], v[90:93]
	v_mfma_f32_16x16x32_bf16 v[78:81], v[160:163], v[192:195], v[78:81]
	v_mfma_f32_16x16x32_bf16 v[74:77], v[168:171], v[192:195], v[74:77]
	v_mfma_f32_16x16x32_bf16 v[70:73], v[160:163], v[204:207], v[70:73]
	v_mfma_f32_16x16x32_bf16 v[66:69], v[168:171], v[204:207], v[66:69]
	v_mfma_f32_16x16x32_bf16 v[110:113], v[164:167], v[180:183], v[110:113]
	v_mfma_f32_16x16x32_bf16 v[106:109], v[172:175], v[180:183], v[106:109]
	v_mfma_f32_16x16x32_bf16 v[94:97], v[164:167], v[188:191], v[94:97]
	v_mfma_f32_16x16x32_bf16 v[90:93], v[172:175], v[188:191], v[90:93]
	v_mfma_f32_16x16x32_bf16 v[78:81], v[164:167], v[200:203], v[78:81]
	v_mfma_f32_16x16x32_bf16 v[74:77], v[172:175], v[200:203], v[74:77]
	v_mfma_f32_16x16x32_bf16 v[70:73], v[164:167], v[208:211], v[70:73]
	v_mfma_f32_16x16x32_bf16 v[66:69], v[172:175], v[208:211], v[66:69]
	s_setprio 0
	s_barrier
	s_mov_b32 m0, s60
	v_lshl_add_u64 v[212:213], s[54:55], 0, v[132:133]
	s_add_u32 s94, s54, 0x40000
	ds_read_b128 v[176:179], v142 offset:16384
	ds_read_b128 v[180:183], v142 offset:17408
	ds_read_b128 v[184:187], v142 offset:18432
	ds_read_b128 v[188:191], v142 offset:19456
	ds_read_b128 v[192:195], v142 offset:20480
	ds_read_b128 v[200:203], v142 offset:21504
	ds_read_b128 v[204:207], v142 offset:22528
	ds_read_b128 v[208:211], v142 offset:23552
	global_load_lds_dwordx4 v132, s[54:55]
	v_lshl_add_u64 v[214:215], s[54:55], 0, v[136:137]
	s_mov_b32 m0, s61
	s_addc_u32 s95, s55, 0
	global_load_lds_dwordx4 v136, s[54:55]
	s_mov_b32 m0, s62
	v_lshl_add_u64 v[218:219], s[56:57], 0, v[134:135]
	global_load_lds_dwordx4 v132, s[94:95]
	s_mov_b32 m0, s63
	s_nop 0
	global_load_lds_dwordx4 v136, s[94:95]
	v_lshl_add_u64 v[216:217], s[56:57], 0, v[130:131]
	s_mov_b32 m0, s59
	s_nop 0
	global_load_lds_dwordx4 v130, s[56:57]
	s_mov_b32 m0, s64
	s_nop 0
	global_load_lds_dwordx4 v134, s[56:57]
	s_waitcnt vmcnt(8)
	s_waitcnt lgkmcnt(0)
	s_barrier
	s_setprio 1
	v_mfma_f32_16x16x32_bf16 v[62:65], v[144:147], v[176:179], v[62:65]
	v_mfma_f32_16x16x32_bf16 v[58:61], v[152:155], v[176:179], v[58:61]
	v_mfma_f32_16x16x32_bf16 v[54:57], v[144:147], v[184:187], v[54:57]
	v_mfma_f32_16x16x32_bf16 v[50:53], v[152:155], v[184:187], v[50:53]
	v_mfma_f32_16x16x32_bf16 v[38:41], v[144:147], v[192:195], v[38:41]
	v_mfma_f32_16x16x32_bf16 v[34:37], v[152:155], v[192:195], v[34:37]
	v_mfma_f32_16x16x32_bf16 v[22:25], v[144:147], v[204:207], v[22:25]
	v_mfma_f32_16x16x32_bf16 v[18:21], v[152:155], v[204:207], v[18:21]
	v_mfma_f32_16x16x32_bf16 v[62:65], v[148:151], v[180:183], v[62:65]
	v_mfma_f32_16x16x32_bf16 v[58:61], v[156:159], v[180:183], v[58:61]
	v_mfma_f32_16x16x32_bf16 v[54:57], v[148:151], v[188:191], v[54:57]
	v_mfma_f32_16x16x32_bf16 v[50:53], v[156:159], v[188:191], v[50:53]
	v_mfma_f32_16x16x32_bf16 v[38:41], v[148:151], v[200:203], v[38:41]
	v_mfma_f32_16x16x32_bf16 v[34:37], v[156:159], v[200:203], v[34:37]
	v_mfma_f32_16x16x32_bf16 v[22:25], v[148:151], v[208:211], v[22:25]
	v_mfma_f32_16x16x32_bf16 v[18:21], v[156:159], v[208:211], v[18:21]
	v_mfma_f32_16x16x32_bf16 v[46:49], v[160:163], v[176:179], v[46:49]
	v_mfma_f32_16x16x32_bf16 v[42:45], v[168:171], v[176:179], v[42:45]
	v_mfma_f32_16x16x32_bf16 v[30:33], v[160:163], v[184:187], v[30:33]
	v_mfma_f32_16x16x32_bf16 v[26:29], v[168:171], v[184:187], v[26:29]
	v_mfma_f32_16x16x32_bf16 v[14:17], v[160:163], v[192:195], v[14:17]
	v_mfma_f32_16x16x32_bf16 v[10:13], v[168:171], v[192:195], v[10:13]
	v_mfma_f32_16x16x32_bf16 v[6:9], v[160:163], v[204:207], v[6:9]
	v_mfma_f32_16x16x32_bf16 v[2:5], v[168:171], v[204:207], v[2:5]
	v_mfma_f32_16x16x32_bf16 v[46:49], v[164:167], v[180:183], v[46:49]
	v_mfma_f32_16x16x32_bf16 v[42:45], v[172:175], v[180:183], v[42:45]
	v_mfma_f32_16x16x32_bf16 v[30:33], v[164:167], v[188:191], v[30:33]
	v_mfma_f32_16x16x32_bf16 v[26:29], v[172:175], v[188:191], v[26:29]
	v_mfma_f32_16x16x32_bf16 v[14:17], v[164:167], v[200:203], v[14:17]
	v_mfma_f32_16x16x32_bf16 v[10:13], v[172:175], v[200:203], v[10:13]
	v_mfma_f32_16x16x32_bf16 v[6:9], v[164:167], v[208:211], v[6:9]
	v_mfma_f32_16x16x32_bf16 v[2:5], v[172:175], v[208:211], v[2:5]
	s_setprio 0
	s_barrier
	v_or_b32_e32 v0, 0x18000, v143
	v_add_u32_e32 v148, 0x18400, v143
	ds_read_b128 v[144:147], v0
	ds_read_b128 v[148:151], v148
	v_add_u32_e32 v0, 0x18800, v143
	v_add_u32_e32 v156, 0x18c00, v143
	ds_read_b128 v[152:155], v0
	ds_read_b128 v[156:159], v156
	v_or_b32_e32 v0, 0x1c000, v143
	v_add_u32_e32 v164, 0x1c400, v143
	ds_read_b128 v[160:163], v0
	ds_read_b128 v[164:167], v164
	v_add_u32_e32 v0, 0x1c800, v143
	v_add_u32_e32 v172, 0x1cc00, v143
	ds_read_b128 v[168:171], v0
	ds_read_b128 v[172:175], v172
	s_add_u32 s56, s56, 0x40000
	s_addc_u32 s57, s57, 0
	s_mov_b32 m0, s65
	ds_read_b128 v[176:179], v142 offset:32768
	ds_read_b128 v[180:183], v142 offset:33792
	ds_read_b128 v[184:187], v142 offset:34816
	ds_read_b128 v[188:191], v142 offset:35840
	ds_read_b128 v[192:195], v142 offset:36864
	ds_read_b128 v[200:203], v142 offset:37888
	ds_read_b128 v[204:207], v142 offset:38912
	ds_read_b128 v[208:211], v142 offset:39936
	global_load_lds_dwordx4 v130, s[56:57]
	s_mov_b32 m0, s66
	s_nop 0
	global_load_lds_dwordx4 v134, s[56:57]
	s_waitcnt vmcnt(8)
	s_waitcnt lgkmcnt(0)
	s_barrier
	s_setprio 1
	v_mfma_f32_16x16x32_bf16 v[126:129], v[144:147], v[176:179], v[126:129]
	v_mfma_f32_16x16x32_bf16 v[122:125], v[152:155], v[176:179], v[122:125]
	v_mfma_f32_16x16x32_bf16 v[118:121], v[144:147], v[184:187], v[118:121]
	v_mfma_f32_16x16x32_bf16 v[114:117], v[152:155], v[184:187], v[114:117]
	v_mfma_f32_16x16x32_bf16 v[102:105], v[144:147], v[192:195], v[102:105]
	v_mfma_f32_16x16x32_bf16 v[98:101], v[152:155], v[192:195], v[98:101]
	v_mfma_f32_16x16x32_bf16 v[86:89], v[144:147], v[204:207], v[86:89]
	v_mfma_f32_16x16x32_bf16 v[82:85], v[152:155], v[204:207], v[82:85]
	v_mfma_f32_16x16x32_bf16 v[126:129], v[148:151], v[180:183], v[126:129]
	v_mfma_f32_16x16x32_bf16 v[122:125], v[156:159], v[180:183], v[122:125]
	v_mfma_f32_16x16x32_bf16 v[118:121], v[148:151], v[188:191], v[118:121]
	v_mfma_f32_16x16x32_bf16 v[114:117], v[156:159], v[188:191], v[114:117]
	v_mfma_f32_16x16x32_bf16 v[102:105], v[148:151], v[200:203], v[102:105]
	v_mfma_f32_16x16x32_bf16 v[98:101], v[156:159], v[200:203], v[98:101]
	v_mfma_f32_16x16x32_bf16 v[86:89], v[148:151], v[208:211], v[86:89]
	v_mfma_f32_16x16x32_bf16 v[82:85], v[156:159], v[208:211], v[82:85]
	v_mfma_f32_16x16x32_bf16 v[110:113], v[160:163], v[176:179], v[110:113]
	v_mfma_f32_16x16x32_bf16 v[106:109], v[168:171], v[176:179], v[106:109]
	v_mfma_f32_16x16x32_bf16 v[94:97], v[160:163], v[184:187], v[94:97]
	v_mfma_f32_16x16x32_bf16 v[90:93], v[168:171], v[184:187], v[90:93]
	v_mfma_f32_16x16x32_bf16 v[78:81], v[160:163], v[192:195], v[78:81]
	v_mfma_f32_16x16x32_bf16 v[74:77], v[168:171], v[192:195], v[74:77]
	v_mfma_f32_16x16x32_bf16 v[70:73], v[160:163], v[204:207], v[70:73]
	v_mfma_f32_16x16x32_bf16 v[66:69], v[168:171], v[204:207], v[66:69]
	v_mfma_f32_16x16x32_bf16 v[110:113], v[164:167], v[180:183], v[110:113]
	v_mfma_f32_16x16x32_bf16 v[106:109], v[172:175], v[180:183], v[106:109]
	v_mfma_f32_16x16x32_bf16 v[94:97], v[164:167], v[188:191], v[94:97]
	v_mfma_f32_16x16x32_bf16 v[90:93], v[172:175], v[188:191], v[90:93]
	v_mfma_f32_16x16x32_bf16 v[78:81], v[164:167], v[200:203], v[78:81]
	v_mfma_f32_16x16x32_bf16 v[74:77], v[172:175], v[200:203], v[74:77]
	v_mfma_f32_16x16x32_bf16 v[70:73], v[164:167], v[208:211], v[70:73]
	v_mfma_f32_16x16x32_bf16 v[66:69], v[172:175], v[208:211], v[66:69]
	s_setprio 0
	s_barrier
	s_mov_b32 m0, s80
	v_lshl_add_u64 v[212:213], v[212:213], 0, s[18:19]
	s_add_u32 s54, s54, 0x40080
	ds_read_b128 v[176:179], v142 offset:49152
	ds_read_b128 v[180:183], v142 offset:50176
	ds_read_b128 v[184:187], v142 offset:51200
	ds_read_b128 v[188:191], v142 offset:52224
	ds_read_b128 v[192:195], v142 offset:53248
	ds_read_b128 v[200:203], v142 offset:54272
	ds_read_b128 v[204:207], v142 offset:55296
	ds_read_b128 v[208:211], v142 offset:56320
	global_load_lds_dwordx4 v[212:213], off
	v_lshl_add_u64 v[212:213], v[214:215], 0, s[18:19]
	s_mov_b32 m0, s82
	s_addc_u32 s55, s55, 0
	global_load_lds_dwordx4 v[212:213], off
	s_mov_b32 m0, s85
	s_nop 0
	global_load_lds_dwordx4 v132, s[54:55]
	s_mov_b32 m0, s88
	s_nop 0
	global_load_lds_dwordx4 v136, s[54:55]
	v_lshl_add_u64 v[212:213], v[216:217], 0, s[18:19]
	s_mov_b32 m0, s83
	s_nop 0
	global_load_lds_dwordx4 v[212:213], off
	v_lshl_add_u64 v[212:213], v[218:219], 0, s[18:19]
	s_mov_b32 m0, s84
	s_nop 0
	global_load_lds_dwordx4 v[212:213], off
	s_waitcnt vmcnt(8)
	s_waitcnt lgkmcnt(0)
	s_barrier
	s_setprio 1
	v_mfma_f32_16x16x32_bf16 v[62:65], v[144:147], v[176:179], v[62:65]
	v_mfma_f32_16x16x32_bf16 v[58:61], v[152:155], v[176:179], v[58:61]
	v_mfma_f32_16x16x32_bf16 v[54:57], v[144:147], v[184:187], v[54:57]
	v_mfma_f32_16x16x32_bf16 v[50:53], v[152:155], v[184:187], v[50:53]
	v_mfma_f32_16x16x32_bf16 v[38:41], v[144:147], v[192:195], v[38:41]
	v_mfma_f32_16x16x32_bf16 v[34:37], v[152:155], v[192:195], v[34:37]
	v_mfma_f32_16x16x32_bf16 v[22:25], v[144:147], v[204:207], v[22:25]
	v_mfma_f32_16x16x32_bf16 v[18:21], v[152:155], v[204:207], v[18:21]
	v_mfma_f32_16x16x32_bf16 v[62:65], v[148:151], v[180:183], v[62:65]
	v_mfma_f32_16x16x32_bf16 v[58:61], v[156:159], v[180:183], v[58:61]
	v_mfma_f32_16x16x32_bf16 v[54:57], v[148:151], v[188:191], v[54:57]
	v_mfma_f32_16x16x32_bf16 v[50:53], v[156:159], v[188:191], v[50:53]
	v_mfma_f32_16x16x32_bf16 v[38:41], v[148:151], v[200:203], v[38:41]
	v_mfma_f32_16x16x32_bf16 v[34:37], v[156:159], v[200:203], v[34:37]
	v_mfma_f32_16x16x32_bf16 v[22:25], v[148:151], v[208:211], v[22:25]
	v_mfma_f32_16x16x32_bf16 v[18:21], v[156:159], v[208:211], v[18:21]
	v_mfma_f32_16x16x32_bf16 v[46:49], v[160:163], v[176:179], v[46:49]
	v_mfma_f32_16x16x32_bf16 v[42:45], v[168:171], v[176:179], v[42:45]
	v_mfma_f32_16x16x32_bf16 v[30:33], v[160:163], v[184:187], v[30:33]
	v_mfma_f32_16x16x32_bf16 v[26:29], v[168:171], v[184:187], v[26:29]
	v_mfma_f32_16x16x32_bf16 v[14:17], v[160:163], v[192:195], v[14:17]
	v_mfma_f32_16x16x32_bf16 v[10:13], v[168:171], v[192:195], v[10:13]
	v_mfma_f32_16x16x32_bf16 v[6:9], v[160:163], v[204:207], v[6:9]
	v_mfma_f32_16x16x32_bf16 v[2:5], v[168:171], v[204:207], v[2:5]
	v_mfma_f32_16x16x32_bf16 v[46:49], v[164:167], v[180:183], v[46:49]
	v_mfma_f32_16x16x32_bf16 v[42:45], v[172:175], v[180:183], v[42:45]
	v_mfma_f32_16x16x32_bf16 v[30:33], v[164:167], v[188:191], v[30:33]
	v_mfma_f32_16x16x32_bf16 v[26:29], v[172:175], v[188:191], v[26:29]
	v_mfma_f32_16x16x32_bf16 v[14:17], v[164:167], v[200:203], v[14:17]
	v_mfma_f32_16x16x32_bf16 v[10:13], v[172:175], v[200:203], v[10:13]
	v_mfma_f32_16x16x32_bf16 v[6:9], v[164:167], v[208:211], v[6:9]
	v_mfma_f32_16x16x32_bf16 v[2:5], v[172:175], v[208:211], v[2:5]
	s_setprio 0
	s_barrier
	s_add_i32 s39, s39, 2
	s_add_u32 s52, s52, 0x100
	s_addc_u32 s53, s53, 0
	s_add_u32 s17, s17, 0x100
	s_addc_u32 s29, s29, 0
	s_cmp_gt_u32 s39, 13
	s_cbranch_scc0 .LBB0_2067
	s_and_b64 vcc, exec, s[14:15]
	s_cbranch_vccz .LBB0_2070
	s_barrier
